# hand-written 3-deep down-weight conversion with 64k x 64n items (256 B contiguous per source row, was 128 B), on top of best
# baseline (speedup 1.0000x reference)
;     __device__ __forceinline__ void operator()(const f32x4 (&acc)[2][2][4][2], const Unit& u, int wr, int wc, int fr, int fq) const {
;         asm volatile("" : "+v"(fr), "+v"(fq));
;         const int e = blkE[u.z], c0 = u.pn * 128 + wc * 32 + 8 * fq, row0 = wr * 64 + fr;
;         const float* bg = bup + (size_t)e * 2 * FF + c0; const f32x4 g0 = *(const f32x4*)bg, g1 = *(const f32x4*)(bg + 4), l0 = *(const f32x4*)(bg + FF), l1 = *(const f32x4*)(bg + FF + 4);
;         float rsb[8];
; #pragma unroll
;         for (int q = 0; q < 8; ++q) rsb[q] = ssq[tokTab[u.pm * 256 + row0 + (q >> 2) * 128 + (q & 3) * 16]] * W8_INV;
; #pragma unroll
;         for (int ai = 0; ai < 2; ++ai)
; #pragma unroll
;             for (int m = 0; m < 4; ++m) { const int r = row0 + ai * 128 + m * 16; const float rs = rsb[ai * 4 + m];
;                 float a[8];
; #pragma unroll
;                 for (int j = 0; j < 8; ++j) { const float gb = j < 4 ? g0[j & 3] : g1[j & 3], lb = j < 4 ? l0[j & 3] : l1[j & 3];
;                     const float gl = fminf(acc[ai][0][m][j >> 2][j & 3] * rs + gb, 7.0f), ln = fminf(fmaxf(acc[ai][1][m][j >> 2][j & 3] * rs + lb, -7.0f), 7.0f);
;                     a[j] = gl * __builtin_amdgcn_rcpf(1.0f + __builtin_amdgcn_exp2f(-1.702f * 1.4426950408889634f * gl)) * (ln + 1.0f); }
;                 v2u w; w.x = pk4_fp8(a[0], a[1], a[2], a[3]); w.y = pk4_fp8(a[4], a[5], a[6], a[7]);
.LBB0_1534:
	s_lshl_b32 s4, s40, 7
	v_mov_b32_e32 v2, v218
	v_mov_b32_e32 v3, v219
	s_or_b32 s4, s4, s89
	v_mov_b32_e32 v0, s35
	v_lshl_add_u32 v16, v3, 3, s4
	v_readlane_b32 s0, v254, 2
	v_readlane_b32 s4, v254, 6
	s_lshl_b32 s4, s65, 10
	v_add_u32_e32 v18, s88, v2
	s_add_i32 s4, s4, 0
	v_lshl_add_u32 v2, v18, 2, s4
	v_add_u32_e32 v9, 0x20400, v2
	ds_read2_b32 v[4:5], v9 offset1:16
	ds_read_b32 v0, v0
	v_readlane_b32 s1, v254, 3
	v_ashrrev_i32_e32 v17, 31, v16
	ds_read2_b32 v[20:21], v9 offset0:160 offset1:176
	s_waitcnt lgkmcnt(0)
	v_ashrrev_i32_e32 v11, 31, v4
	v_mov_b32_e32 v10, v4
	v_lshl_add_u64 v[10:11], v[10:11], 2, s[14:15]
	global_load_dword v19, v[10:11], off
	ds_read2_b32 v[10:11], v9 offset0:32 offset1:48
	v_ashrrev_i32_e32 v13, 31, v5
	v_mov_b32_e32 v12, v5
	v_lshl_add_u64 v[4:5], v[12:13], 2, s[14:15]
	global_load_dword v24, v[4:5], off
	s_waitcnt lgkmcnt(0)
	v_ashrrev_i32_e32 v5, 31, v10
	v_mov_b32_e32 v4, v10
	v_lshl_add_u64 v[4:5], v[4:5], 2, s[14:15]
	global_load_dword v25, v[4:5], off
	ds_read2_b32 v[4:5], v9 offset0:128 offset1:144
	v_ashrrev_i32_e32 v13, 31, v11
	v_mov_b32_e32 v12, v11
	v_lshl_add_u64 v[10:11], v[12:13], 2, s[14:15]
	v_ashrrev_i32_e32 v1, 31, v0
	global_load_dword v26, v[10:11], off
	s_waitcnt lgkmcnt(0)
	v_ashrrev_i32_e32 v11, 31, v4
	v_mov_b32_e32 v10, v4
	v_lshlrev_b64 v[0:1], 14, v[0:1]
	v_lshl_add_u64 v[10:11], v[10:11], 2, s[14:15]
	v_lshl_add_u64 v[0:1], s[0:1], 0, v[0:1]
	global_load_dword v27, v[10:11], off
	v_ashrrev_i32_e32 v11, 31, v5
	v_mov_b32_e32 v10, v5
	v_lshl_add_u64 v[6:7], v[16:17], 2, v[0:1]
	v_lshl_add_u64 v[4:5], v[10:11], 2, s[14:15]
	global_load_dwordx4 v[0:3], v[6:7], off
	global_load_dword v28, v[4:5], off
	v_ashrrev_i32_e32 v5, 31, v20
	v_mov_b32_e32 v4, v20
	v_add_co_u32_e32 v8, vcc, s56, v6
	v_lshl_add_u64 v[4:5], v[4:5], 2, s[14:15]
	global_load_dword v29, v[4:5], off
	v_addc_co_u32_e32 v9, vcc, 0, v7, vcc
	global_load_dwordx4 v[8:11], v[8:9], off
	s_nop 0
	global_load_dwordx4 v[12:15], v[6:7], off offset:16
	v_readlane_b32 s5, v254, 7
	s_mov_b64 s[4:5], 0x2000
	v_ashrrev_i32_e32 v23, 31, v21
	v_lshl_add_u64 v[4:5], v[6:7], 0, s[4:5]
	global_load_dwordx4 v[4:7], v[4:5], off offset:16
	v_mov_b32_e32 v22, v21
	v_lshl_add_u64 v[20:21], v[22:23], 2, s[14:15]
	global_load_dword v20, v[20:21], off
	s_ashr_i32 s39, s38, 31
	s_lshl_b64 s[4:5], s[38:39], 19
	s_add_u32 s4, s93, s4
	s_addc_u32 s5, s87, s5
	v_readlane_b32 s0, v254, 10
	s_cmp_lg_u32 s65, s0
	v_readlane_b32 s2, v254, 4
	v_readlane_b32 s3, v254, 5
	v_readlane_b32 s6, v254, 8
	v_readlane_b32 s7, v254, 9
	s_waitcnt vmcnt(0)
	v_mul_f32_e32 v19, 0x3b800000, v19
	v_mul_f32_e32 v30, 0x3b800000, v24
	v_mul_f32_e32 v25, 0x3b800000, v25
	v_mul_f32_e32 v24, 0x3b800000, v26
	v_mul_f32_e32 v23, 0x3b800000, v27
	v_fma_f32 v26, v192, v19, v0
	v_mul_f32_e32 v22, 0x3b800000, v28
	v_fma_f32 v28, v193, v19, v1
	v_min_f32_e32 v26, 0x40e00000, v26
	v_min_f32_e32 v28, 0x40e00000, v28
	v_fma_f32 v31, v194, v19, v2
	v_mul_f32_e32 v34, 0xc01d265f, v26
	v_mul_f32_e32 v35, 0xc01d265f, v28
	v_min_f32_e32 v31, 0x40e00000, v31
	v_exp_f32_e32 v34, v34
	v_exp_f32_e32 v35, v35
	v_mul_f32_e32 v36, 0xc01d265f, v31
	v_fma_f32 v33, v195, v19, v3
	v_exp_f32_e32 v36, v36
	v_min_f32_e32 v33, 0x40e00000, v33
	v_mul_f32_e32 v37, 0xc01d265f, v33
	v_add_f32_e32 v34, 1.0, v34
	v_add_f32_e32 v35, 1.0, v35
	v_exp_f32_e32 v37, v37
	v_rcp_f32_e32 v34, v34
	v_rcp_f32_e32 v35, v35
	v_add_f32_e32 v36, 1.0, v36
	v_mul_f32_e32 v21, 0x3b800000, v29
	v_fma_f32 v27, v188, v19, v8
	v_fma_f32 v29, v189, v19, v9
	v_rcp_f32_e32 v36, v36
	v_med3_f32 v27, v27, s23, v236
	v_med3_f32 v29, v29, s23, v236
	v_fma_f32 v32, v190, v19, v10
	v_add_f32_e32 v27, 1.0, v27
	v_add_f32_e32 v29, 1.0, v29
	v_add_f32_e32 v37, 1.0, v37
	v_mul_f32_e32 v26, v26, v34
	v_mul_f32_e32 v28, v28, v35
	v_med3_f32 v32, v32, s23, v236
	v_mul_f32_e32 v26, v27, v26
	v_mul_f32_e32 v27, v29, v28
	v_rcp_f32_e32 v28, v37
	v_add_f32_e32 v32, 1.0, v32
	v_mul_f32_e32 v31, v31, v36
	v_mul_f32_e32 v29, v32, v31
	v_fma_f32 v32, v184, v19, v12
	v_min_f32_e32 v32, 0x40e00000, v32
	v_mul_f32_e32 v28, v33, v28
	v_mul_f32_e32 v33, 0xc01d265f, v32
	v_exp_f32_e32 v33, v33
	v_fma_f32 v34, v185, v19, v13
	v_min_f32_e32 v34, 0x40e00000, v34
	v_mul_f32_e32 v35, 0xc01d265f, v34
	v_add_f32_e32 v33, 1.0, v33
	v_rcp_f32_e32 v33, v33
	v_exp_f32_e32 v35, v35
	v_fma_f32 v31, v191, v19, v11
	v_fma_f32 v36, v187, v19, v15
	v_mul_f32_e32 v32, v32, v33
	v_add_f32_e32 v33, 1.0, v35
	v_rcp_f32_e32 v33, v33
	v_med3_f32 v31, v31, s23, v236
	v_min_f32_e32 v36, 0x40e00000, v36
	v_add_f32_e32 v31, 1.0, v31
	v_mul_f32_e32 v33, v34, v33
	v_fma_f32 v34, v186, v19, v14
	v_min_f32_e32 v34, 0x40e00000, v34
	v_mul_f32_e32 v35, 0xc01d265f, v34
	v_exp_f32_e32 v35, v35
	v_mul_f32_e32 v37, 0xc01d265f, v36
	v_mul_f32_e32 v28, v31, v28
	v_fma_f32 v31, v180, v19, v4
	v_add_f32_e32 v35, 1.0, v35
	v_rcp_f32_e32 v35, v35
	v_exp_f32_e32 v37, v37
	v_med3_f32 v31, v31, s23, v236
	v_add_f32_e32 v31, 1.0, v31
	v_mul_f32_e32 v31, v31, v32
	v_fma_f32 v32, v181, v19, v5
	v_med3_f32 v32, v32, s23, v236
	v_mul_f32_e32 v34, v34, v35
	v_add_f32_e32 v35, 1.0, v37
	v_add_f32_e32 v32, 1.0, v32
	v_rcp_f32_e32 v35, v35
	v_mul_f32_e32 v32, v32, v33
	v_fma_f32 v33, v182, v19, v6
	v_med3_f32 v33, v33, s23, v236
	v_fma_f32 v19, v183, v19, v7
	v_add_f32_e32 v33, 1.0, v33
	v_med3_f32 v19, v19, s23, v236
	v_mul_f32_e32 v33, v33, v34
	v_mul_f32_e32 v34, v36, v35
	v_add_f32_e32 v19, 1.0, v19
	v_mul_f32_e32 v19, v19, v34
	v_med3_f32 v34, v26, s24, v237
	v_med3_f32 v27, v27, s24, v237
	v_mov_b32_e32 v26, v65
	v_cvt_pk_fp8_f32 v26, v34, v27
	v_med3_f32 v31, v31, s24, v237
	v_med3_f32 v32, v32, s24, v237
;     __device__ __forceinline__ void operator()(const f32x4 (&acc)[2][2][4][2], const Unit& u, int wr, int wc, int fr, int fq) const {
;     ...
;         const int e = blkE[u.z], c0 = u.pn * 128 + wc * 32 + 8 * fq, row0 = wr * 64 + fr;
;         const float* bg = bup + (size_t)e * 2 * FF + c0; const f32x4 g0 = *(const f32x4*)bg, g1 = *(const f32x4*)(bg + 4), l0 = *(const f32x4*)(bg + FF), l1 = *(const f32x4*)(bg + FF + 4);
;         float rsb[8];
; #pragma unroll
;         for (int q = 0; q < 8; ++q) rsb[q] = ssq[tokTab[u.pm * 256 + row0 + (q >> 2) * 128 + (q & 3) * 16]] * W8_INV;
; #pragma unroll
;         for (int ai = 0; ai < 2; ++ai)
; #pragma unroll
;             for (int m = 0; m < 4; ++m) { const int r = row0 + ai * 128 + m * 16; const float rs = rsb[ai * 4 + m];
;                 float a[8];
; #pragma unroll
;                 for (int j = 0; j < 8; ++j) { const float gb = j < 4 ? g0[j & 3] : g1[j & 3], lb = j < 4 ? l0[j & 3] : l1[j & 3];
;                     const float gl = fminf(acc[ai][0][m][j >> 2][j & 3] * rs + gb, 7.0f), ln = fminf(fmaxf(acc[ai][1][m][j >> 2][j & 3] * rs + lb, -7.0f), 7.0f);
;                     a[j] = gl * __builtin_amdgcn_rcpf(1.0f + __builtin_amdgcn_exp2f(-1.702f * 1.4426950408889634f * gl)) * (ln + 1.0f); }
;                 v2u w; w.x = pk4_fp8(a[0], a[1], a[2], a[3]); w.y = pk4_fp8(a[4], a[5], a[6], a[7]);
;                 *(v2u*)(ACT + ((size_t)u.z * 256 + r) * FF + c0) = w; }
	v_mov_b32_e32 v27, v65
	v_cvt_pk_fp8_f32 v27, v31, v32
	v_med3_f32 v29, v29, s24, v237
	v_med3_f32 v28, v28, s24, v237
	v_cvt_pk_fp8_f32 v26, v29, v28 op_sel:[0,0,1]
	v_med3_f32 v28, v33, s24, v237
	v_med3_f32 v19, v19, s24, v237
	v_cvt_pk_fp8_f32 v27, v28, v19 op_sel:[0,0,1]
	v_ashrrev_i32_e32 v19, 31, v18
	v_lshlrev_b64 v[18:19], 11, v[18:19]
	v_lshl_add_u64 v[18:19], s[4:5], 0, v[18:19]
	v_lshl_add_u64 v[16:17], v[18:19], 0, v[16:17]
	global_store_dwordx2 v[16:17], v[26:27], off
	v_fma_f32 v26, v177, v30, v1
	v_min_f32_e32 v26, 0x40e00000, v26
	v_fma_f32 v28, v176, v30, v0
	v_mul_f32_e32 v27, 0xc01d265f, v26
	v_min_f32_e32 v28, 0x40e00000, v28
	v_exp_f32_e32 v27, v27
	v_mul_f32_e32 v29, 0xc01d265f, v28
	v_exp_f32_e32 v29, v29
	v_fma_f32 v32, v169, v30, v13
	v_add_f32_e32 v27, 1.0, v27
	v_rcp_f32_e32 v27, v27
	v_add_f32_e32 v19, 1.0, v29
	v_rcp_f32_e32 v19, v19
	v_fma_f32 v29, v179, v30, v3
	v_mul_f32_e32 v26, v26, v27
	v_fma_f32 v27, v178, v30, v2
	v_min_f32_e32 v27, 0x40e00000, v27
	v_mul_f32_e32 v19, v28, v19
	v_mul_f32_e32 v28, 0xc01d265f, v27
	v_exp_f32_e32 v28, v28
	v_min_f32_e32 v29, 0x40e00000, v29
	v_mul_f32_e32 v31, 0xc01d265f, v29
	v_exp_f32_e32 v31, v31
	v_add_f32_e32 v28, 1.0, v28
	v_rcp_f32_e32 v28, v28
	v_min_f32_e32 v32, 0x40e00000, v32
	v_mul_f32_e32 v33, 0xc01d265f, v32
	v_exp_f32_e32 v33, v33
	v_mul_f32_e32 v27, v27, v28
	v_add_f32_e32 v28, 1.0, v31
	v_rcp_f32_e32 v28, v28
	v_fma_f32 v18, v172, v30, v8
	v_med3_f32 v18, v18, s23, v236
	v_add_f32_e32 v18, 1.0, v18
	v_mul_f32_e32 v28, v29, v28
	v_fma_f32 v29, v168, v30, v12
	v_min_f32_e32 v29, 0x40e00000, v29
	v_mul_f32_e32 v31, 0xc01d265f, v29
	v_exp_f32_e32 v31, v31
	v_mul_f32_e32 v18, v18, v19
	v_fma_f32 v19, v173, v30, v9
	v_med3_f32 v19, v19, s23, v236
	v_add_f32_e32 v31, 1.0, v31
	v_rcp_f32_e32 v31, v31
	v_add_f32_e32 v19, 1.0, v19
	v_mul_f32_e32 v19, v19, v26
	v_fma_f32 v26, v174, v30, v10
	v_mul_f32_e32 v29, v29, v31
	v_add_f32_e32 v31, 1.0, v33
	v_rcp_f32_e32 v31, v31
	v_med3_f32 v26, v26, s23, v236
	v_add_f32_e32 v26, 1.0, v26
	v_mul_f32_e32 v26, v26, v27
	v_mul_f32_e32 v31, v32, v31
	v_fma_f32 v32, v170, v30, v14
	v_min_f32_e32 v32, 0x40e00000, v32
	v_mul_f32_e32 v33, 0xc01d265f, v32
	v_exp_f32_e32 v33, v33
	v_fma_f32 v27, v175, v30, v11
	v_fma_f32 v34, v171, v30, v15
	v_med3_f32 v27, v27, s23, v236
	v_min_f32_e32 v34, 0x40e00000, v34
	v_add_f32_e32 v27, 1.0, v27
	v_add_f32_e32 v33, 1.0, v33
	v_mul_f32_e32 v35, 0xc01d265f, v34
	v_mul_f32_e32 v27, v27, v28
	v_fma_f32 v28, v164, v30, v4
	v_rcp_f32_e32 v33, v33
	v_exp_f32_e32 v35, v35
	v_med3_f32 v28, v28, s23, v236
	v_add_f32_e32 v28, 1.0, v28
	v_mul_f32_e32 v28, v28, v29
	v_fma_f32 v29, v165, v30, v5
	v_med3_f32 v29, v29, s23, v236
	v_mul_f32_e32 v32, v32, v33
	v_add_f32_e32 v33, 1.0, v35
	v_add_f32_e32 v29, 1.0, v29
	v_rcp_f32_e32 v33, v33
	v_mul_f32_e32 v29, v29, v31
	v_fma_f32 v31, v166, v30, v6
	v_med3_f32 v31, v31, s23, v236
	v_fma_f32 v30, v167, v30, v7
	v_add_f32_e32 v31, 1.0, v31
	v_med3_f32 v30, v30, s23, v236
	v_mul_f32_e32 v31, v31, v32
	v_mul_f32_e32 v32, v34, v33
	v_add_f32_e32 v30, 1.0, v30
	v_mul_f32_e32 v30, v30, v32
	v_med3_f32 v32, v18, s24, v237
	v_med3_f32 v19, v19, s24, v237
	v_mov_b32_e32 v18, v65
	v_cvt_pk_fp8_f32 v18, v32, v19
	v_med3_f32 v28, v28, s24, v237
	v_med3_f32 v29, v29, s24, v237
	v_mov_b32_e32 v19, v65
	v_cvt_pk_fp8_f32 v19, v28, v29
	v_med3_f32 v26, v26, s24, v237
	v_med3_f32 v27, v27, s24, v237
	v_cvt_pk_fp8_f32 v18, v26, v27 op_sel:[0,0,1]
	v_med3_f32 v26, v31, s24, v237
	v_med3_f32 v27, v30, s24, v237
	v_cvt_pk_fp8_f32 v19, v26, v27 op_sel:[0,0,1]
	v_fma_f32 v27, v160, v25, v0
	v_min_f32_e32 v28, 0x40e00000, v27
	v_add_co_u32_e32 v26, vcc, s73, v16
	v_mul_f32_e32 v27, 0xc01d265f, v28
	v_exp_f32_e32 v29, v27
	v_addc_co_u32_e32 v27, vcc, 0, v17, vcc
	global_store_dwordx2 v[26:27], v[18:19], off
	v_fma_f32 v26, v161, v25, v1
	v_min_f32_e32 v26, 0x40e00000, v26
	v_mul_f32_e32 v27, 0xc01d265f, v26
	v_exp_f32_e32 v27, v27
	v_add_f32_e32 v19, 1.0, v29
	v_rcp_f32_e32 v19, v19
	v_fma_f32 v29, v163, v25, v3
	v_add_f32_e32 v27, 1.0, v27
	v_rcp_f32_e32 v27, v27
	v_mul_f32_e32 v19, v28, v19
	v_min_f32_e32 v29, 0x40e00000, v29
	v_mul_f32_e32 v30, 0xc01d265f, v29
	v_mul_f32_e32 v26, v26, v27
	v_fma_f32 v27, v162, v25, v2
	v_min_f32_e32 v27, 0x40e00000, v27
	v_mul_f32_e32 v28, 0xc01d265f, v27
	v_exp_f32_e32 v28, v28
	v_exp_f32_e32 v30, v30
	v_fma_f32 v31, v153, v25, v13
	v_min_f32_e32 v31, 0x40e00000, v31
	v_add_f32_e32 v28, 1.0, v28
	v_rcp_f32_e32 v28, v28
	v_mul_f32_e32 v32, 0xc01d265f, v31
	v_exp_f32_e32 v32, v32
	v_fma_f32 v18, v156, v25, v8
	v_mul_f32_e32 v27, v27, v28
	v_add_f32_e32 v28, 1.0, v30
	v_rcp_f32_e32 v28, v28
	v_med3_f32 v18, v18, s23, v236
	v_add_f32_e32 v18, 1.0, v18
	v_mul_f32_e32 v18, v18, v19
	v_mul_f32_e32 v28, v29, v28
	v_fma_f32 v29, v152, v25, v12
	v_min_f32_e32 v29, 0x40e00000, v29
	v_mul_f32_e32 v30, 0xc01d265f, v29
	v_exp_f32_e32 v30, v30
	v_fma_f32 v19, v157, v25, v9
	v_med3_f32 v19, v19, s23, v236
	v_add_f32_e32 v19, 1.0, v19
	v_add_f32_e32 v30, 1.0, v30
	v_rcp_f32_e32 v30, v30
	v_mul_f32_e32 v19, v19, v26
	v_fma_f32 v26, v158, v25, v10
	v_med3_f32 v26, v26, s23, v236
	v_mul_f32_e32 v29, v29, v30
	v_add_f32_e32 v30, 1.0, v32
	v_rcp_f32_e32 v30, v30
	v_add_f32_e32 v26, 1.0, v26
	v_mul_f32_e32 v26, v26, v27
	v_fma_f32 v27, v159, v25, v11
	v_mul_f32_e32 v30, v31, v30
	v_fma_f32 v31, v154, v25, v14
	v_min_f32_e32 v31, 0x40e00000, v31
	v_mul_f32_e32 v32, 0xc01d265f, v31
	v_exp_f32_e32 v32, v32
	v_fma_f32 v33, v155, v25, v15
	v_med3_f32 v27, v27, s23, v236
	v_min_f32_e32 v33, 0x40e00000, v33
	v_add_f32_e32 v27, 1.0, v27
	v_add_f32_e32 v32, 1.0, v32
;     __device__ __forceinline__ void operator()(const f32x4 (&acc)[2][2][4][2], const Unit& u, int wr, int wc, int fr, int fq) const {
;     ...
;         const int e = blkE[u.z], c0 = u.pn * 128 + wc * 32 + 8 * fq, row0 = wr * 64 + fr;
;         const float* bg = bup + (size_t)e * 2 * FF + c0; const f32x4 g0 = *(const f32x4*)bg, g1 = *(const f32x4*)(bg + 4), l0 = *(const f32x4*)(bg + FF), l1 = *(const f32x4*)(bg + FF + 4);
;         float rsb[8];
; #pragma unroll
;         for (int q = 0; q < 8; ++q) rsb[q] = ssq[tokTab[u.pm * 256 + row0 + (q >> 2) * 128 + (q & 3) * 16]] * W8_INV;
; #pragma unroll
;         for (int ai = 0; ai < 2; ++ai)
; #pragma unroll
;             for (int m = 0; m < 4; ++m) { const int r = row0 + ai * 128 + m * 16; const float rs = rsb[ai * 4 + m];
;                 float a[8];
; #pragma unroll
;                 for (int j = 0; j < 8; ++j) { const float gb = j < 4 ? g0[j & 3] : g1[j & 3], lb = j < 4 ? l0[j & 3] : l1[j & 3];
;                     const float gl = fminf(acc[ai][0][m][j >> 2][j & 3] * rs + gb, 7.0f), ln = fminf(fmaxf(acc[ai][1][m][j >> 2][j & 3] * rs + lb, -7.0f), 7.0f);
;                     a[j] = gl * __builtin_amdgcn_rcpf(1.0f + __builtin_amdgcn_exp2f(-1.702f * 1.4426950408889634f * gl)) * (ln + 1.0f); }
;                 v2u w; w.x = pk4_fp8(a[0], a[1], a[2], a[3]); w.y = pk4_fp8(a[4], a[5], a[6], a[7]);
;                 *(v2u*)(ACT + ((size_t)u.z * 256 + r) * FF + c0) = w; }
	v_mul_f32_e32 v34, 0xc01d265f, v33
	v_mul_f32_e32 v27, v27, v28
	v_fma_f32 v28, v148, v25, v4
	v_rcp_f32_e32 v32, v32
	v_exp_f32_e32 v34, v34
	v_med3_f32 v28, v28, s23, v236
	v_add_f32_e32 v28, 1.0, v28
	v_mul_f32_e32 v28, v28, v29
	v_fma_f32 v29, v149, v25, v5
	v_med3_f32 v29, v29, s23, v236
	v_mul_f32_e32 v31, v31, v32
	v_add_f32_e32 v32, 1.0, v34
	v_add_f32_e32 v29, 1.0, v29
	v_rcp_f32_e32 v32, v32
	v_mul_f32_e32 v29, v29, v30
	v_fma_f32 v30, v150, v25, v6
	v_med3_f32 v30, v30, s23, v236
	v_fma_f32 v25, v151, v25, v7
	v_add_f32_e32 v30, 1.0, v30
	v_med3_f32 v25, v25, s23, v236
	v_mul_f32_e32 v30, v30, v31
	v_mul_f32_e32 v31, v33, v32
	v_add_f32_e32 v25, 1.0, v25
	v_mul_f32_e32 v25, v25, v31
	v_med3_f32 v31, v18, s24, v237
	v_med3_f32 v19, v19, s24, v237
	v_mov_b32_e32 v18, v65
	v_cvt_pk_fp8_f32 v18, v31, v19
	v_med3_f32 v28, v28, s24, v237
	v_med3_f32 v29, v29, s24, v237
	v_mov_b32_e32 v19, v65
	v_cvt_pk_fp8_f32 v19, v28, v29
	v_med3_f32 v26, v26, s24, v237
	v_med3_f32 v27, v27, s24, v237
	v_cvt_pk_fp8_f32 v18, v26, v27 op_sel:[0,0,1]
	v_med3_f32 v26, v30, s24, v237
	v_med3_f32 v25, v25, s24, v237
	v_cvt_pk_fp8_f32 v19, v26, v25 op_sel:[0,0,1]
	v_fma_f32 v25, v144, v24, v0
	v_min_f32_e32 v25, 0x40e00000, v25
	v_mul_f32_e32 v27, 0xc01d265f, v25
	v_add_co_u32_e32 v26, vcc, s57, v16
	v_exp_f32_e32 v28, v27
	s_nop 0
	v_addc_co_u32_e32 v27, vcc, 0, v17, vcc
	global_store_dwordx2 v[26:27], v[18:19], off
	v_fma_f32 v26, v145, v24, v1
	v_min_f32_e32 v26, 0x40e00000, v26
	v_add_f32_e32 v19, 1.0, v28
	v_mul_f32_e32 v27, 0xc01d265f, v26
	v_rcp_f32_e32 v19, v19
	v_exp_f32_e32 v27, v27
	v_fma_f32 v28, v147, v24, v3
	v_min_f32_e32 v28, 0x40e00000, v28
	v_mul_f32_e32 v19, v25, v19
	v_add_f32_e32 v25, 1.0, v27
	v_rcp_f32_e32 v25, v25
	v_mul_f32_e32 v29, 0xc01d265f, v28
	v_exp_f32_e32 v29, v29
	v_fma_f32 v30, v137, v24, v13
	v_mul_f32_e32 v25, v26, v25
	v_fma_f32 v26, v146, v24, v2
	v_min_f32_e32 v26, 0x40e00000, v26
	v_mul_f32_e32 v27, 0xc01d265f, v26
	v_exp_f32_e32 v27, v27
	v_min_f32_e32 v30, 0x40e00000, v30
	v_mul_f32_e32 v31, 0xc01d265f, v30
	v_exp_f32_e32 v31, v31
	v_add_f32_e32 v27, 1.0, v27
	v_rcp_f32_e32 v27, v27
	v_fma_f32 v18, v140, v24, v8
	v_med3_f32 v18, v18, s23, v236
	v_add_f32_e32 v18, 1.0, v18
	v_mul_f32_e32 v26, v26, v27
	v_add_f32_e32 v27, 1.0, v29
	v_rcp_f32_e32 v27, v27
	v_mul_f32_e32 v18, v18, v19
	v_fma_f32 v19, v141, v24, v9
	v_med3_f32 v19, v19, s23, v236
	v_mul_f32_e32 v27, v28, v27
	v_fma_f32 v28, v136, v24, v12
	v_min_f32_e32 v28, 0x40e00000, v28
	v_mul_f32_e32 v29, 0xc01d265f, v28
	v_exp_f32_e32 v29, v29
	v_add_f32_e32 v19, 1.0, v19
	v_mul_f32_e32 v19, v19, v25
	v_fma_f32 v25, v142, v24, v10
	v_add_f32_e32 v29, 1.0, v29
	v_rcp_f32_e32 v29, v29
	v_med3_f32 v25, v25, s23, v236
	v_add_f32_e32 v25, 1.0, v25
	v_mul_f32_e32 v25, v25, v26
	v_mul_f32_e32 v28, v28, v29
	v_add_f32_e32 v29, 1.0, v31
	v_rcp_f32_e32 v29, v29
	v_fma_f32 v26, v143, v24, v11
	v_fma_f32 v32, v139, v24, v15
	v_med3_f32 v26, v26, s23, v236
	v_mul_f32_e32 v29, v30, v29
	v_fma_f32 v30, v138, v24, v14
	v_min_f32_e32 v30, 0x40e00000, v30
	v_mul_f32_e32 v31, 0xc01d265f, v30
	v_exp_f32_e32 v31, v31
	v_min_f32_e32 v32, 0x40e00000, v32
	v_add_f32_e32 v26, 1.0, v26
	v_mul_f32_e32 v33, 0xc01d265f, v32
	v_add_f32_e32 v31, 1.0, v31
	v_mul_f32_e32 v26, v26, v27
	v_fma_f32 v27, v132, v24, v4
	v_rcp_f32_e32 v31, v31
	v_exp_f32_e32 v33, v33
	v_med3_f32 v27, v27, s23, v236
	v_add_f32_e32 v27, 1.0, v27
	v_mul_f32_e32 v27, v27, v28
	v_fma_f32 v28, v133, v24, v5
	v_med3_f32 v28, v28, s23, v236
	v_mul_f32_e32 v30, v30, v31
	v_add_f32_e32 v31, 1.0, v33
	v_add_f32_e32 v28, 1.0, v28
	v_rcp_f32_e32 v31, v31
	v_mul_f32_e32 v28, v28, v29
	v_fma_f32 v29, v134, v24, v6
	v_med3_f32 v29, v29, s23, v236
	v_fma_f32 v24, v135, v24, v7
	v_add_f32_e32 v29, 1.0, v29
	v_med3_f32 v24, v24, s23, v236
	v_mul_f32_e32 v29, v29, v30
	v_mul_f32_e32 v30, v32, v31
	v_add_f32_e32 v24, 1.0, v24
	v_mul_f32_e32 v24, v24, v30
	v_med3_f32 v30, v18, s24, v237
	v_med3_f32 v19, v19, s24, v237
	v_mov_b32_e32 v18, v65
	v_cvt_pk_fp8_f32 v18, v30, v19
	v_med3_f32 v27, v27, s24, v237
	v_med3_f32 v28, v28, s24, v237
	v_mov_b32_e32 v19, v65
	v_cvt_pk_fp8_f32 v19, v27, v28
	v_med3_f32 v25, v25, s24, v237
	v_med3_f32 v26, v26, s24, v237
	v_cvt_pk_fp8_f32 v18, v25, v26 op_sel:[0,0,1]
	v_med3_f32 v25, v29, s24, v237
	v_med3_f32 v24, v24, s24, v237
	v_cvt_pk_fp8_f32 v19, v25, v24 op_sel:[0,0,1]
	v_fma_f32 v25, v128, v23, v0
	v_min_f32_e32 v26, 0x40e00000, v25
	v_add_co_u32_e32 v24, vcc, s69, v16
	v_mul_f32_e32 v25, 0xc01d265f, v26
	v_exp_f32_e32 v27, v25
	v_addc_co_u32_e32 v25, vcc, 0, v17, vcc
	global_store_dwordx2 v[24:25], v[18:19], off
	v_fma_f32 v24, v129, v23, v1
	v_min_f32_e32 v24, 0x40e00000, v24
	v_mul_f32_e32 v25, 0xc01d265f, v24
	v_exp_f32_e32 v25, v25
	v_add_f32_e32 v19, 1.0, v27
	v_rcp_f32_e32 v19, v19
	v_fma_f32 v27, v131, v23, v3
	v_add_f32_e32 v25, 1.0, v25
	v_rcp_f32_e32 v25, v25
	v_mul_f32_e32 v19, v26, v19
	v_min_f32_e32 v27, 0x40e00000, v27
	v_mul_f32_e32 v28, 0xc01d265f, v27
	v_mul_f32_e32 v24, v24, v25
	v_fma_f32 v25, v130, v23, v2
	v_min_f32_e32 v25, 0x40e00000, v25
	v_mul_f32_e32 v26, 0xc01d265f, v25
	v_exp_f32_e32 v26, v26
	v_exp_f32_e32 v28, v28
	v_fma_f32 v29, v121, v23, v13
	v_min_f32_e32 v29, 0x40e00000, v29
	v_add_f32_e32 v26, 1.0, v26
	v_rcp_f32_e32 v26, v26
	v_mul_f32_e32 v30, 0xc01d265f, v29
	v_exp_f32_e32 v30, v30
	v_fma_f32 v18, v124, v23, v8
	v_mul_f32_e32 v25, v25, v26
	v_add_f32_e32 v26, 1.0, v28
	v_rcp_f32_e32 v26, v26
	v_med3_f32 v18, v18, s23, v236
	v_add_f32_e32 v18, 1.0, v18
	v_mul_f32_e32 v18, v18, v19
	v_mul_f32_e32 v26, v27, v26
	v_fma_f32 v27, v120, v23, v12
;     __device__ __forceinline__ void operator()(const f32x4 (&acc)[2][2][4][2], const Unit& u, int wr, int wc, int fr, int fq) const {
;     ...
;         const int e = blkE[u.z], c0 = u.pn * 128 + wc * 32 + 8 * fq, row0 = wr * 64 + fr;
;         const float* bg = bup + (size_t)e * 2 * FF + c0; const f32x4 g0 = *(const f32x4*)bg, g1 = *(const f32x4*)(bg + 4), l0 = *(const f32x4*)(bg + FF), l1 = *(const f32x4*)(bg + FF + 4);
;         float rsb[8];
; #pragma unroll
;         for (int q = 0; q < 8; ++q) rsb[q] = ssq[tokTab[u.pm * 256 + row0 + (q >> 2) * 128 + (q & 3) * 16]] * W8_INV;
; #pragma unroll
;         for (int ai = 0; ai < 2; ++ai)
; #pragma unroll
;             for (int m = 0; m < 4; ++m) { const int r = row0 + ai * 128 + m * 16; const float rs = rsb[ai * 4 + m];
;                 float a[8];
; #pragma unroll
;                 for (int j = 0; j < 8; ++j) { const float gb = j < 4 ? g0[j & 3] : g1[j & 3], lb = j < 4 ? l0[j & 3] : l1[j & 3];
;                     const float gl = fminf(acc[ai][0][m][j >> 2][j & 3] * rs + gb, 7.0f), ln = fminf(fmaxf(acc[ai][1][m][j >> 2][j & 3] * rs + lb, -7.0f), 7.0f);
;                     a[j] = gl * __builtin_amdgcn_rcpf(1.0f + __builtin_amdgcn_exp2f(-1.702f * 1.4426950408889634f * gl)) * (ln + 1.0f); }
;                 v2u w; w.x = pk4_fp8(a[0], a[1], a[2], a[3]); w.y = pk4_fp8(a[4], a[5], a[6], a[7]);
;                 *(v2u*)(ACT + ((size_t)u.z * 256 + r) * FF + c0) = w; }
	v_min_f32_e32 v27, 0x40e00000, v27
	v_mul_f32_e32 v28, 0xc01d265f, v27
	v_exp_f32_e32 v28, v28
	v_fma_f32 v19, v125, v23, v9
	v_med3_f32 v19, v19, s23, v236
	v_add_f32_e32 v19, 1.0, v19
	v_add_f32_e32 v28, 1.0, v28
	v_rcp_f32_e32 v28, v28
	v_mul_f32_e32 v19, v19, v24
	v_fma_f32 v24, v126, v23, v10
	v_med3_f32 v24, v24, s23, v236
	v_mul_f32_e32 v27, v27, v28
	v_add_f32_e32 v28, 1.0, v30
	v_rcp_f32_e32 v28, v28
	v_add_f32_e32 v24, 1.0, v24
	v_mul_f32_e32 v24, v24, v25
	v_fma_f32 v25, v127, v23, v11
	v_mul_f32_e32 v28, v29, v28
	v_fma_f32 v29, v122, v23, v14
	v_min_f32_e32 v29, 0x40e00000, v29
	v_mul_f32_e32 v30, 0xc01d265f, v29
	v_exp_f32_e32 v30, v30
	v_fma_f32 v31, v123, v23, v15
	v_med3_f32 v25, v25, s23, v236
	v_min_f32_e32 v31, 0x40e00000, v31
	v_add_f32_e32 v25, 1.0, v25
	v_add_f32_e32 v30, 1.0, v30
	v_mul_f32_e32 v32, 0xc01d265f, v31
	v_mul_f32_e32 v25, v25, v26
	v_fma_f32 v26, v116, v23, v4
	v_rcp_f32_e32 v30, v30
	v_exp_f32_e32 v32, v32
	v_med3_f32 v26, v26, s23, v236
	v_add_f32_e32 v26, 1.0, v26
	v_mul_f32_e32 v26, v26, v27
	v_fma_f32 v27, v117, v23, v5
	v_med3_f32 v27, v27, s23, v236
	v_mul_f32_e32 v29, v29, v30
	v_add_f32_e32 v30, 1.0, v32
	v_add_f32_e32 v27, 1.0, v27
	v_rcp_f32_e32 v30, v30
	v_mul_f32_e32 v27, v27, v28
	v_fma_f32 v28, v118, v23, v6
	v_med3_f32 v28, v28, s23, v236
	v_fma_f32 v23, v119, v23, v7
	v_add_f32_e32 v28, 1.0, v28
	v_med3_f32 v23, v23, s23, v236
	v_mul_f32_e32 v28, v28, v29
	v_mul_f32_e32 v29, v31, v30
	v_add_f32_e32 v23, 1.0, v23
	v_mul_f32_e32 v23, v23, v29
	v_med3_f32 v29, v18, s24, v237
	v_med3_f32 v19, v19, s24, v237
	v_mov_b32_e32 v18, v65
	v_cvt_pk_fp8_f32 v18, v29, v19
	v_med3_f32 v26, v26, s24, v237
	v_med3_f32 v27, v27, s24, v237
	v_mov_b32_e32 v19, v65
	v_cvt_pk_fp8_f32 v19, v26, v27
	v_med3_f32 v24, v24, s24, v237
	v_med3_f32 v25, v25, s24, v237
	v_cvt_pk_fp8_f32 v18, v24, v25 op_sel:[0,0,1]
	v_med3_f32 v24, v28, s24, v237
	v_med3_f32 v23, v23, s24, v237
	v_cvt_pk_fp8_f32 v19, v24, v23 op_sel:[0,0,1]
	v_fma_f32 v23, v112, v22, v0
	v_min_f32_e32 v23, 0x40e00000, v23
	s_mov_b32 s4, 0x40000
	v_mul_f32_e32 v25, 0xc01d265f, v23
	v_add_co_u32_e32 v24, vcc, s4, v16
	v_exp_f32_e32 v26, v25
	s_nop 0
	v_addc_co_u32_e32 v25, vcc, 0, v17, vcc
	global_store_dwordx2 v[24:25], v[18:19], off
	v_fma_f32 v24, v113, v22, v1
	v_min_f32_e32 v24, 0x40e00000, v24
	v_add_f32_e32 v19, 1.0, v26
	v_mul_f32_e32 v25, 0xc01d265f, v24
	v_rcp_f32_e32 v19, v19
	v_exp_f32_e32 v25, v25
	v_fma_f32 v26, v115, v22, v3
	v_min_f32_e32 v26, 0x40e00000, v26
	v_mul_f32_e32 v19, v23, v19
	v_add_f32_e32 v23, 1.0, v25
	v_rcp_f32_e32 v23, v23
	v_mul_f32_e32 v27, 0xc01d265f, v26
	v_exp_f32_e32 v27, v27
	v_fma_f32 v28, v105, v22, v13
	v_mul_f32_e32 v23, v24, v23
	v_fma_f32 v24, v114, v22, v2
	v_min_f32_e32 v24, 0x40e00000, v24
	v_mul_f32_e32 v25, 0xc01d265f, v24
	v_exp_f32_e32 v25, v25
	v_min_f32_e32 v28, 0x40e00000, v28
	v_mul_f32_e32 v29, 0xc01d265f, v28
	v_exp_f32_e32 v29, v29
	v_add_f32_e32 v25, 1.0, v25
	v_rcp_f32_e32 v25, v25
	v_fma_f32 v18, v108, v22, v8
	v_med3_f32 v18, v18, s23, v236
	v_add_f32_e32 v18, 1.0, v18
	v_mul_f32_e32 v24, v24, v25
	v_add_f32_e32 v25, 1.0, v27
	v_rcp_f32_e32 v25, v25
	v_mul_f32_e32 v18, v18, v19
	v_fma_f32 v19, v109, v22, v9
	v_med3_f32 v19, v19, s23, v236
	v_mul_f32_e32 v25, v26, v25
	v_fma_f32 v26, v104, v22, v12
	v_min_f32_e32 v26, 0x40e00000, v26
	v_mul_f32_e32 v27, 0xc01d265f, v26
	v_exp_f32_e32 v27, v27
	v_add_f32_e32 v19, 1.0, v19
	v_mul_f32_e32 v19, v19, v23
	v_fma_f32 v23, v110, v22, v10
	v_add_f32_e32 v27, 1.0, v27
	v_rcp_f32_e32 v27, v27
	v_med3_f32 v23, v23, s23, v236
	v_add_f32_e32 v23, 1.0, v23
	v_mul_f32_e32 v23, v23, v24
	v_mul_f32_e32 v26, v26, v27
	v_add_f32_e32 v27, 1.0, v29
	v_rcp_f32_e32 v27, v27
	v_fma_f32 v24, v111, v22, v11
	v_fma_f32 v30, v107, v22, v15
	v_med3_f32 v24, v24, s23, v236
	v_mul_f32_e32 v27, v28, v27
	v_fma_f32 v28, v106, v22, v14
	v_min_f32_e32 v28, 0x40e00000, v28
	v_mul_f32_e32 v29, 0xc01d265f, v28
	v_exp_f32_e32 v29, v29
	v_min_f32_e32 v30, 0x40e00000, v30
	v_add_f32_e32 v24, 1.0, v24
	v_mul_f32_e32 v31, 0xc01d265f, v30
	v_add_f32_e32 v29, 1.0, v29
	v_mul_f32_e32 v24, v24, v25
	v_fma_f32 v25, v100, v22, v4
	v_rcp_f32_e32 v29, v29
	v_exp_f32_e32 v31, v31
	v_med3_f32 v25, v25, s23, v236
	v_add_f32_e32 v25, 1.0, v25
	v_mul_f32_e32 v25, v25, v26
	v_fma_f32 v26, v101, v22, v5
	v_med3_f32 v26, v26, s23, v236
	v_mul_f32_e32 v28, v28, v29
	v_add_f32_e32 v29, 1.0, v31
	v_add_f32_e32 v26, 1.0, v26
	v_rcp_f32_e32 v29, v29
	v_mul_f32_e32 v26, v26, v27
	v_fma_f32 v27, v102, v22, v6
	v_med3_f32 v27, v27, s23, v236
	v_fma_f32 v22, v103, v22, v7
	v_add_f32_e32 v27, 1.0, v27
	v_med3_f32 v22, v22, s23, v236
	v_mul_f32_e32 v27, v27, v28
	v_mul_f32_e32 v28, v30, v29
	v_add_f32_e32 v22, 1.0, v22
	v_mul_f32_e32 v22, v22, v28
	v_med3_f32 v28, v18, s24, v237
	v_med3_f32 v19, v19, s24, v237
	v_mov_b32_e32 v18, v65
	v_cvt_pk_fp8_f32 v18, v28, v19
	v_med3_f32 v25, v25, s24, v237
	v_med3_f32 v26, v26, s24, v237
	v_mov_b32_e32 v19, v65
	v_cvt_pk_fp8_f32 v19, v25, v26
	v_med3_f32 v23, v23, s24, v237
	v_med3_f32 v24, v24, s24, v237
	v_cvt_pk_fp8_f32 v18, v23, v24 op_sel:[0,0,1]
	v_med3_f32 v23, v27, s24, v237
	v_med3_f32 v22, v22, s24, v237
	v_cvt_pk_fp8_f32 v19, v23, v22 op_sel:[0,0,1]
	v_fma_f32 v23, v96, v21, v0
	s_mov_b32 s4, 0x48000
	v_min_f32_e32 v24, 0x40e00000, v23
	v_add_co_u32_e32 v22, vcc, s4, v16
	v_mul_f32_e32 v23, 0xc01d265f, v24
	v_exp_f32_e32 v25, v23
	v_addc_co_u32_e32 v23, vcc, 0, v17, vcc
	global_store_dwordx2 v[22:23], v[18:19], off
	v_fma_f32 v22, v97, v21, v1
	v_min_f32_e32 v22, 0x40e00000, v22
	v_mul_f32_e32 v23, 0xc01d265f, v22
	v_exp_f32_e32 v23, v23
	v_add_f32_e32 v19, 1.0, v25
;     __device__ __forceinline__ void operator()(const f32x4 (&acc)[2][2][4][2], const Unit& u, int wr, int wc, int fr, int fq) const {
;     ...
;         for (int q = 0; q < 8; ++q) rsb[q] = ssq[tokTab[u.pm * 256 + row0 + (q >> 2) * 128 + (q & 3) * 16]] * W8_INV;
; #pragma unroll
;         for (int ai = 0; ai < 2; ++ai)
; #pragma unroll
;             for (int m = 0; m < 4; ++m) { const int r = row0 + ai * 128 + m * 16; const float rs = rsb[ai * 4 + m];
;                 float a[8];
; #pragma unroll
;                 for (int j = 0; j < 8; ++j) { const float gb = j < 4 ? g0[j & 3] : g1[j & 3], lb = j < 4 ? l0[j & 3] : l1[j & 3];
;                     const float gl = fminf(acc[ai][0][m][j >> 2][j & 3] * rs + gb, 7.0f), ln = fminf(fmaxf(acc[ai][1][m][j >> 2][j & 3] * rs + lb, -7.0f), 7.0f);
;                     a[j] = gl * __builtin_amdgcn_rcpf(1.0f + __builtin_amdgcn_exp2f(-1.702f * 1.4426950408889634f * gl)) * (ln + 1.0f); }
;                 v2u w; w.x = pk4_fp8(a[0], a[1], a[2], a[3]); w.y = pk4_fp8(a[4], a[5], a[6], a[7]);
;                 *(v2u*)(ACT + ((size_t)u.z * 256 + r) * FF + c0) = w; }
;     }
	v_rcp_f32_e32 v19, v19
	v_fma_f32 v25, v99, v21, v3
	v_add_f32_e32 v23, 1.0, v23
	v_rcp_f32_e32 v23, v23
	v_mul_f32_e32 v19, v24, v19
	v_min_f32_e32 v25, 0x40e00000, v25
	v_mul_f32_e32 v26, 0xc01d265f, v25
	v_mul_f32_e32 v22, v22, v23
	v_fma_f32 v23, v98, v21, v2
	v_min_f32_e32 v23, 0x40e00000, v23
	v_mul_f32_e32 v24, 0xc01d265f, v23
	v_exp_f32_e32 v24, v24
	v_exp_f32_e32 v26, v26
	v_fma_f32 v27, v89, v21, v13
	v_min_f32_e32 v27, 0x40e00000, v27
	v_add_f32_e32 v24, 1.0, v24
	v_rcp_f32_e32 v24, v24
	v_mul_f32_e32 v28, 0xc01d265f, v27
	v_exp_f32_e32 v28, v28
	v_fma_f32 v18, v92, v21, v8
	v_mul_f32_e32 v23, v23, v24
	v_add_f32_e32 v24, 1.0, v26
	v_rcp_f32_e32 v24, v24
	v_med3_f32 v18, v18, s23, v236
	v_add_f32_e32 v18, 1.0, v18
	v_mul_f32_e32 v18, v18, v19
	v_mul_f32_e32 v24, v25, v24
	v_fma_f32 v25, v88, v21, v12
	v_min_f32_e32 v25, 0x40e00000, v25
	v_mul_f32_e32 v26, 0xc01d265f, v25
	v_exp_f32_e32 v26, v26
	v_fma_f32 v19, v93, v21, v9
	v_med3_f32 v19, v19, s23, v236
	v_add_f32_e32 v19, 1.0, v19
	v_add_f32_e32 v26, 1.0, v26
	v_rcp_f32_e32 v26, v26
	v_mul_f32_e32 v19, v19, v22
	v_fma_f32 v22, v94, v21, v10
	v_med3_f32 v22, v22, s23, v236
	v_mul_f32_e32 v25, v25, v26
	v_add_f32_e32 v26, 1.0, v28
	v_rcp_f32_e32 v26, v26
	v_add_f32_e32 v22, 1.0, v22
	v_mul_f32_e32 v22, v22, v23
	v_fma_f32 v23, v95, v21, v11
	v_mul_f32_e32 v26, v27, v26
	v_fma_f32 v27, v90, v21, v14
	v_min_f32_e32 v27, 0x40e00000, v27
	v_mul_f32_e32 v28, 0xc01d265f, v27
	v_exp_f32_e32 v28, v28
	v_fma_f32 v29, v91, v21, v15
	v_med3_f32 v23, v23, s23, v236
	v_min_f32_e32 v29, 0x40e00000, v29
	v_add_f32_e32 v23, 1.0, v23
	v_add_f32_e32 v28, 1.0, v28
	v_mul_f32_e32 v30, 0xc01d265f, v29
	v_mul_f32_e32 v23, v23, v24
	v_fma_f32 v24, v84, v21, v4
	v_rcp_f32_e32 v28, v28
	v_exp_f32_e32 v30, v30
	v_med3_f32 v24, v24, s23, v236
	v_add_f32_e32 v24, 1.0, v24
	v_mul_f32_e32 v24, v24, v25
	v_fma_f32 v25, v85, v21, v5
	v_med3_f32 v25, v25, s23, v236
	v_mul_f32_e32 v27, v27, v28
	v_add_f32_e32 v28, 1.0, v30
	v_add_f32_e32 v25, 1.0, v25
	v_rcp_f32_e32 v28, v28
	v_mul_f32_e32 v25, v25, v26
	v_fma_f32 v26, v86, v21, v6
	v_med3_f32 v26, v26, s23, v236
	v_fma_f32 v21, v87, v21, v7
	v_add_f32_e32 v26, 1.0, v26
	v_med3_f32 v21, v21, s23, v236
	v_mul_f32_e32 v26, v26, v27
	v_mul_f32_e32 v27, v29, v28
	v_add_f32_e32 v21, 1.0, v21
	v_mul_f32_e32 v21, v21, v27
	v_med3_f32 v27, v18, s24, v237
	v_med3_f32 v19, v19, s24, v237
	v_mov_b32_e32 v18, v65
	v_cvt_pk_fp8_f32 v18, v27, v19
	v_med3_f32 v24, v24, s24, v237
	v_med3_f32 v25, v25, s24, v237
	v_mov_b32_e32 v19, v65
	v_cvt_pk_fp8_f32 v19, v24, v25
	v_mul_f32_e32 v20, 0x3b800000, v20
	v_med3_f32 v22, v22, s24, v237
	v_med3_f32 v23, v23, s24, v237
	v_fma_f32 v14, v74, v20, v14
	v_cvt_pk_fp8_f32 v18, v22, v23 op_sel:[0,0,1]
	v_med3_f32 v22, v26, s24, v237
	v_med3_f32 v21, v21, s24, v237
	v_min_f32_e32 v14, 0x40e00000, v14
	v_cvt_pk_fp8_f32 v19, v22, v21 op_sel:[0,0,1]
	v_mul_f32_e32 v21, 0xc01d265f, v14
	v_exp_f32_e32 v21, v21
	s_mov_b32 s4, 0x50000
	v_add_co_u32_e32 v22, vcc, s4, v16
	v_fma_f32 v13, v73, v20, v13
	s_nop 0
	v_addc_co_u32_e32 v23, vcc, 0, v17, vcc
	global_store_dwordx2 v[22:23], v[18:19], off
	v_add_f32_e32 v18, 1.0, v21
	v_rcp_f32_e32 v18, v18
	v_min_f32_e32 v13, 0x40e00000, v13
	v_fma_f32 v6, v70, v20, v6
	v_med3_f32 v6, v6, s23, v236
	v_mul_f32_e32 v14, v14, v18
	v_mul_f32_e32 v18, 0xc01d265f, v13
	v_exp_f32_e32 v18, v18
	v_add_f32_e32 v6, 1.0, v6
	v_fma_f32 v12, v72, v20, v12
	v_mul_f32_e32 v6, v6, v14
	v_add_f32_e32 v14, 1.0, v18
	v_min_f32_e32 v12, 0x40e00000, v12
	v_rcp_f32_e32 v14, v14
	v_mul_f32_e32 v18, 0xc01d265f, v12
	v_exp_f32_e32 v18, v18
	v_fma_f32 v5, v69, v20, v5
	v_med3_f32 v5, v5, s23, v236
	v_add_f32_e32 v5, 1.0, v5
	v_mul_f32_e32 v13, v13, v14
	v_mul_f32_e32 v5, v5, v13
	v_add_f32_e32 v13, 1.0, v18
	v_rcp_f32_e32 v13, v13
	v_fma_f32 v3, v83, v20, v3
	v_min_f32_e32 v3, 0x40e00000, v3
	v_fma_f32 v4, v68, v20, v4
	v_mul_f32_e32 v12, v12, v13
	v_mul_f32_e32 v13, 0xc01d265f, v3
	v_exp_f32_e32 v13, v13
	v_med3_f32 v4, v4, s23, v236
	v_add_f32_e32 v4, 1.0, v4
	v_fma_f32 v2, v82, v20, v2
	v_mul_f32_e32 v4, v4, v12
	v_add_f32_e32 v12, 1.0, v13
	v_min_f32_e32 v2, 0x40e00000, v2
	v_rcp_f32_e32 v12, v12
	v_mul_f32_e32 v13, 0xc01d265f, v2
	v_exp_f32_e32 v13, v13
	v_fma_f32 v11, v79, v20, v11
	v_med3_f32 v11, v11, s23, v236
	v_add_f32_e32 v11, 1.0, v11
	v_mul_f32_e32 v3, v3, v12
	v_mul_f32_e32 v3, v11, v3
	v_add_f32_e32 v11, 1.0, v13
	v_rcp_f32_e32 v11, v11
	v_fma_f32 v10, v78, v20, v10
	v_med3_f32 v10, v10, s23, v236
	v_fma_f32 v1, v81, v20, v1
	v_add_f32_e32 v10, 1.0, v10
	v_mul_f32_e32 v2, v2, v11
	v_min_f32_e32 v1, 0x40e00000, v1
	v_mul_f32_e32 v2, v10, v2
	v_mul_f32_e32 v10, 0xc01d265f, v1
	v_exp_f32_e32 v10, v10
	v_fmac_f32_e32 v0, v80, v20
	v_min_f32_e32 v0, 0x40e00000, v0
	v_mul_f32_e32 v11, 0xc01d265f, v0
	v_add_f32_e32 v10, 1.0, v10
	v_rcp_f32_e32 v10, v10
	v_exp_f32_e32 v11, v11
	v_fma_f32 v9, v77, v20, v9
	v_med3_f32 v9, v9, s23, v236
	v_fmac_f32_e32 v15, v75, v20
	v_add_f32_e32 v9, 1.0, v9
	v_mul_f32_e32 v1, v1, v10
	v_min_f32_e32 v10, 0x40e00000, v15
	v_mul_f32_e32 v1, v9, v1
	v_add_f32_e32 v9, 1.0, v11
	v_mul_f32_e32 v11, 0xc01d265f, v10
	v_rcp_f32_e32 v9, v9
	v_exp_f32_e32 v11, v11
	v_fmac_f32_e32 v8, v76, v20
	v_med3_f32 v8, v8, s23, v236
	v_mul_f32_e32 v0, v0, v9
	v_add_f32_e32 v9, 1.0, v11
	v_rcp_f32_e32 v9, v9
	v_fmac_f32_e32 v7, v71, v20
	v_add_f32_e32 v8, 1.0, v8
	v_med3_f32 v7, v7, s23, v236
	v_mul_f32_e32 v0, v8, v0
	v_mul_f32_e32 v8, v10, v9
	v_add_f32_e32 v7, 1.0, v7
	v_mul_f32_e32 v7, v7, v8
	v_med3_f32 v8, v0, s24, v237
	v_med3_f32 v1, v1, s24, v237
	v_mov_b32_e32 v0, v65
	v_cvt_pk_fp8_f32 v0, v8, v1
	v_med3_f32 v4, v4, s24, v237
	v_med3_f32 v5, v5, s24, v237
	v_mov_b32_e32 v1, v65
	v_cvt_pk_fp8_f32 v1, v4, v5
	v_med3_f32 v2, v2, s24, v237
	v_med3_f32 v3, v3, s24, v237
	v_cvt_pk_fp8_f32 v0, v2, v3 op_sel:[0,0,1]
	v_med3_f32 v2, v6, s24, v237
	v_med3_f32 v3, v7, s24, v237
	v_cvt_pk_fp8_f32 v1, v2, v3 op_sel:[0,0,1]
	v_add_co_u32_e32 v2, vcc, 0x58000, v16
	s_nop 1
	v_addc_co_u32_e32 v3, vcc, 0, v17, vcc
	global_store_dwordx2 v[2:3], v[0:1], off
	s_cbranch_scc1 .LBB0_1541
; __device__ __forceinline__ int lane_id_now() { unsigned z = 0u; asm volatile("" : "+v"(z)); return (int)__builtin_amdgcn_mbcnt_hi(~0u, __builtin_amdgcn_mbcnt_lo(~0u, z)); }
; #define GAS __attribute__((address_space(1)))
; template <bool GAIN, bool NT = false> __device__ __forceinline__ void titem8_load(const TItem& d, int lane, f32x4 (&r)[16], f32x4 (&g)[4]) {
;     const int q = lane & 7, kg = lane >> 3; const unsigned lo = (unsigned)((16 * kg) * d.N + 4 * q) * 4u;
;     const GAS char* base = (const GAS char*)d.src;
; #pragma unroll
;     for (int j = 0; j < 16; ++j) { const GAS f32x4* p = (const GAS f32x4*)(base + (size_t)j * (size_t)d.N * 4 + lo); r[j] = NT ? __builtin_nontemporal_load(p) : *p; }
;     __device__ __forceinline__ void convert_share() const {
;         const int lane = lane_id_now(), gw = c * NWAVES + wave, NGW = G * NWAVES;
;         constexpr int NIT = E * (FF / 128) * (D / 32);
;         TSTREAM(NIT, dec_dn, TI8L_NT, TI8S_NT);
;     }
	v_readlane_b32 s0, v254, 26
	v_readlane_b32 s1, v254, 27
	v_mov_b32_e32 v0, v65
	s_andn2_b64 vcc, exec, s[0:1]
	s_cbranch_vccnz .LBB0_1541
	v_mbcnt_lo_u32_b32 v64, -1, 0
	v_mbcnt_hi_u32_b32 v64, -1, v64
	v_and_b32_e32 v194, 15, v64
	v_lshrrev_b32_e32 v195, 4, v64
	v_lshlrev_b32_e32 v246, 17, v195
	v_lshl_or_b32 v246, v194, 4, v246
	v_add_u32_e32 v247, 0x2000, v246
	v_add_u32_e32 v248, 0x4000, v246
	v_add_u32_e32 v249, 0x6000, v246
	v_lshlrev_b32_e32 v250, 13, v194
	v_lshl_or_b32 v250, v195, 4, v250
	v_add_u32_e32 v251, 0x1000, v250
	v_readlane_b32 s0, v254, 60
	v_readlane_b32 s4, v254, 4
	v_readlane_b32 s5, v254, 5
	s_nop 3
	s_lshl_b32 s1, s92, 3
	s_add_i32 s0, s0, s1
	s_lshr_b32 s1, s0, 10
	s_and_b32 s0, s0, 0x3ff
	s_lshr_b32 s2, s0, 5
	s_and_b32 s0, s0, 31
	s_lshl_b32 s35, s1, 24
	s_lshl_b32 s38, s2, 19
	s_add_i32 s35, s35, s38
	s_lshl_b32 s38, s0, 8
	s_add_i32 s35, s35, s38
	s_add_u32 s4, s4, s35
	s_addc_u32 s5, s5, 0
	s_add_u32 s6, s4, 0x8000
	s_addc_u32 s7, s5, 0
	s_add_u32 s8, s4, 0x10000
	s_addc_u32 s9, s5, 0
	s_add_u32 s38, s4, 0x18000
	s_addc_u32 s39, s5, 0
	s_lshl_b32 s35, s1, 22
	s_lshl_b32 s40, s0, 17
	s_add_i32 s35, s35, s40
	s_lshl_b32 s40, s2, 6
	s_add_i32 s35, s35, s40
	s_add_u32 s42, s78, 0x57dc8000
	s_addc_u32 s43, s79, 0
	s_add_u32 s42, s42, s35
	s_addc_u32 s43, s43, 0
	global_load_dwordx4 v[0:3], v246, s[4:5] nt
	global_load_dwordx4 v[4:7], v247, s[4:5] nt
	global_load_dwordx4 v[8:11], v248, s[4:5] nt
	global_load_dwordx4 v[12:15], v249, s[4:5] nt
	global_load_dwordx4 v[16:19], v246, s[6:7] nt
	global_load_dwordx4 v[20:23], v247, s[6:7] nt
	global_load_dwordx4 v[24:27], v248, s[6:7] nt
	global_load_dwordx4 v[28:31], v249, s[6:7] nt
	global_load_dwordx4 v[32:35], v246, s[8:9] nt
	global_load_dwordx4 v[36:39], v247, s[8:9] nt
	global_load_dwordx4 v[40:43], v248, s[8:9] nt
	global_load_dwordx4 v[44:47], v249, s[8:9] nt
	global_load_dwordx4 v[48:51], v246, s[38:39] nt
	global_load_dwordx4 v[52:55], v247, s[38:39] nt
	global_load_dwordx4 v[56:59], v248, s[38:39] nt
	global_load_dwordx4 v[60:63], v249, s[38:39] nt
	s_add_u32 s4, s4, 0x2000000
	s_addc_u32 s5, s5, 0
	s_add_u32 s6, s6, 0x2000000
	s_addc_u32 s7, s7, 0
	s_add_u32 s8, s8, 0x2000000
	s_addc_u32 s9, s9, 0
	s_add_u32 s38, s38, 0x2000000
	s_addc_u32 s39, s39, 0
	global_load_dwordx4 v[66:69], v246, s[4:5] nt
	global_load_dwordx4 v[70:73], v247, s[4:5] nt
	global_load_dwordx4 v[74:77], v248, s[4:5] nt
	global_load_dwordx4 v[78:81], v249, s[4:5] nt
	global_load_dwordx4 v[82:85], v246, s[6:7] nt
	global_load_dwordx4 v[86:89], v247, s[6:7] nt
	global_load_dwordx4 v[90:93], v248, s[6:7] nt
	global_load_dwordx4 v[94:97], v249, s[6:7] nt
	global_load_dwordx4 v[98:101], v246, s[8:9] nt
	global_load_dwordx4 v[102:105], v247, s[8:9] nt
	global_load_dwordx4 v[106:109], v248, s[8:9] nt
	global_load_dwordx4 v[110:113], v249, s[8:9] nt
	global_load_dwordx4 v[114:117], v246, s[38:39] nt
	global_load_dwordx4 v[118:121], v247, s[38:39] nt
	global_load_dwordx4 v[122:125], v248, s[38:39] nt
	global_load_dwordx4 v[126:129], v249, s[38:39] nt
	s_add_u32 s4, s4, 0x2000000
	s_addc_u32 s5, s5, 0
	s_add_u32 s6, s6, 0x2000000
	s_addc_u32 s7, s7, 0
	s_add_u32 s8, s8, 0x2000000
	s_addc_u32 s9, s9, 0
	s_add_u32 s38, s38, 0x2000000
	s_addc_u32 s39, s39, 0
	global_load_dwordx4 v[130:133], v246, s[4:5] nt
	global_load_dwordx4 v[134:137], v247, s[4:5] nt
	global_load_dwordx4 v[138:141], v248, s[4:5] nt
	global_load_dwordx4 v[142:145], v249, s[4:5] nt
	global_load_dwordx4 v[146:149], v246, s[6:7] nt
	global_load_dwordx4 v[150:153], v247, s[6:7] nt
	global_load_dwordx4 v[154:157], v248, s[6:7] nt
	global_load_dwordx4 v[158:161], v249, s[6:7] nt
	global_load_dwordx4 v[162:165], v246, s[8:9] nt
	global_load_dwordx4 v[166:169], v247, s[8:9] nt
	global_load_dwordx4 v[170:173], v248, s[8:9] nt
	global_load_dwordx4 v[174:177], v249, s[8:9] nt
	global_load_dwordx4 v[178:181], v246, s[38:39] nt
	global_load_dwordx4 v[182:185], v247, s[38:39] nt
	global_load_dwordx4 v[186:189], v248, s[38:39] nt
	global_load_dwordx4 v[190:193], v249, s[38:39] nt
	s_add_u32 s4, s4, 0x2000000
	s_addc_u32 s5, s5, 0
	s_add_u32 s6, s6, 0x2000000
	s_addc_u32 s7, s7, 0
	s_add_u32 s8, s8, 0x2000000
	s_addc_u32 s9, s9, 0
	s_add_u32 s38, s38, 0x2000000
	s_addc_u32 s39, s39, 0
	s_waitcnt vmcnt(32)
; #define GAS __attribute__((address_space(1)))
; template <bool GAIN, bool NT = false> __device__ __forceinline__ void titem8_load(const TItem& d, int lane, f32x4 (&r)[16], f32x4 (&g)[4]) {
;     const int q = lane & 7, kg = lane >> 3; const unsigned lo = (unsigned)((16 * kg) * d.N + 4 * q) * 4u;
;     const GAS char* base = (const GAS char*)d.src;
; #pragma unroll
;     for (int j = 0; j < 16; ++j) { const GAS f32x4* p = (const GAS f32x4*)(base + (size_t)j * (size_t)d.N * 4 + lo); r[j] = NT ? __builtin_nontemporal_load(p) : *p; }
; template <bool GAIN, bool NT = false> __device__ __forceinline__ void titem8_store(const TItem& d, int lane, const f32x4 (&r)[16], const f32x4 (&g)[4]) {
;     const int q = lane & 7, kg = lane >> 3; const unsigned lo = (unsigned)((4 * q) * d.ldk + 16 * kg);
;     GAS char* base = (GAS char*)d.dst;
;     f32x4 s[16];
; #pragma unroll
;     for (int j = 0; j < 16; ++j) s[j] = r[j] * ((GAIN ? g[j >> 2][j & 3] : 1.0f) * W8_SCALE);
; #pragma unroll
;     for (int i = 0; i < 4; ++i) { v4u w;
;         w.x = pk4_fp8w(s[0][i], s[1][i], s[2][i], s[3][i]); w.y = pk4_fp8w(s[4][i], s[5][i], s[6][i], s[7][i]);
;         w.z = pk4_fp8w(s[8][i], s[9][i], s[10][i], s[11][i]); w.w = pk4_fp8w(s[12][i], s[13][i], s[14][i], s[15][i]);
;         GAS v4u* p = (GAS v4u*)(base + (size_t)i * (size_t)d.ldk + lo);
;         if (NT) __builtin_nontemporal_store(w, p); else *p = w; }
; }
	v_pk_mul_f32 v[0:1], v[0:1], s[30:31] op_sel_hi:[1,0]
	v_pk_mul_f32 v[2:3], v[2:3], s[30:31] op_sel_hi:[1,0]
	v_pk_mul_f32 v[4:5], v[4:5], s[30:31] op_sel_hi:[1,0]
	v_pk_mul_f32 v[6:7], v[6:7], s[30:31] op_sel_hi:[1,0]
	v_pk_mul_f32 v[8:9], v[8:9], s[30:31] op_sel_hi:[1,0]
	v_pk_mul_f32 v[10:11], v[10:11], s[30:31] op_sel_hi:[1,0]
	v_pk_mul_f32 v[12:13], v[12:13], s[30:31] op_sel_hi:[1,0]
	v_pk_mul_f32 v[14:15], v[14:15], s[30:31] op_sel_hi:[1,0]
	v_pk_mul_f32 v[16:17], v[16:17], s[30:31] op_sel_hi:[1,0]
	v_pk_mul_f32 v[18:19], v[18:19], s[30:31] op_sel_hi:[1,0]
	v_pk_mul_f32 v[20:21], v[20:21], s[30:31] op_sel_hi:[1,0]
	v_pk_mul_f32 v[22:23], v[22:23], s[30:31] op_sel_hi:[1,0]
	v_pk_mul_f32 v[24:25], v[24:25], s[30:31] op_sel_hi:[1,0]
	v_pk_mul_f32 v[26:27], v[26:27], s[30:31] op_sel_hi:[1,0]
	v_pk_mul_f32 v[28:29], v[28:29], s[30:31] op_sel_hi:[1,0]
	v_pk_mul_f32 v[30:31], v[30:31], s[30:31] op_sel_hi:[1,0]
	v_pk_mul_f32 v[32:33], v[32:33], s[30:31] op_sel_hi:[1,0]
	v_pk_mul_f32 v[34:35], v[34:35], s[30:31] op_sel_hi:[1,0]
	v_pk_mul_f32 v[36:37], v[36:37], s[30:31] op_sel_hi:[1,0]
	v_pk_mul_f32 v[38:39], v[38:39], s[30:31] op_sel_hi:[1,0]
	v_pk_mul_f32 v[40:41], v[40:41], s[30:31] op_sel_hi:[1,0]
	v_pk_mul_f32 v[42:43], v[42:43], s[30:31] op_sel_hi:[1,0]
	v_pk_mul_f32 v[44:45], v[44:45], s[30:31] op_sel_hi:[1,0]
	v_pk_mul_f32 v[46:47], v[46:47], s[30:31] op_sel_hi:[1,0]
	v_pk_mul_f32 v[48:49], v[48:49], s[30:31] op_sel_hi:[1,0]
	v_pk_mul_f32 v[50:51], v[50:51], s[30:31] op_sel_hi:[1,0]
	v_pk_mul_f32 v[52:53], v[52:53], s[30:31] op_sel_hi:[1,0]
	v_pk_mul_f32 v[54:55], v[54:55], s[30:31] op_sel_hi:[1,0]
	v_pk_mul_f32 v[56:57], v[56:57], s[30:31] op_sel_hi:[1,0]
	v_pk_mul_f32 v[58:59], v[58:59], s[30:31] op_sel_hi:[1,0]
	v_pk_mul_f32 v[60:61], v[60:61], s[30:31] op_sel_hi:[1,0]
	v_pk_mul_f32 v[62:63], v[62:63], s[30:31] op_sel_hi:[1,0]
	v_med3_f32 v0, v0, s24, v237
	v_med3_f32 v1, v1, s24, v237
	v_med3_f32 v2, v2, s24, v237
	v_med3_f32 v3, v3, s24, v237
	v_med3_f32 v4, v4, s24, v237
	v_med3_f32 v5, v5, s24, v237
	v_med3_f32 v6, v6, s24, v237
	v_med3_f32 v7, v7, s24, v237
	v_med3_f32 v8, v8, s24, v237
	v_med3_f32 v9, v9, s24, v237
	v_med3_f32 v10, v10, s24, v237
	v_med3_f32 v11, v11, s24, v237
	v_med3_f32 v12, v12, s24, v237
	v_med3_f32 v13, v13, s24, v237
	v_med3_f32 v14, v14, s24, v237
	v_med3_f32 v15, v15, s24, v237
	v_med3_f32 v16, v16, s24, v237
	v_med3_f32 v17, v17, s24, v237
	v_med3_f32 v18, v18, s24, v237
	v_med3_f32 v19, v19, s24, v237
	v_med3_f32 v20, v20, s24, v237
	v_med3_f32 v21, v21, s24, v237
	v_med3_f32 v22, v22, s24, v237
	v_med3_f32 v23, v23, s24, v237
	v_med3_f32 v24, v24, s24, v237
	v_med3_f32 v25, v25, s24, v237
	v_med3_f32 v26, v26, s24, v237
	v_med3_f32 v27, v27, s24, v237
	v_med3_f32 v28, v28, s24, v237
	v_med3_f32 v29, v29, s24, v237
	v_med3_f32 v30, v30, s24, v237
	v_med3_f32 v31, v31, s24, v237
	v_med3_f32 v32, v32, s24, v237
	v_med3_f32 v33, v33, s24, v237
	v_med3_f32 v34, v34, s24, v237
	v_med3_f32 v35, v35, s24, v237
	v_med3_f32 v36, v36, s24, v237
	v_med3_f32 v37, v37, s24, v237
	v_med3_f32 v38, v38, s24, v237
	v_med3_f32 v39, v39, s24, v237
	v_med3_f32 v40, v40, s24, v237
	v_med3_f32 v41, v41, s24, v237
	v_med3_f32 v42, v42, s24, v237
	v_med3_f32 v43, v43, s24, v237
	v_med3_f32 v44, v44, s24, v237
	v_med3_f32 v45, v45, s24, v237
	v_med3_f32 v46, v46, s24, v237
	v_med3_f32 v47, v47, s24, v237
	v_med3_f32 v48, v48, s24, v237
	v_med3_f32 v49, v49, s24, v237
	v_med3_f32 v50, v50, s24, v237
	v_med3_f32 v51, v51, s24, v237
	v_med3_f32 v52, v52, s24, v237
	v_med3_f32 v53, v53, s24, v237
	v_med3_f32 v54, v54, s24, v237
	v_med3_f32 v55, v55, s24, v237
	v_med3_f32 v56, v56, s24, v237
	v_med3_f32 v57, v57, s24, v237
	v_med3_f32 v58, v58, s24, v237
	v_med3_f32 v59, v59, s24, v237
	v_med3_f32 v60, v60, s24, v237
	v_med3_f32 v61, v61, s24, v237
	v_med3_f32 v62, v62, s24, v237
	v_med3_f32 v63, v63, s24, v237
	v_cvt_pk_fp8_f32 v0, v0, v4
	v_cvt_pk_fp8_f32 v0, v8, v12 op_sel:[0,0,1]
	v_cvt_pk_fp8_f32 v4, v1, v5
	v_cvt_pk_fp8_f32 v4, v9, v13 op_sel:[0,0,1]
	v_cvt_pk_fp8_f32 v8, v2, v6
	v_cvt_pk_fp8_f32 v8, v10, v14 op_sel:[0,0,1]
	v_cvt_pk_fp8_f32 v12, v3, v7
	v_cvt_pk_fp8_f32 v12, v11, v15 op_sel:[0,0,1]
	v_cvt_pk_fp8_f32 v1, v16, v20
	v_cvt_pk_fp8_f32 v1, v24, v28 op_sel:[0,0,1]
	v_cvt_pk_fp8_f32 v5, v17, v21
	v_cvt_pk_fp8_f32 v5, v25, v29 op_sel:[0,0,1]
	v_cvt_pk_fp8_f32 v9, v18, v22
	v_cvt_pk_fp8_f32 v9, v26, v30 op_sel:[0,0,1]
	v_cvt_pk_fp8_f32 v13, v19, v23
	v_cvt_pk_fp8_f32 v13, v27, v31 op_sel:[0,0,1]
	v_cvt_pk_fp8_f32 v2, v32, v36
	v_cvt_pk_fp8_f32 v2, v40, v44 op_sel:[0,0,1]
	v_cvt_pk_fp8_f32 v6, v33, v37
	v_cvt_pk_fp8_f32 v6, v41, v45 op_sel:[0,0,1]
	v_cvt_pk_fp8_f32 v10, v34, v38
	v_cvt_pk_fp8_f32 v10, v42, v46 op_sel:[0,0,1]
	v_cvt_pk_fp8_f32 v14, v35, v39
	v_cvt_pk_fp8_f32 v14, v43, v47 op_sel:[0,0,1]
	v_cvt_pk_fp8_f32 v3, v48, v52
	v_cvt_pk_fp8_f32 v3, v56, v60 op_sel:[0,0,1]
	v_cvt_pk_fp8_f32 v7, v49, v53
	v_cvt_pk_fp8_f32 v7, v57, v61 op_sel:[0,0,1]
	v_cvt_pk_fp8_f32 v11, v50, v54
	v_cvt_pk_fp8_f32 v11, v58, v62 op_sel:[0,0,1]
	v_cvt_pk_fp8_f32 v15, v51, v55
	v_cvt_pk_fp8_f32 v15, v59, v63 op_sel:[0,0,1]
	global_store_dwordx4 v250, v[0:3], s[42:43] nt
	global_store_dwordx4 v250, v[4:7], s[42:43] offset:2048 nt
	global_store_dwordx4 v251, v[8:11], s[42:43] nt
	global_store_dwordx4 v251, v[12:15], s[42:43] offset:2048 nt
	s_add_u32 s42, s42, 0x800000
	s_addc_u32 s43, s43, 0
	global_load_dwordx4 v[0:3], v246, s[4:5] nt
	global_load_dwordx4 v[4:7], v247, s[4:5] nt
	global_load_dwordx4 v[8:11], v248, s[4:5] nt
	global_load_dwordx4 v[12:15], v249, s[4:5] nt
	global_load_dwordx4 v[16:19], v246, s[6:7] nt
	global_load_dwordx4 v[20:23], v247, s[6:7] nt
	global_load_dwordx4 v[24:27], v248, s[6:7] nt
	global_load_dwordx4 v[28:31], v249, s[6:7] nt
	global_load_dwordx4 v[32:35], v246, s[8:9] nt
	global_load_dwordx4 v[36:39], v247, s[8:9] nt
	global_load_dwordx4 v[40:43], v248, s[8:9] nt
	global_load_dwordx4 v[44:47], v249, s[8:9] nt
	global_load_dwordx4 v[48:51], v246, s[38:39] nt
	global_load_dwordx4 v[52:55], v247, s[38:39] nt
	global_load_dwordx4 v[56:59], v248, s[38:39] nt
	global_load_dwordx4 v[60:63], v249, s[38:39] nt
	s_add_u32 s4, s4, 0x2000000
	s_addc_u32 s5, s5, 0
	s_add_u32 s6, s6, 0x2000000
	s_addc_u32 s7, s7, 0
	s_add_u32 s8, s8, 0x2000000
	s_addc_u32 s9, s9, 0
	s_add_u32 s38, s38, 0x2000000
	s_addc_u32 s39, s39, 0
	s_waitcnt vmcnt(36)
; #define GAS __attribute__((address_space(1)))
; template <bool GAIN, bool NT = false> __device__ __forceinline__ void titem8_load(const TItem& d, int lane, f32x4 (&r)[16], f32x4 (&g)[4]) {
;     const int q = lane & 7, kg = lane >> 3; const unsigned lo = (unsigned)((16 * kg) * d.N + 4 * q) * 4u;
;     const GAS char* base = (const GAS char*)d.src;
; #pragma unroll
;     for (int j = 0; j < 16; ++j) { const GAS f32x4* p = (const GAS f32x4*)(base + (size_t)j * (size_t)d.N * 4 + lo); r[j] = NT ? __builtin_nontemporal_load(p) : *p; }
; template <bool GAIN, bool NT = false> __device__ __forceinline__ void titem8_store(const TItem& d, int lane, const f32x4 (&r)[16], const f32x4 (&g)[4]) {
;     const int q = lane & 7, kg = lane >> 3; const unsigned lo = (unsigned)((4 * q) * d.ldk + 16 * kg);
;     GAS char* base = (GAS char*)d.dst;
;     f32x4 s[16];
; #pragma unroll
;     for (int j = 0; j < 16; ++j) s[j] = r[j] * ((GAIN ? g[j >> 2][j & 3] : 1.0f) * W8_SCALE);
; #pragma unroll
;     for (int i = 0; i < 4; ++i) { v4u w;
;         w.x = pk4_fp8w(s[0][i], s[1][i], s[2][i], s[3][i]); w.y = pk4_fp8w(s[4][i], s[5][i], s[6][i], s[7][i]);
;         w.z = pk4_fp8w(s[8][i], s[9][i], s[10][i], s[11][i]); w.w = pk4_fp8w(s[12][i], s[13][i], s[14][i], s[15][i]);
;         GAS v4u* p = (GAS v4u*)(base + (size_t)i * (size_t)d.ldk + lo);
;         if (NT) __builtin_nontemporal_store(w, p); else *p = w; }
; }
	v_pk_mul_f32 v[66:67], v[66:67], s[30:31] op_sel_hi:[1,0]
	v_pk_mul_f32 v[68:69], v[68:69], s[30:31] op_sel_hi:[1,0]
	v_pk_mul_f32 v[70:71], v[70:71], s[30:31] op_sel_hi:[1,0]
	v_pk_mul_f32 v[72:73], v[72:73], s[30:31] op_sel_hi:[1,0]
	v_pk_mul_f32 v[74:75], v[74:75], s[30:31] op_sel_hi:[1,0]
	v_pk_mul_f32 v[76:77], v[76:77], s[30:31] op_sel_hi:[1,0]
	v_pk_mul_f32 v[78:79], v[78:79], s[30:31] op_sel_hi:[1,0]
	v_pk_mul_f32 v[80:81], v[80:81], s[30:31] op_sel_hi:[1,0]
	v_pk_mul_f32 v[82:83], v[82:83], s[30:31] op_sel_hi:[1,0]
	v_pk_mul_f32 v[84:85], v[84:85], s[30:31] op_sel_hi:[1,0]
	v_pk_mul_f32 v[86:87], v[86:87], s[30:31] op_sel_hi:[1,0]
	v_pk_mul_f32 v[88:89], v[88:89], s[30:31] op_sel_hi:[1,0]
	v_pk_mul_f32 v[90:91], v[90:91], s[30:31] op_sel_hi:[1,0]
	v_pk_mul_f32 v[92:93], v[92:93], s[30:31] op_sel_hi:[1,0]
	v_pk_mul_f32 v[94:95], v[94:95], s[30:31] op_sel_hi:[1,0]
	v_pk_mul_f32 v[96:97], v[96:97], s[30:31] op_sel_hi:[1,0]
	v_pk_mul_f32 v[98:99], v[98:99], s[30:31] op_sel_hi:[1,0]
	v_pk_mul_f32 v[100:101], v[100:101], s[30:31] op_sel_hi:[1,0]
	v_pk_mul_f32 v[102:103], v[102:103], s[30:31] op_sel_hi:[1,0]
	v_pk_mul_f32 v[104:105], v[104:105], s[30:31] op_sel_hi:[1,0]
	v_pk_mul_f32 v[106:107], v[106:107], s[30:31] op_sel_hi:[1,0]
	v_pk_mul_f32 v[108:109], v[108:109], s[30:31] op_sel_hi:[1,0]
	v_pk_mul_f32 v[110:111], v[110:111], s[30:31] op_sel_hi:[1,0]
	v_pk_mul_f32 v[112:113], v[112:113], s[30:31] op_sel_hi:[1,0]
	v_pk_mul_f32 v[114:115], v[114:115], s[30:31] op_sel_hi:[1,0]
	v_pk_mul_f32 v[116:117], v[116:117], s[30:31] op_sel_hi:[1,0]
	v_pk_mul_f32 v[118:119], v[118:119], s[30:31] op_sel_hi:[1,0]
	v_pk_mul_f32 v[120:121], v[120:121], s[30:31] op_sel_hi:[1,0]
	v_pk_mul_f32 v[122:123], v[122:123], s[30:31] op_sel_hi:[1,0]
	v_pk_mul_f32 v[124:125], v[124:125], s[30:31] op_sel_hi:[1,0]
	v_pk_mul_f32 v[126:127], v[126:127], s[30:31] op_sel_hi:[1,0]
	v_pk_mul_f32 v[128:129], v[128:129], s[30:31] op_sel_hi:[1,0]
	v_med3_f32 v66, v66, s24, v237
	v_med3_f32 v67, v67, s24, v237
	v_med3_f32 v68, v68, s24, v237
	v_med3_f32 v69, v69, s24, v237
	v_med3_f32 v70, v70, s24, v237
	v_med3_f32 v71, v71, s24, v237
	v_med3_f32 v72, v72, s24, v237
	v_med3_f32 v73, v73, s24, v237
	v_med3_f32 v74, v74, s24, v237
	v_med3_f32 v75, v75, s24, v237
	v_med3_f32 v76, v76, s24, v237
	v_med3_f32 v77, v77, s24, v237
	v_med3_f32 v78, v78, s24, v237
	v_med3_f32 v79, v79, s24, v237
	v_med3_f32 v80, v80, s24, v237
	v_med3_f32 v81, v81, s24, v237
	v_med3_f32 v82, v82, s24, v237
	v_med3_f32 v83, v83, s24, v237
	v_med3_f32 v84, v84, s24, v237
	v_med3_f32 v85, v85, s24, v237
	v_med3_f32 v86, v86, s24, v237
	v_med3_f32 v87, v87, s24, v237
	v_med3_f32 v88, v88, s24, v237
	v_med3_f32 v89, v89, s24, v237
	v_med3_f32 v90, v90, s24, v237
	v_med3_f32 v91, v91, s24, v237
	v_med3_f32 v92, v92, s24, v237
	v_med3_f32 v93, v93, s24, v237
	v_med3_f32 v94, v94, s24, v237
	v_med3_f32 v95, v95, s24, v237
	v_med3_f32 v96, v96, s24, v237
	v_med3_f32 v97, v97, s24, v237
	v_med3_f32 v98, v98, s24, v237
	v_med3_f32 v99, v99, s24, v237
	v_med3_f32 v100, v100, s24, v237
	v_med3_f32 v101, v101, s24, v237
	v_med3_f32 v102, v102, s24, v237
	v_med3_f32 v103, v103, s24, v237
	v_med3_f32 v104, v104, s24, v237
	v_med3_f32 v105, v105, s24, v237
	v_med3_f32 v106, v106, s24, v237
	v_med3_f32 v107, v107, s24, v237
	v_med3_f32 v108, v108, s24, v237
	v_med3_f32 v109, v109, s24, v237
	v_med3_f32 v110, v110, s24, v237
	v_med3_f32 v111, v111, s24, v237
	v_med3_f32 v112, v112, s24, v237
	v_med3_f32 v113, v113, s24, v237
	v_med3_f32 v114, v114, s24, v237
	v_med3_f32 v115, v115, s24, v237
	v_med3_f32 v116, v116, s24, v237
	v_med3_f32 v117, v117, s24, v237
	v_med3_f32 v118, v118, s24, v237
	v_med3_f32 v119, v119, s24, v237
	v_med3_f32 v120, v120, s24, v237
	v_med3_f32 v121, v121, s24, v237
	v_med3_f32 v122, v122, s24, v237
	v_med3_f32 v123, v123, s24, v237
	v_med3_f32 v124, v124, s24, v237
	v_med3_f32 v125, v125, s24, v237
	v_med3_f32 v126, v126, s24, v237
	v_med3_f32 v127, v127, s24, v237
	v_med3_f32 v128, v128, s24, v237
	v_med3_f32 v129, v129, s24, v237
	v_cvt_pk_fp8_f32 v66, v66, v70
	v_cvt_pk_fp8_f32 v66, v74, v78 op_sel:[0,0,1]
	v_cvt_pk_fp8_f32 v70, v67, v71
	v_cvt_pk_fp8_f32 v70, v75, v79 op_sel:[0,0,1]
	v_cvt_pk_fp8_f32 v74, v68, v72
	v_cvt_pk_fp8_f32 v74, v76, v80 op_sel:[0,0,1]
	v_cvt_pk_fp8_f32 v78, v69, v73
	v_cvt_pk_fp8_f32 v78, v77, v81 op_sel:[0,0,1]
	v_cvt_pk_fp8_f32 v67, v82, v86
	v_cvt_pk_fp8_f32 v67, v90, v94 op_sel:[0,0,1]
	v_cvt_pk_fp8_f32 v71, v83, v87
	v_cvt_pk_fp8_f32 v71, v91, v95 op_sel:[0,0,1]
	v_cvt_pk_fp8_f32 v75, v84, v88
	v_cvt_pk_fp8_f32 v75, v92, v96 op_sel:[0,0,1]
	v_cvt_pk_fp8_f32 v79, v85, v89
	v_cvt_pk_fp8_f32 v79, v93, v97 op_sel:[0,0,1]
	v_cvt_pk_fp8_f32 v68, v98, v102
	v_cvt_pk_fp8_f32 v68, v106, v110 op_sel:[0,0,1]
	v_cvt_pk_fp8_f32 v72, v99, v103
	v_cvt_pk_fp8_f32 v72, v107, v111 op_sel:[0,0,1]
	v_cvt_pk_fp8_f32 v76, v100, v104
	v_cvt_pk_fp8_f32 v76, v108, v112 op_sel:[0,0,1]
	v_cvt_pk_fp8_f32 v80, v101, v105
	v_cvt_pk_fp8_f32 v80, v109, v113 op_sel:[0,0,1]
	v_cvt_pk_fp8_f32 v69, v114, v118
	v_cvt_pk_fp8_f32 v69, v122, v126 op_sel:[0,0,1]
	v_cvt_pk_fp8_f32 v73, v115, v119
	v_cvt_pk_fp8_f32 v73, v123, v127 op_sel:[0,0,1]
	v_cvt_pk_fp8_f32 v77, v116, v120
	v_cvt_pk_fp8_f32 v77, v124, v128 op_sel:[0,0,1]
	v_cvt_pk_fp8_f32 v81, v117, v121
	v_cvt_pk_fp8_f32 v81, v125, v129 op_sel:[0,0,1]
	global_store_dwordx4 v250, v[66:69], s[42:43] nt
	global_store_dwordx4 v250, v[70:73], s[42:43] offset:2048 nt
	global_store_dwordx4 v251, v[74:77], s[42:43] nt
	global_store_dwordx4 v251, v[78:81], s[42:43] offset:2048 nt
	s_add_u32 s42, s42, 0x800000
	s_addc_u32 s43, s43, 0
	global_load_dwordx4 v[66:69], v246, s[4:5] nt
	global_load_dwordx4 v[70:73], v247, s[4:5] nt
	global_load_dwordx4 v[74:77], v248, s[4:5] nt
	global_load_dwordx4 v[78:81], v249, s[4:5] nt
	global_load_dwordx4 v[82:85], v246, s[6:7] nt
	global_load_dwordx4 v[86:89], v247, s[6:7] nt
	global_load_dwordx4 v[90:93], v248, s[6:7] nt
	global_load_dwordx4 v[94:97], v249, s[6:7] nt
	global_load_dwordx4 v[98:101], v246, s[8:9] nt
	global_load_dwordx4 v[102:105], v247, s[8:9] nt
	global_load_dwordx4 v[106:109], v248, s[8:9] nt
	global_load_dwordx4 v[110:113], v249, s[8:9] nt
	global_load_dwordx4 v[114:117], v246, s[38:39] nt
	global_load_dwordx4 v[118:121], v247, s[38:39] nt
	global_load_dwordx4 v[122:125], v248, s[38:39] nt
	global_load_dwordx4 v[126:129], v249, s[38:39] nt
	s_add_u32 s4, s4, 0x2000000
	s_addc_u32 s5, s5, 0
	s_add_u32 s6, s6, 0x2000000
	s_addc_u32 s7, s7, 0
	s_add_u32 s8, s8, 0x2000000
	s_addc_u32 s9, s9, 0
	s_add_u32 s38, s38, 0x2000000
	s_addc_u32 s39, s39, 0
	s_waitcnt vmcnt(40)
; #define GAS __attribute__((address_space(1)))
; template <bool GAIN, bool NT = false> __device__ __forceinline__ void titem8_load(const TItem& d, int lane, f32x4 (&r)[16], f32x4 (&g)[4]) {
;     const int q = lane & 7, kg = lane >> 3; const unsigned lo = (unsigned)((16 * kg) * d.N + 4 * q) * 4u;
;     const GAS char* base = (const GAS char*)d.src;
; #pragma unroll
;     for (int j = 0; j < 16; ++j) { const GAS f32x4* p = (const GAS f32x4*)(base + (size_t)j * (size_t)d.N * 4 + lo); r[j] = NT ? __builtin_nontemporal_load(p) : *p; }
; template <bool GAIN, bool NT = false> __device__ __forceinline__ void titem8_store(const TItem& d, int lane, const f32x4 (&r)[16], const f32x4 (&g)[4]) {
;     const int q = lane & 7, kg = lane >> 3; const unsigned lo = (unsigned)((4 * q) * d.ldk + 16 * kg);
;     GAS char* base = (GAS char*)d.dst;
;     f32x4 s[16];
; #pragma unroll
;     for (int j = 0; j < 16; ++j) s[j] = r[j] * ((GAIN ? g[j >> 2][j & 3] : 1.0f) * W8_SCALE);
; #pragma unroll
;     for (int i = 0; i < 4; ++i) { v4u w;
;         w.x = pk4_fp8w(s[0][i], s[1][i], s[2][i], s[3][i]); w.y = pk4_fp8w(s[4][i], s[5][i], s[6][i], s[7][i]);
;         w.z = pk4_fp8w(s[8][i], s[9][i], s[10][i], s[11][i]); w.w = pk4_fp8w(s[12][i], s[13][i], s[14][i], s[15][i]);
;         GAS v4u* p = (GAS v4u*)(base + (size_t)i * (size_t)d.ldk + lo);
;         if (NT) __builtin_nontemporal_store(w, p); else *p = w; }
; }
	v_pk_mul_f32 v[130:131], v[130:131], s[30:31] op_sel_hi:[1,0]
	v_pk_mul_f32 v[132:133], v[132:133], s[30:31] op_sel_hi:[1,0]
	v_pk_mul_f32 v[134:135], v[134:135], s[30:31] op_sel_hi:[1,0]
	v_pk_mul_f32 v[136:137], v[136:137], s[30:31] op_sel_hi:[1,0]
	v_pk_mul_f32 v[138:139], v[138:139], s[30:31] op_sel_hi:[1,0]
	v_pk_mul_f32 v[140:141], v[140:141], s[30:31] op_sel_hi:[1,0]
	v_pk_mul_f32 v[142:143], v[142:143], s[30:31] op_sel_hi:[1,0]
	v_pk_mul_f32 v[144:145], v[144:145], s[30:31] op_sel_hi:[1,0]
	v_pk_mul_f32 v[146:147], v[146:147], s[30:31] op_sel_hi:[1,0]
	v_pk_mul_f32 v[148:149], v[148:149], s[30:31] op_sel_hi:[1,0]
	v_pk_mul_f32 v[150:151], v[150:151], s[30:31] op_sel_hi:[1,0]
	v_pk_mul_f32 v[152:153], v[152:153], s[30:31] op_sel_hi:[1,0]
	v_pk_mul_f32 v[154:155], v[154:155], s[30:31] op_sel_hi:[1,0]
	v_pk_mul_f32 v[156:157], v[156:157], s[30:31] op_sel_hi:[1,0]
	v_pk_mul_f32 v[158:159], v[158:159], s[30:31] op_sel_hi:[1,0]
	v_pk_mul_f32 v[160:161], v[160:161], s[30:31] op_sel_hi:[1,0]
	v_pk_mul_f32 v[162:163], v[162:163], s[30:31] op_sel_hi:[1,0]
	v_pk_mul_f32 v[164:165], v[164:165], s[30:31] op_sel_hi:[1,0]
	v_pk_mul_f32 v[166:167], v[166:167], s[30:31] op_sel_hi:[1,0]
	v_pk_mul_f32 v[168:169], v[168:169], s[30:31] op_sel_hi:[1,0]
	v_pk_mul_f32 v[170:171], v[170:171], s[30:31] op_sel_hi:[1,0]
	v_pk_mul_f32 v[172:173], v[172:173], s[30:31] op_sel_hi:[1,0]
	v_pk_mul_f32 v[174:175], v[174:175], s[30:31] op_sel_hi:[1,0]
	v_pk_mul_f32 v[176:177], v[176:177], s[30:31] op_sel_hi:[1,0]
	v_pk_mul_f32 v[178:179], v[178:179], s[30:31] op_sel_hi:[1,0]
	v_pk_mul_f32 v[180:181], v[180:181], s[30:31] op_sel_hi:[1,0]
	v_pk_mul_f32 v[182:183], v[182:183], s[30:31] op_sel_hi:[1,0]
	v_pk_mul_f32 v[184:185], v[184:185], s[30:31] op_sel_hi:[1,0]
	v_pk_mul_f32 v[186:187], v[186:187], s[30:31] op_sel_hi:[1,0]
	v_pk_mul_f32 v[188:189], v[188:189], s[30:31] op_sel_hi:[1,0]
	v_pk_mul_f32 v[190:191], v[190:191], s[30:31] op_sel_hi:[1,0]
	v_pk_mul_f32 v[192:193], v[192:193], s[30:31] op_sel_hi:[1,0]
	v_med3_f32 v130, v130, s24, v237
	v_med3_f32 v131, v131, s24, v237
	v_med3_f32 v132, v132, s24, v237
	v_med3_f32 v133, v133, s24, v237
	v_med3_f32 v134, v134, s24, v237
	v_med3_f32 v135, v135, s24, v237
	v_med3_f32 v136, v136, s24, v237
	v_med3_f32 v137, v137, s24, v237
	v_med3_f32 v138, v138, s24, v237
	v_med3_f32 v139, v139, s24, v237
	v_med3_f32 v140, v140, s24, v237
	v_med3_f32 v141, v141, s24, v237
	v_med3_f32 v142, v142, s24, v237
	v_med3_f32 v143, v143, s24, v237
	v_med3_f32 v144, v144, s24, v237
	v_med3_f32 v145, v145, s24, v237
	v_med3_f32 v146, v146, s24, v237
	v_med3_f32 v147, v147, s24, v237
	v_med3_f32 v148, v148, s24, v237
	v_med3_f32 v149, v149, s24, v237
	v_med3_f32 v150, v150, s24, v237
	v_med3_f32 v151, v151, s24, v237
	v_med3_f32 v152, v152, s24, v237
	v_med3_f32 v153, v153, s24, v237
	v_med3_f32 v154, v154, s24, v237
	v_med3_f32 v155, v155, s24, v237
	v_med3_f32 v156, v156, s24, v237
	v_med3_f32 v157, v157, s24, v237
	v_med3_f32 v158, v158, s24, v237
	v_med3_f32 v159, v159, s24, v237
	v_med3_f32 v160, v160, s24, v237
	v_med3_f32 v161, v161, s24, v237
	v_med3_f32 v162, v162, s24, v237
	v_med3_f32 v163, v163, s24, v237
	v_med3_f32 v164, v164, s24, v237
	v_med3_f32 v165, v165, s24, v237
	v_med3_f32 v166, v166, s24, v237
	v_med3_f32 v167, v167, s24, v237
	v_med3_f32 v168, v168, s24, v237
	v_med3_f32 v169, v169, s24, v237
	v_med3_f32 v170, v170, s24, v237
	v_med3_f32 v171, v171, s24, v237
	v_med3_f32 v172, v172, s24, v237
	v_med3_f32 v173, v173, s24, v237
	v_med3_f32 v174, v174, s24, v237
	v_med3_f32 v175, v175, s24, v237
	v_med3_f32 v176, v176, s24, v237
	v_med3_f32 v177, v177, s24, v237
	v_med3_f32 v178, v178, s24, v237
	v_med3_f32 v179, v179, s24, v237
	v_med3_f32 v180, v180, s24, v237
	v_med3_f32 v181, v181, s24, v237
	v_med3_f32 v182, v182, s24, v237
	v_med3_f32 v183, v183, s24, v237
	v_med3_f32 v184, v184, s24, v237
	v_med3_f32 v185, v185, s24, v237
	v_med3_f32 v186, v186, s24, v237
	v_med3_f32 v187, v187, s24, v237
	v_med3_f32 v188, v188, s24, v237
	v_med3_f32 v189, v189, s24, v237
	v_med3_f32 v190, v190, s24, v237
	v_med3_f32 v191, v191, s24, v237
	v_med3_f32 v192, v192, s24, v237
	v_med3_f32 v193, v193, s24, v237
	v_cvt_pk_fp8_f32 v130, v130, v134
	v_cvt_pk_fp8_f32 v130, v138, v142 op_sel:[0,0,1]
	v_cvt_pk_fp8_f32 v134, v131, v135
	v_cvt_pk_fp8_f32 v134, v139, v143 op_sel:[0,0,1]
	v_cvt_pk_fp8_f32 v138, v132, v136
	v_cvt_pk_fp8_f32 v138, v140, v144 op_sel:[0,0,1]
	v_cvt_pk_fp8_f32 v142, v133, v137
	v_cvt_pk_fp8_f32 v142, v141, v145 op_sel:[0,0,1]
	v_cvt_pk_fp8_f32 v131, v146, v150
	v_cvt_pk_fp8_f32 v131, v154, v158 op_sel:[0,0,1]
	v_cvt_pk_fp8_f32 v135, v147, v151
	v_cvt_pk_fp8_f32 v135, v155, v159 op_sel:[0,0,1]
	v_cvt_pk_fp8_f32 v139, v148, v152
	v_cvt_pk_fp8_f32 v139, v156, v160 op_sel:[0,0,1]
	v_cvt_pk_fp8_f32 v143, v149, v153
	v_cvt_pk_fp8_f32 v143, v157, v161 op_sel:[0,0,1]
	v_cvt_pk_fp8_f32 v132, v162, v166
	v_cvt_pk_fp8_f32 v132, v170, v174 op_sel:[0,0,1]
	v_cvt_pk_fp8_f32 v136, v163, v167
	v_cvt_pk_fp8_f32 v136, v171, v175 op_sel:[0,0,1]
	v_cvt_pk_fp8_f32 v140, v164, v168
	v_cvt_pk_fp8_f32 v140, v172, v176 op_sel:[0,0,1]
	v_cvt_pk_fp8_f32 v144, v165, v169
	v_cvt_pk_fp8_f32 v144, v173, v177 op_sel:[0,0,1]
	v_cvt_pk_fp8_f32 v133, v178, v182
	v_cvt_pk_fp8_f32 v133, v186, v190 op_sel:[0,0,1]
	v_cvt_pk_fp8_f32 v137, v179, v183
	v_cvt_pk_fp8_f32 v137, v187, v191 op_sel:[0,0,1]
	v_cvt_pk_fp8_f32 v141, v180, v184
	v_cvt_pk_fp8_f32 v141, v188, v192 op_sel:[0,0,1]
	v_cvt_pk_fp8_f32 v145, v181, v185
	v_cvt_pk_fp8_f32 v145, v189, v193 op_sel:[0,0,1]
	global_store_dwordx4 v250, v[130:133], s[42:43] nt
	global_store_dwordx4 v250, v[134:137], s[42:43] offset:2048 nt
	global_store_dwordx4 v251, v[138:141], s[42:43] nt
	global_store_dwordx4 v251, v[142:145], s[42:43] offset:2048 nt
	s_add_u32 s42, s42, 0x800000
	s_addc_u32 s43, s43, 0
	global_load_dwordx4 v[130:133], v246, s[4:5] nt
	global_load_dwordx4 v[134:137], v247, s[4:5] nt
	global_load_dwordx4 v[138:141], v248, s[4:5] nt
	global_load_dwordx4 v[142:145], v249, s[4:5] nt
	global_load_dwordx4 v[146:149], v246, s[6:7] nt
	global_load_dwordx4 v[150:153], v247, s[6:7] nt
	global_load_dwordx4 v[154:157], v248, s[6:7] nt
	global_load_dwordx4 v[158:161], v249, s[6:7] nt
	global_load_dwordx4 v[162:165], v246, s[8:9] nt
	global_load_dwordx4 v[166:169], v247, s[8:9] nt
	global_load_dwordx4 v[170:173], v248, s[8:9] nt
	global_load_dwordx4 v[174:177], v249, s[8:9] nt
	global_load_dwordx4 v[178:181], v246, s[38:39] nt
	global_load_dwordx4 v[182:185], v247, s[38:39] nt
	global_load_dwordx4 v[186:189], v248, s[38:39] nt
	global_load_dwordx4 v[190:193], v249, s[38:39] nt
	s_add_u32 s4, s4, 0x2000000
	s_addc_u32 s5, s5, 0
	s_add_u32 s6, s6, 0x2000000
	s_addc_u32 s7, s7, 0
	s_add_u32 s8, s8, 0x2000000
	s_addc_u32 s9, s9, 0
	s_add_u32 s38, s38, 0x2000000
	s_addc_u32 s39, s39, 0
	s_waitcnt vmcnt(40)
; #define GAS __attribute__((address_space(1)))
; template <bool GAIN, bool NT = false> __device__ __forceinline__ void titem8_load(const TItem& d, int lane, f32x4 (&r)[16], f32x4 (&g)[4]) {
;     const int q = lane & 7, kg = lane >> 3; const unsigned lo = (unsigned)((16 * kg) * d.N + 4 * q) * 4u;
;     const GAS char* base = (const GAS char*)d.src;
; #pragma unroll
;     for (int j = 0; j < 16; ++j) { const GAS f32x4* p = (const GAS f32x4*)(base + (size_t)j * (size_t)d.N * 4 + lo); r[j] = NT ? __builtin_nontemporal_load(p) : *p; }
; template <bool GAIN, bool NT = false> __device__ __forceinline__ void titem8_store(const TItem& d, int lane, const f32x4 (&r)[16], const f32x4 (&g)[4]) {
;     const int q = lane & 7, kg = lane >> 3; const unsigned lo = (unsigned)((4 * q) * d.ldk + 16 * kg);
;     GAS char* base = (GAS char*)d.dst;
;     f32x4 s[16];
; #pragma unroll
;     for (int j = 0; j < 16; ++j) s[j] = r[j] * ((GAIN ? g[j >> 2][j & 3] : 1.0f) * W8_SCALE);
; #pragma unroll
;     for (int i = 0; i < 4; ++i) { v4u w;
;         w.x = pk4_fp8w(s[0][i], s[1][i], s[2][i], s[3][i]); w.y = pk4_fp8w(s[4][i], s[5][i], s[6][i], s[7][i]);
;         w.z = pk4_fp8w(s[8][i], s[9][i], s[10][i], s[11][i]); w.w = pk4_fp8w(s[12][i], s[13][i], s[14][i], s[15][i]);
;         GAS v4u* p = (GAS v4u*)(base + (size_t)i * (size_t)d.ldk + lo);
;         if (NT) __builtin_nontemporal_store(w, p); else *p = w; }
; }
	v_pk_mul_f32 v[0:1], v[0:1], s[30:31] op_sel_hi:[1,0]
	v_pk_mul_f32 v[2:3], v[2:3], s[30:31] op_sel_hi:[1,0]
	v_pk_mul_f32 v[4:5], v[4:5], s[30:31] op_sel_hi:[1,0]
	v_pk_mul_f32 v[6:7], v[6:7], s[30:31] op_sel_hi:[1,0]
	v_pk_mul_f32 v[8:9], v[8:9], s[30:31] op_sel_hi:[1,0]
	v_pk_mul_f32 v[10:11], v[10:11], s[30:31] op_sel_hi:[1,0]
	v_pk_mul_f32 v[12:13], v[12:13], s[30:31] op_sel_hi:[1,0]
	v_pk_mul_f32 v[14:15], v[14:15], s[30:31] op_sel_hi:[1,0]
	v_pk_mul_f32 v[16:17], v[16:17], s[30:31] op_sel_hi:[1,0]
	v_pk_mul_f32 v[18:19], v[18:19], s[30:31] op_sel_hi:[1,0]
	v_pk_mul_f32 v[20:21], v[20:21], s[30:31] op_sel_hi:[1,0]
	v_pk_mul_f32 v[22:23], v[22:23], s[30:31] op_sel_hi:[1,0]
	v_pk_mul_f32 v[24:25], v[24:25], s[30:31] op_sel_hi:[1,0]
	v_pk_mul_f32 v[26:27], v[26:27], s[30:31] op_sel_hi:[1,0]
	v_pk_mul_f32 v[28:29], v[28:29], s[30:31] op_sel_hi:[1,0]
	v_pk_mul_f32 v[30:31], v[30:31], s[30:31] op_sel_hi:[1,0]
	v_pk_mul_f32 v[32:33], v[32:33], s[30:31] op_sel_hi:[1,0]
	v_pk_mul_f32 v[34:35], v[34:35], s[30:31] op_sel_hi:[1,0]
	v_pk_mul_f32 v[36:37], v[36:37], s[30:31] op_sel_hi:[1,0]
	v_pk_mul_f32 v[38:39], v[38:39], s[30:31] op_sel_hi:[1,0]
	v_pk_mul_f32 v[40:41], v[40:41], s[30:31] op_sel_hi:[1,0]
	v_pk_mul_f32 v[42:43], v[42:43], s[30:31] op_sel_hi:[1,0]
	v_pk_mul_f32 v[44:45], v[44:45], s[30:31] op_sel_hi:[1,0]
	v_pk_mul_f32 v[46:47], v[46:47], s[30:31] op_sel_hi:[1,0]
	v_pk_mul_f32 v[48:49], v[48:49], s[30:31] op_sel_hi:[1,0]
	v_pk_mul_f32 v[50:51], v[50:51], s[30:31] op_sel_hi:[1,0]
	v_pk_mul_f32 v[52:53], v[52:53], s[30:31] op_sel_hi:[1,0]
	v_pk_mul_f32 v[54:55], v[54:55], s[30:31] op_sel_hi:[1,0]
	v_pk_mul_f32 v[56:57], v[56:57], s[30:31] op_sel_hi:[1,0]
	v_pk_mul_f32 v[58:59], v[58:59], s[30:31] op_sel_hi:[1,0]
	v_pk_mul_f32 v[60:61], v[60:61], s[30:31] op_sel_hi:[1,0]
	v_pk_mul_f32 v[62:63], v[62:63], s[30:31] op_sel_hi:[1,0]
	v_med3_f32 v0, v0, s24, v237
	v_med3_f32 v1, v1, s24, v237
	v_med3_f32 v2, v2, s24, v237
	v_med3_f32 v3, v3, s24, v237
	v_med3_f32 v4, v4, s24, v237
	v_med3_f32 v5, v5, s24, v237
	v_med3_f32 v6, v6, s24, v237
	v_med3_f32 v7, v7, s24, v237
	v_med3_f32 v8, v8, s24, v237
	v_med3_f32 v9, v9, s24, v237
	v_med3_f32 v10, v10, s24, v237
	v_med3_f32 v11, v11, s24, v237
	v_med3_f32 v12, v12, s24, v237
	v_med3_f32 v13, v13, s24, v237
	v_med3_f32 v14, v14, s24, v237
	v_med3_f32 v15, v15, s24, v237
	v_med3_f32 v16, v16, s24, v237
	v_med3_f32 v17, v17, s24, v237
	v_med3_f32 v18, v18, s24, v237
	v_med3_f32 v19, v19, s24, v237
	v_med3_f32 v20, v20, s24, v237
	v_med3_f32 v21, v21, s24, v237
	v_med3_f32 v22, v22, s24, v237
	v_med3_f32 v23, v23, s24, v237
	v_med3_f32 v24, v24, s24, v237
	v_med3_f32 v25, v25, s24, v237
	v_med3_f32 v26, v26, s24, v237
	v_med3_f32 v27, v27, s24, v237
	v_med3_f32 v28, v28, s24, v237
	v_med3_f32 v29, v29, s24, v237
	v_med3_f32 v30, v30, s24, v237
	v_med3_f32 v31, v31, s24, v237
	v_med3_f32 v32, v32, s24, v237
	v_med3_f32 v33, v33, s24, v237
	v_med3_f32 v34, v34, s24, v237
	v_med3_f32 v35, v35, s24, v237
	v_med3_f32 v36, v36, s24, v237
	v_med3_f32 v37, v37, s24, v237
	v_med3_f32 v38, v38, s24, v237
	v_med3_f32 v39, v39, s24, v237
	v_med3_f32 v40, v40, s24, v237
	v_med3_f32 v41, v41, s24, v237
	v_med3_f32 v42, v42, s24, v237
	v_med3_f32 v43, v43, s24, v237
	v_med3_f32 v44, v44, s24, v237
	v_med3_f32 v45, v45, s24, v237
	v_med3_f32 v46, v46, s24, v237
	v_med3_f32 v47, v47, s24, v237
	v_med3_f32 v48, v48, s24, v237
	v_med3_f32 v49, v49, s24, v237
	v_med3_f32 v50, v50, s24, v237
	v_med3_f32 v51, v51, s24, v237
	v_med3_f32 v52, v52, s24, v237
	v_med3_f32 v53, v53, s24, v237
	v_med3_f32 v54, v54, s24, v237
	v_med3_f32 v55, v55, s24, v237
	v_med3_f32 v56, v56, s24, v237
	v_med3_f32 v57, v57, s24, v237
	v_med3_f32 v58, v58, s24, v237
	v_med3_f32 v59, v59, s24, v237
	v_med3_f32 v60, v60, s24, v237
	v_med3_f32 v61, v61, s24, v237
	v_med3_f32 v62, v62, s24, v237
	v_med3_f32 v63, v63, s24, v237
	v_cvt_pk_fp8_f32 v0, v0, v4
	v_cvt_pk_fp8_f32 v0, v8, v12 op_sel:[0,0,1]
	v_cvt_pk_fp8_f32 v4, v1, v5
	v_cvt_pk_fp8_f32 v4, v9, v13 op_sel:[0,0,1]
	v_cvt_pk_fp8_f32 v8, v2, v6
	v_cvt_pk_fp8_f32 v8, v10, v14 op_sel:[0,0,1]
	v_cvt_pk_fp8_f32 v12, v3, v7
	v_cvt_pk_fp8_f32 v12, v11, v15 op_sel:[0,0,1]
	v_cvt_pk_fp8_f32 v1, v16, v20
	v_cvt_pk_fp8_f32 v1, v24, v28 op_sel:[0,0,1]
	v_cvt_pk_fp8_f32 v5, v17, v21
	v_cvt_pk_fp8_f32 v5, v25, v29 op_sel:[0,0,1]
	v_cvt_pk_fp8_f32 v9, v18, v22
	v_cvt_pk_fp8_f32 v9, v26, v30 op_sel:[0,0,1]
	v_cvt_pk_fp8_f32 v13, v19, v23
	v_cvt_pk_fp8_f32 v13, v27, v31 op_sel:[0,0,1]
	v_cvt_pk_fp8_f32 v2, v32, v36
	v_cvt_pk_fp8_f32 v2, v40, v44 op_sel:[0,0,1]
	v_cvt_pk_fp8_f32 v6, v33, v37
	v_cvt_pk_fp8_f32 v6, v41, v45 op_sel:[0,0,1]
	v_cvt_pk_fp8_f32 v10, v34, v38
	v_cvt_pk_fp8_f32 v10, v42, v46 op_sel:[0,0,1]
	v_cvt_pk_fp8_f32 v14, v35, v39
	v_cvt_pk_fp8_f32 v14, v43, v47 op_sel:[0,0,1]
	v_cvt_pk_fp8_f32 v3, v48, v52
	v_cvt_pk_fp8_f32 v3, v56, v60 op_sel:[0,0,1]
	v_cvt_pk_fp8_f32 v7, v49, v53
	v_cvt_pk_fp8_f32 v7, v57, v61 op_sel:[0,0,1]
	v_cvt_pk_fp8_f32 v11, v50, v54
	v_cvt_pk_fp8_f32 v11, v58, v62 op_sel:[0,0,1]
	v_cvt_pk_fp8_f32 v15, v51, v55
	v_cvt_pk_fp8_f32 v15, v59, v63 op_sel:[0,0,1]
	global_store_dwordx4 v250, v[0:3], s[42:43] nt
	global_store_dwordx4 v250, v[4:7], s[42:43] offset:2048 nt
	global_store_dwordx4 v251, v[8:11], s[42:43] nt
	global_store_dwordx4 v251, v[12:15], s[42:43] offset:2048 nt
	s_add_u32 s42, s42, 0x800000
	s_addc_u32 s43, s43, 0
	global_load_dwordx4 v[0:3], v246, s[4:5] nt
	global_load_dwordx4 v[4:7], v247, s[4:5] nt
	global_load_dwordx4 v[8:11], v248, s[4:5] nt
	global_load_dwordx4 v[12:15], v249, s[4:5] nt
	global_load_dwordx4 v[16:19], v246, s[6:7] nt
	global_load_dwordx4 v[20:23], v247, s[6:7] nt
	global_load_dwordx4 v[24:27], v248, s[6:7] nt
	global_load_dwordx4 v[28:31], v249, s[6:7] nt
	global_load_dwordx4 v[32:35], v246, s[8:9] nt
	global_load_dwordx4 v[36:39], v247, s[8:9] nt
	global_load_dwordx4 v[40:43], v248, s[8:9] nt
	global_load_dwordx4 v[44:47], v249, s[8:9] nt
	global_load_dwordx4 v[48:51], v246, s[38:39] nt
	global_load_dwordx4 v[52:55], v247, s[38:39] nt
	global_load_dwordx4 v[56:59], v248, s[38:39] nt
	global_load_dwordx4 v[60:63], v249, s[38:39] nt
	s_add_u32 s4, s4, 0x2000000
	s_addc_u32 s5, s5, 0
	s_add_u32 s6, s6, 0x2000000
	s_addc_u32 s7, s7, 0
	s_add_u32 s8, s8, 0x2000000
	s_addc_u32 s9, s9, 0
	s_add_u32 s38, s38, 0x2000000
	s_addc_u32 s39, s39, 0
	s_waitcnt vmcnt(40)
; #define GAS __attribute__((address_space(1)))
; template <bool GAIN, bool NT = false> __device__ __forceinline__ void titem8_load(const TItem& d, int lane, f32x4 (&r)[16], f32x4 (&g)[4]) {
;     const int q = lane & 7, kg = lane >> 3; const unsigned lo = (unsigned)((16 * kg) * d.N + 4 * q) * 4u;
;     const GAS char* base = (const GAS char*)d.src;
; #pragma unroll
;     for (int j = 0; j < 16; ++j) { const GAS f32x4* p = (const GAS f32x4*)(base + (size_t)j * (size_t)d.N * 4 + lo); r[j] = NT ? __builtin_nontemporal_load(p) : *p; }
; template <bool GAIN, bool NT = false> __device__ __forceinline__ void titem8_store(const TItem& d, int lane, const f32x4 (&r)[16], const f32x4 (&g)[4]) {
;     const int q = lane & 7, kg = lane >> 3; const unsigned lo = (unsigned)((4 * q) * d.ldk + 16 * kg);
;     GAS char* base = (GAS char*)d.dst;
;     f32x4 s[16];
; #pragma unroll
;     for (int j = 0; j < 16; ++j) s[j] = r[j] * ((GAIN ? g[j >> 2][j & 3] : 1.0f) * W8_SCALE);
; #pragma unroll
;     for (int i = 0; i < 4; ++i) { v4u w;
;         w.x = pk4_fp8w(s[0][i], s[1][i], s[2][i], s[3][i]); w.y = pk4_fp8w(s[4][i], s[5][i], s[6][i], s[7][i]);
;         w.z = pk4_fp8w(s[8][i], s[9][i], s[10][i], s[11][i]); w.w = pk4_fp8w(s[12][i], s[13][i], s[14][i], s[15][i]);
;         GAS v4u* p = (GAS v4u*)(base + (size_t)i * (size_t)d.ldk + lo);
;         if (NT) __builtin_nontemporal_store(w, p); else *p = w; }
; }
	v_pk_mul_f32 v[66:67], v[66:67], s[30:31] op_sel_hi:[1,0]
	v_pk_mul_f32 v[68:69], v[68:69], s[30:31] op_sel_hi:[1,0]
	v_pk_mul_f32 v[70:71], v[70:71], s[30:31] op_sel_hi:[1,0]
	v_pk_mul_f32 v[72:73], v[72:73], s[30:31] op_sel_hi:[1,0]
	v_pk_mul_f32 v[74:75], v[74:75], s[30:31] op_sel_hi:[1,0]
	v_pk_mul_f32 v[76:77], v[76:77], s[30:31] op_sel_hi:[1,0]
	v_pk_mul_f32 v[78:79], v[78:79], s[30:31] op_sel_hi:[1,0]
	v_pk_mul_f32 v[80:81], v[80:81], s[30:31] op_sel_hi:[1,0]
	v_pk_mul_f32 v[82:83], v[82:83], s[30:31] op_sel_hi:[1,0]
	v_pk_mul_f32 v[84:85], v[84:85], s[30:31] op_sel_hi:[1,0]
	v_pk_mul_f32 v[86:87], v[86:87], s[30:31] op_sel_hi:[1,0]
	v_pk_mul_f32 v[88:89], v[88:89], s[30:31] op_sel_hi:[1,0]
	v_pk_mul_f32 v[90:91], v[90:91], s[30:31] op_sel_hi:[1,0]
	v_pk_mul_f32 v[92:93], v[92:93], s[30:31] op_sel_hi:[1,0]
	v_pk_mul_f32 v[94:95], v[94:95], s[30:31] op_sel_hi:[1,0]
	v_pk_mul_f32 v[96:97], v[96:97], s[30:31] op_sel_hi:[1,0]
	v_pk_mul_f32 v[98:99], v[98:99], s[30:31] op_sel_hi:[1,0]
	v_pk_mul_f32 v[100:101], v[100:101], s[30:31] op_sel_hi:[1,0]
	v_pk_mul_f32 v[102:103], v[102:103], s[30:31] op_sel_hi:[1,0]
	v_pk_mul_f32 v[104:105], v[104:105], s[30:31] op_sel_hi:[1,0]
	v_pk_mul_f32 v[106:107], v[106:107], s[30:31] op_sel_hi:[1,0]
	v_pk_mul_f32 v[108:109], v[108:109], s[30:31] op_sel_hi:[1,0]
	v_pk_mul_f32 v[110:111], v[110:111], s[30:31] op_sel_hi:[1,0]
	v_pk_mul_f32 v[112:113], v[112:113], s[30:31] op_sel_hi:[1,0]
	v_pk_mul_f32 v[114:115], v[114:115], s[30:31] op_sel_hi:[1,0]
	v_pk_mul_f32 v[116:117], v[116:117], s[30:31] op_sel_hi:[1,0]
	v_pk_mul_f32 v[118:119], v[118:119], s[30:31] op_sel_hi:[1,0]
	v_pk_mul_f32 v[120:121], v[120:121], s[30:31] op_sel_hi:[1,0]
	v_pk_mul_f32 v[122:123], v[122:123], s[30:31] op_sel_hi:[1,0]
	v_pk_mul_f32 v[124:125], v[124:125], s[30:31] op_sel_hi:[1,0]
	v_pk_mul_f32 v[126:127], v[126:127], s[30:31] op_sel_hi:[1,0]
	v_pk_mul_f32 v[128:129], v[128:129], s[30:31] op_sel_hi:[1,0]
	v_med3_f32 v66, v66, s24, v237
	v_med3_f32 v67, v67, s24, v237
	v_med3_f32 v68, v68, s24, v237
	v_med3_f32 v69, v69, s24, v237
	v_med3_f32 v70, v70, s24, v237
	v_med3_f32 v71, v71, s24, v237
	v_med3_f32 v72, v72, s24, v237
	v_med3_f32 v73, v73, s24, v237
	v_med3_f32 v74, v74, s24, v237
	v_med3_f32 v75, v75, s24, v237
	v_med3_f32 v76, v76, s24, v237
	v_med3_f32 v77, v77, s24, v237
	v_med3_f32 v78, v78, s24, v237
	v_med3_f32 v79, v79, s24, v237
	v_med3_f32 v80, v80, s24, v237
	v_med3_f32 v81, v81, s24, v237
	v_med3_f32 v82, v82, s24, v237
	v_med3_f32 v83, v83, s24, v237
	v_med3_f32 v84, v84, s24, v237
	v_med3_f32 v85, v85, s24, v237
	v_med3_f32 v86, v86, s24, v237
	v_med3_f32 v87, v87, s24, v237
	v_med3_f32 v88, v88, s24, v237
	v_med3_f32 v89, v89, s24, v237
	v_med3_f32 v90, v90, s24, v237
	v_med3_f32 v91, v91, s24, v237
	v_med3_f32 v92, v92, s24, v237
	v_med3_f32 v93, v93, s24, v237
	v_med3_f32 v94, v94, s24, v237
	v_med3_f32 v95, v95, s24, v237
	v_med3_f32 v96, v96, s24, v237
	v_med3_f32 v97, v97, s24, v237
	v_med3_f32 v98, v98, s24, v237
	v_med3_f32 v99, v99, s24, v237
	v_med3_f32 v100, v100, s24, v237
	v_med3_f32 v101, v101, s24, v237
	v_med3_f32 v102, v102, s24, v237
	v_med3_f32 v103, v103, s24, v237
	v_med3_f32 v104, v104, s24, v237
	v_med3_f32 v105, v105, s24, v237
	v_med3_f32 v106, v106, s24, v237
	v_med3_f32 v107, v107, s24, v237
	v_med3_f32 v108, v108, s24, v237
	v_med3_f32 v109, v109, s24, v237
	v_med3_f32 v110, v110, s24, v237
	v_med3_f32 v111, v111, s24, v237
	v_med3_f32 v112, v112, s24, v237
	v_med3_f32 v113, v113, s24, v237
	v_med3_f32 v114, v114, s24, v237
	v_med3_f32 v115, v115, s24, v237
	v_med3_f32 v116, v116, s24, v237
	v_med3_f32 v117, v117, s24, v237
	v_med3_f32 v118, v118, s24, v237
	v_med3_f32 v119, v119, s24, v237
	v_med3_f32 v120, v120, s24, v237
	v_med3_f32 v121, v121, s24, v237
	v_med3_f32 v122, v122, s24, v237
	v_med3_f32 v123, v123, s24, v237
	v_med3_f32 v124, v124, s24, v237
	v_med3_f32 v125, v125, s24, v237
	v_med3_f32 v126, v126, s24, v237
	v_med3_f32 v127, v127, s24, v237
	v_med3_f32 v128, v128, s24, v237
	v_med3_f32 v129, v129, s24, v237
	v_cvt_pk_fp8_f32 v66, v66, v70
	v_cvt_pk_fp8_f32 v66, v74, v78 op_sel:[0,0,1]
	v_cvt_pk_fp8_f32 v70, v67, v71
	v_cvt_pk_fp8_f32 v70, v75, v79 op_sel:[0,0,1]
	v_cvt_pk_fp8_f32 v74, v68, v72
	v_cvt_pk_fp8_f32 v74, v76, v80 op_sel:[0,0,1]
	v_cvt_pk_fp8_f32 v78, v69, v73
	v_cvt_pk_fp8_f32 v78, v77, v81 op_sel:[0,0,1]
	v_cvt_pk_fp8_f32 v67, v82, v86
	v_cvt_pk_fp8_f32 v67, v90, v94 op_sel:[0,0,1]
	v_cvt_pk_fp8_f32 v71, v83, v87
	v_cvt_pk_fp8_f32 v71, v91, v95 op_sel:[0,0,1]
	v_cvt_pk_fp8_f32 v75, v84, v88
	v_cvt_pk_fp8_f32 v75, v92, v96 op_sel:[0,0,1]
	v_cvt_pk_fp8_f32 v79, v85, v89
	v_cvt_pk_fp8_f32 v79, v93, v97 op_sel:[0,0,1]
	v_cvt_pk_fp8_f32 v68, v98, v102
	v_cvt_pk_fp8_f32 v68, v106, v110 op_sel:[0,0,1]
	v_cvt_pk_fp8_f32 v72, v99, v103
	v_cvt_pk_fp8_f32 v72, v107, v111 op_sel:[0,0,1]
	v_cvt_pk_fp8_f32 v76, v100, v104
	v_cvt_pk_fp8_f32 v76, v108, v112 op_sel:[0,0,1]
	v_cvt_pk_fp8_f32 v80, v101, v105
	v_cvt_pk_fp8_f32 v80, v109, v113 op_sel:[0,0,1]
	v_cvt_pk_fp8_f32 v69, v114, v118
	v_cvt_pk_fp8_f32 v69, v122, v126 op_sel:[0,0,1]
	v_cvt_pk_fp8_f32 v73, v115, v119
	v_cvt_pk_fp8_f32 v73, v123, v127 op_sel:[0,0,1]
	v_cvt_pk_fp8_f32 v77, v116, v120
	v_cvt_pk_fp8_f32 v77, v124, v128 op_sel:[0,0,1]
	v_cvt_pk_fp8_f32 v81, v117, v121
	v_cvt_pk_fp8_f32 v81, v125, v129 op_sel:[0,0,1]
	global_store_dwordx4 v250, v[66:69], s[42:43] nt
	global_store_dwordx4 v250, v[70:73], s[42:43] offset:2048 nt
	global_store_dwordx4 v251, v[74:77], s[42:43] nt
	global_store_dwordx4 v251, v[78:81], s[42:43] offset:2048 nt
	s_add_u32 s42, s42, 0x800000
	s_addc_u32 s43, s43, 0
	global_load_dwordx4 v[66:69], v246, s[4:5] nt
	global_load_dwordx4 v[70:73], v247, s[4:5] nt
	global_load_dwordx4 v[74:77], v248, s[4:5] nt
	global_load_dwordx4 v[78:81], v249, s[4:5] nt
	global_load_dwordx4 v[82:85], v246, s[6:7] nt
	global_load_dwordx4 v[86:89], v247, s[6:7] nt
	global_load_dwordx4 v[90:93], v248, s[6:7] nt
	global_load_dwordx4 v[94:97], v249, s[6:7] nt
	global_load_dwordx4 v[98:101], v246, s[8:9] nt
	global_load_dwordx4 v[102:105], v247, s[8:9] nt
	global_load_dwordx4 v[106:109], v248, s[8:9] nt
	global_load_dwordx4 v[110:113], v249, s[8:9] nt
	global_load_dwordx4 v[114:117], v246, s[38:39] nt
	global_load_dwordx4 v[118:121], v247, s[38:39] nt
	global_load_dwordx4 v[122:125], v248, s[38:39] nt
	global_load_dwordx4 v[126:129], v249, s[38:39] nt
	s_add_u32 s4, s4, 0x2000000
	s_addc_u32 s5, s5, 0
	s_add_u32 s6, s6, 0x2000000
	s_addc_u32 s7, s7, 0
	s_add_u32 s8, s8, 0x2000000
	s_addc_u32 s9, s9, 0
	s_add_u32 s38, s38, 0x2000000
	s_addc_u32 s39, s39, 0
	s_waitcnt vmcnt(40)
; #define GAS __attribute__((address_space(1)))
; template <bool GAIN, bool NT = false> __device__ __forceinline__ void titem8_load(const TItem& d, int lane, f32x4 (&r)[16], f32x4 (&g)[4]) {
;     const int q = lane & 7, kg = lane >> 3; const unsigned lo = (unsigned)((16 * kg) * d.N + 4 * q) * 4u;
;     const GAS char* base = (const GAS char*)d.src;
; #pragma unroll
;     for (int j = 0; j < 16; ++j) { const GAS f32x4* p = (const GAS f32x4*)(base + (size_t)j * (size_t)d.N * 4 + lo); r[j] = NT ? __builtin_nontemporal_load(p) : *p; }
; template <bool GAIN, bool NT = false> __device__ __forceinline__ void titem8_store(const TItem& d, int lane, const f32x4 (&r)[16], const f32x4 (&g)[4]) {
;     const int q = lane & 7, kg = lane >> 3; const unsigned lo = (unsigned)((4 * q) * d.ldk + 16 * kg);
;     GAS char* base = (GAS char*)d.dst;
;     f32x4 s[16];
; #pragma unroll
;     for (int j = 0; j < 16; ++j) s[j] = r[j] * ((GAIN ? g[j >> 2][j & 3] : 1.0f) * W8_SCALE);
; #pragma unroll
;     for (int i = 0; i < 4; ++i) { v4u w;
;         w.x = pk4_fp8w(s[0][i], s[1][i], s[2][i], s[3][i]); w.y = pk4_fp8w(s[4][i], s[5][i], s[6][i], s[7][i]);
;         w.z = pk4_fp8w(s[8][i], s[9][i], s[10][i], s[11][i]); w.w = pk4_fp8w(s[12][i], s[13][i], s[14][i], s[15][i]);
;         GAS v4u* p = (GAS v4u*)(base + (size_t)i * (size_t)d.ldk + lo);
;         if (NT) __builtin_nontemporal_store(w, p); else *p = w; }
; }
	v_pk_mul_f32 v[130:131], v[130:131], s[30:31] op_sel_hi:[1,0]
	v_pk_mul_f32 v[132:133], v[132:133], s[30:31] op_sel_hi:[1,0]
	v_pk_mul_f32 v[134:135], v[134:135], s[30:31] op_sel_hi:[1,0]
	v_pk_mul_f32 v[136:137], v[136:137], s[30:31] op_sel_hi:[1,0]
	v_pk_mul_f32 v[138:139], v[138:139], s[30:31] op_sel_hi:[1,0]
	v_pk_mul_f32 v[140:141], v[140:141], s[30:31] op_sel_hi:[1,0]
	v_pk_mul_f32 v[142:143], v[142:143], s[30:31] op_sel_hi:[1,0]
	v_pk_mul_f32 v[144:145], v[144:145], s[30:31] op_sel_hi:[1,0]
	v_pk_mul_f32 v[146:147], v[146:147], s[30:31] op_sel_hi:[1,0]
	v_pk_mul_f32 v[148:149], v[148:149], s[30:31] op_sel_hi:[1,0]
	v_pk_mul_f32 v[150:151], v[150:151], s[30:31] op_sel_hi:[1,0]
	v_pk_mul_f32 v[152:153], v[152:153], s[30:31] op_sel_hi:[1,0]
	v_pk_mul_f32 v[154:155], v[154:155], s[30:31] op_sel_hi:[1,0]
	v_pk_mul_f32 v[156:157], v[156:157], s[30:31] op_sel_hi:[1,0]
	v_pk_mul_f32 v[158:159], v[158:159], s[30:31] op_sel_hi:[1,0]
	v_pk_mul_f32 v[160:161], v[160:161], s[30:31] op_sel_hi:[1,0]
	v_pk_mul_f32 v[162:163], v[162:163], s[30:31] op_sel_hi:[1,0]
	v_pk_mul_f32 v[164:165], v[164:165], s[30:31] op_sel_hi:[1,0]
	v_pk_mul_f32 v[166:167], v[166:167], s[30:31] op_sel_hi:[1,0]
	v_pk_mul_f32 v[168:169], v[168:169], s[30:31] op_sel_hi:[1,0]
	v_pk_mul_f32 v[170:171], v[170:171], s[30:31] op_sel_hi:[1,0]
	v_pk_mul_f32 v[172:173], v[172:173], s[30:31] op_sel_hi:[1,0]
	v_pk_mul_f32 v[174:175], v[174:175], s[30:31] op_sel_hi:[1,0]
	v_pk_mul_f32 v[176:177], v[176:177], s[30:31] op_sel_hi:[1,0]
	v_pk_mul_f32 v[178:179], v[178:179], s[30:31] op_sel_hi:[1,0]
	v_pk_mul_f32 v[180:181], v[180:181], s[30:31] op_sel_hi:[1,0]
	v_pk_mul_f32 v[182:183], v[182:183], s[30:31] op_sel_hi:[1,0]
	v_pk_mul_f32 v[184:185], v[184:185], s[30:31] op_sel_hi:[1,0]
	v_pk_mul_f32 v[186:187], v[186:187], s[30:31] op_sel_hi:[1,0]
	v_pk_mul_f32 v[188:189], v[188:189], s[30:31] op_sel_hi:[1,0]
	v_pk_mul_f32 v[190:191], v[190:191], s[30:31] op_sel_hi:[1,0]
	v_pk_mul_f32 v[192:193], v[192:193], s[30:31] op_sel_hi:[1,0]
	v_med3_f32 v130, v130, s24, v237
	v_med3_f32 v131, v131, s24, v237
	v_med3_f32 v132, v132, s24, v237
	v_med3_f32 v133, v133, s24, v237
	v_med3_f32 v134, v134, s24, v237
	v_med3_f32 v135, v135, s24, v237
	v_med3_f32 v136, v136, s24, v237
	v_med3_f32 v137, v137, s24, v237
	v_med3_f32 v138, v138, s24, v237
	v_med3_f32 v139, v139, s24, v237
	v_med3_f32 v140, v140, s24, v237
	v_med3_f32 v141, v141, s24, v237
	v_med3_f32 v142, v142, s24, v237
	v_med3_f32 v143, v143, s24, v237
	v_med3_f32 v144, v144, s24, v237
	v_med3_f32 v145, v145, s24, v237
	v_med3_f32 v146, v146, s24, v237
	v_med3_f32 v147, v147, s24, v237
	v_med3_f32 v148, v148, s24, v237
	v_med3_f32 v149, v149, s24, v237
	v_med3_f32 v150, v150, s24, v237
	v_med3_f32 v151, v151, s24, v237
	v_med3_f32 v152, v152, s24, v237
	v_med3_f32 v153, v153, s24, v237
	v_med3_f32 v154, v154, s24, v237
	v_med3_f32 v155, v155, s24, v237
	v_med3_f32 v156, v156, s24, v237
	v_med3_f32 v157, v157, s24, v237
	v_med3_f32 v158, v158, s24, v237
	v_med3_f32 v159, v159, s24, v237
	v_med3_f32 v160, v160, s24, v237
	v_med3_f32 v161, v161, s24, v237
	v_med3_f32 v162, v162, s24, v237
	v_med3_f32 v163, v163, s24, v237
	v_med3_f32 v164, v164, s24, v237
	v_med3_f32 v165, v165, s24, v237
	v_med3_f32 v166, v166, s24, v237
	v_med3_f32 v167, v167, s24, v237
	v_med3_f32 v168, v168, s24, v237
	v_med3_f32 v169, v169, s24, v237
	v_med3_f32 v170, v170, s24, v237
	v_med3_f32 v171, v171, s24, v237
	v_med3_f32 v172, v172, s24, v237
	v_med3_f32 v173, v173, s24, v237
	v_med3_f32 v174, v174, s24, v237
	v_med3_f32 v175, v175, s24, v237
	v_med3_f32 v176, v176, s24, v237
	v_med3_f32 v177, v177, s24, v237
	v_med3_f32 v178, v178, s24, v237
	v_med3_f32 v179, v179, s24, v237
	v_med3_f32 v180, v180, s24, v237
	v_med3_f32 v181, v181, s24, v237
	v_med3_f32 v182, v182, s24, v237
	v_med3_f32 v183, v183, s24, v237
	v_med3_f32 v184, v184, s24, v237
	v_med3_f32 v185, v185, s24, v237
	v_med3_f32 v186, v186, s24, v237
	v_med3_f32 v187, v187, s24, v237
	v_med3_f32 v188, v188, s24, v237
	v_med3_f32 v189, v189, s24, v237
	v_med3_f32 v190, v190, s24, v237
	v_med3_f32 v191, v191, s24, v237
	v_med3_f32 v192, v192, s24, v237
	v_med3_f32 v193, v193, s24, v237
	v_cvt_pk_fp8_f32 v130, v130, v134
	v_cvt_pk_fp8_f32 v130, v138, v142 op_sel:[0,0,1]
	v_cvt_pk_fp8_f32 v134, v131, v135
	v_cvt_pk_fp8_f32 v134, v139, v143 op_sel:[0,0,1]
	v_cvt_pk_fp8_f32 v138, v132, v136
	v_cvt_pk_fp8_f32 v138, v140, v144 op_sel:[0,0,1]
	v_cvt_pk_fp8_f32 v142, v133, v137
	v_cvt_pk_fp8_f32 v142, v141, v145 op_sel:[0,0,1]
	v_cvt_pk_fp8_f32 v131, v146, v150
	v_cvt_pk_fp8_f32 v131, v154, v158 op_sel:[0,0,1]
	v_cvt_pk_fp8_f32 v135, v147, v151
	v_cvt_pk_fp8_f32 v135, v155, v159 op_sel:[0,0,1]
	v_cvt_pk_fp8_f32 v139, v148, v152
	v_cvt_pk_fp8_f32 v139, v156, v160 op_sel:[0,0,1]
	v_cvt_pk_fp8_f32 v143, v149, v153
	v_cvt_pk_fp8_f32 v143, v157, v161 op_sel:[0,0,1]
	v_cvt_pk_fp8_f32 v132, v162, v166
	v_cvt_pk_fp8_f32 v132, v170, v174 op_sel:[0,0,1]
	v_cvt_pk_fp8_f32 v136, v163, v167
	v_cvt_pk_fp8_f32 v136, v171, v175 op_sel:[0,0,1]
	v_cvt_pk_fp8_f32 v140, v164, v168
	v_cvt_pk_fp8_f32 v140, v172, v176 op_sel:[0,0,1]
	v_cvt_pk_fp8_f32 v144, v165, v169
	v_cvt_pk_fp8_f32 v144, v173, v177 op_sel:[0,0,1]
	v_cvt_pk_fp8_f32 v133, v178, v182
	v_cvt_pk_fp8_f32 v133, v186, v190 op_sel:[0,0,1]
	v_cvt_pk_fp8_f32 v137, v179, v183
	v_cvt_pk_fp8_f32 v137, v187, v191 op_sel:[0,0,1]
	v_cvt_pk_fp8_f32 v141, v180, v184
	v_cvt_pk_fp8_f32 v141, v188, v192 op_sel:[0,0,1]
	v_cvt_pk_fp8_f32 v145, v181, v185
	v_cvt_pk_fp8_f32 v145, v189, v193 op_sel:[0,0,1]
	global_store_dwordx4 v250, v[130:133], s[42:43] nt
	global_store_dwordx4 v250, v[134:137], s[42:43] offset:2048 nt
	global_store_dwordx4 v251, v[138:141], s[42:43] nt
	global_store_dwordx4 v251, v[142:145], s[42:43] offset:2048 nt
	s_add_u32 s42, s42, 0x800000
	s_addc_u32 s43, s43, 0
	global_load_dwordx4 v[130:133], v246, s[4:5] nt
	global_load_dwordx4 v[134:137], v247, s[4:5] nt
	global_load_dwordx4 v[138:141], v248, s[4:5] nt
	global_load_dwordx4 v[142:145], v249, s[4:5] nt
	global_load_dwordx4 v[146:149], v246, s[6:7] nt
	global_load_dwordx4 v[150:153], v247, s[6:7] nt
	global_load_dwordx4 v[154:157], v248, s[6:7] nt
	global_load_dwordx4 v[158:161], v249, s[6:7] nt
	global_load_dwordx4 v[162:165], v246, s[8:9] nt
	global_load_dwordx4 v[166:169], v247, s[8:9] nt
	global_load_dwordx4 v[170:173], v248, s[8:9] nt
	global_load_dwordx4 v[174:177], v249, s[8:9] nt
	global_load_dwordx4 v[178:181], v246, s[38:39] nt
	global_load_dwordx4 v[182:185], v247, s[38:39] nt
	global_load_dwordx4 v[186:189], v248, s[38:39] nt
	global_load_dwordx4 v[190:193], v249, s[38:39] nt
	s_add_u32 s4, s4, 0x2000000
	s_addc_u32 s5, s5, 0
	s_add_u32 s6, s6, 0x2000000
	s_addc_u32 s7, s7, 0
	s_add_u32 s8, s8, 0x2000000
	s_addc_u32 s9, s9, 0
	s_add_u32 s38, s38, 0x2000000
	s_addc_u32 s39, s39, 0
	s_waitcnt vmcnt(40)
; #define GAS __attribute__((address_space(1)))
; template <bool GAIN, bool NT = false> __device__ __forceinline__ void titem8_load(const TItem& d, int lane, f32x4 (&r)[16], f32x4 (&g)[4]) {
;     const int q = lane & 7, kg = lane >> 3; const unsigned lo = (unsigned)((16 * kg) * d.N + 4 * q) * 4u;
;     const GAS char* base = (const GAS char*)d.src;
; #pragma unroll
;     for (int j = 0; j < 16; ++j) { const GAS f32x4* p = (const GAS f32x4*)(base + (size_t)j * (size_t)d.N * 4 + lo); r[j] = NT ? __builtin_nontemporal_load(p) : *p; }
; template <bool GAIN, bool NT = false> __device__ __forceinline__ void titem8_store(const TItem& d, int lane, const f32x4 (&r)[16], const f32x4 (&g)[4]) {
;     const int q = lane & 7, kg = lane >> 3; const unsigned lo = (unsigned)((4 * q) * d.ldk + 16 * kg);
;     GAS char* base = (GAS char*)d.dst;
;     f32x4 s[16];
; #pragma unroll
;     for (int j = 0; j < 16; ++j) s[j] = r[j] * ((GAIN ? g[j >> 2][j & 3] : 1.0f) * W8_SCALE);
; #pragma unroll
;     for (int i = 0; i < 4; ++i) { v4u w;
;         w.x = pk4_fp8w(s[0][i], s[1][i], s[2][i], s[3][i]); w.y = pk4_fp8w(s[4][i], s[5][i], s[6][i], s[7][i]);
;         w.z = pk4_fp8w(s[8][i], s[9][i], s[10][i], s[11][i]); w.w = pk4_fp8w(s[12][i], s[13][i], s[14][i], s[15][i]);
;         GAS v4u* p = (GAS v4u*)(base + (size_t)i * (size_t)d.ldk + lo);
;         if (NT) __builtin_nontemporal_store(w, p); else *p = w; }
; }
	v_pk_mul_f32 v[0:1], v[0:1], s[30:31] op_sel_hi:[1,0]
	v_pk_mul_f32 v[2:3], v[2:3], s[30:31] op_sel_hi:[1,0]
	v_pk_mul_f32 v[4:5], v[4:5], s[30:31] op_sel_hi:[1,0]
	v_pk_mul_f32 v[6:7], v[6:7], s[30:31] op_sel_hi:[1,0]
	v_pk_mul_f32 v[8:9], v[8:9], s[30:31] op_sel_hi:[1,0]
	v_pk_mul_f32 v[10:11], v[10:11], s[30:31] op_sel_hi:[1,0]
	v_pk_mul_f32 v[12:13], v[12:13], s[30:31] op_sel_hi:[1,0]
	v_pk_mul_f32 v[14:15], v[14:15], s[30:31] op_sel_hi:[1,0]
	v_pk_mul_f32 v[16:17], v[16:17], s[30:31] op_sel_hi:[1,0]
	v_pk_mul_f32 v[18:19], v[18:19], s[30:31] op_sel_hi:[1,0]
	v_pk_mul_f32 v[20:21], v[20:21], s[30:31] op_sel_hi:[1,0]
	v_pk_mul_f32 v[22:23], v[22:23], s[30:31] op_sel_hi:[1,0]
	v_pk_mul_f32 v[24:25], v[24:25], s[30:31] op_sel_hi:[1,0]
	v_pk_mul_f32 v[26:27], v[26:27], s[30:31] op_sel_hi:[1,0]
	v_pk_mul_f32 v[28:29], v[28:29], s[30:31] op_sel_hi:[1,0]
	v_pk_mul_f32 v[30:31], v[30:31], s[30:31] op_sel_hi:[1,0]
	v_pk_mul_f32 v[32:33], v[32:33], s[30:31] op_sel_hi:[1,0]
	v_pk_mul_f32 v[34:35], v[34:35], s[30:31] op_sel_hi:[1,0]
	v_pk_mul_f32 v[36:37], v[36:37], s[30:31] op_sel_hi:[1,0]
	v_pk_mul_f32 v[38:39], v[38:39], s[30:31] op_sel_hi:[1,0]
	v_pk_mul_f32 v[40:41], v[40:41], s[30:31] op_sel_hi:[1,0]
	v_pk_mul_f32 v[42:43], v[42:43], s[30:31] op_sel_hi:[1,0]
	v_pk_mul_f32 v[44:45], v[44:45], s[30:31] op_sel_hi:[1,0]
	v_pk_mul_f32 v[46:47], v[46:47], s[30:31] op_sel_hi:[1,0]
	v_pk_mul_f32 v[48:49], v[48:49], s[30:31] op_sel_hi:[1,0]
	v_pk_mul_f32 v[50:51], v[50:51], s[30:31] op_sel_hi:[1,0]
	v_pk_mul_f32 v[52:53], v[52:53], s[30:31] op_sel_hi:[1,0]
	v_pk_mul_f32 v[54:55], v[54:55], s[30:31] op_sel_hi:[1,0]
	v_pk_mul_f32 v[56:57], v[56:57], s[30:31] op_sel_hi:[1,0]
	v_pk_mul_f32 v[58:59], v[58:59], s[30:31] op_sel_hi:[1,0]
	v_pk_mul_f32 v[60:61], v[60:61], s[30:31] op_sel_hi:[1,0]
	v_pk_mul_f32 v[62:63], v[62:63], s[30:31] op_sel_hi:[1,0]
	v_med3_f32 v0, v0, s24, v237
	v_med3_f32 v1, v1, s24, v237
	v_med3_f32 v2, v2, s24, v237
	v_med3_f32 v3, v3, s24, v237
	v_med3_f32 v4, v4, s24, v237
	v_med3_f32 v5, v5, s24, v237
	v_med3_f32 v6, v6, s24, v237
	v_med3_f32 v7, v7, s24, v237
	v_med3_f32 v8, v8, s24, v237
	v_med3_f32 v9, v9, s24, v237
	v_med3_f32 v10, v10, s24, v237
	v_med3_f32 v11, v11, s24, v237
	v_med3_f32 v12, v12, s24, v237
	v_med3_f32 v13, v13, s24, v237
	v_med3_f32 v14, v14, s24, v237
	v_med3_f32 v15, v15, s24, v237
	v_med3_f32 v16, v16, s24, v237
	v_med3_f32 v17, v17, s24, v237
	v_med3_f32 v18, v18, s24, v237
	v_med3_f32 v19, v19, s24, v237
	v_med3_f32 v20, v20, s24, v237
	v_med3_f32 v21, v21, s24, v237
	v_med3_f32 v22, v22, s24, v237
	v_med3_f32 v23, v23, s24, v237
	v_med3_f32 v24, v24, s24, v237
	v_med3_f32 v25, v25, s24, v237
	v_med3_f32 v26, v26, s24, v237
	v_med3_f32 v27, v27, s24, v237
	v_med3_f32 v28, v28, s24, v237
	v_med3_f32 v29, v29, s24, v237
	v_med3_f32 v30, v30, s24, v237
	v_med3_f32 v31, v31, s24, v237
	v_med3_f32 v32, v32, s24, v237
	v_med3_f32 v33, v33, s24, v237
	v_med3_f32 v34, v34, s24, v237
	v_med3_f32 v35, v35, s24, v237
	v_med3_f32 v36, v36, s24, v237
	v_med3_f32 v37, v37, s24, v237
	v_med3_f32 v38, v38, s24, v237
	v_med3_f32 v39, v39, s24, v237
	v_med3_f32 v40, v40, s24, v237
	v_med3_f32 v41, v41, s24, v237
	v_med3_f32 v42, v42, s24, v237
	v_med3_f32 v43, v43, s24, v237
	v_med3_f32 v44, v44, s24, v237
	v_med3_f32 v45, v45, s24, v237
	v_med3_f32 v46, v46, s24, v237
	v_med3_f32 v47, v47, s24, v237
	v_med3_f32 v48, v48, s24, v237
	v_med3_f32 v49, v49, s24, v237
	v_med3_f32 v50, v50, s24, v237
	v_med3_f32 v51, v51, s24, v237
	v_med3_f32 v52, v52, s24, v237
	v_med3_f32 v53, v53, s24, v237
	v_med3_f32 v54, v54, s24, v237
	v_med3_f32 v55, v55, s24, v237
	v_med3_f32 v56, v56, s24, v237
	v_med3_f32 v57, v57, s24, v237
	v_med3_f32 v58, v58, s24, v237
	v_med3_f32 v59, v59, s24, v237
	v_med3_f32 v60, v60, s24, v237
	v_med3_f32 v61, v61, s24, v237
	v_med3_f32 v62, v62, s24, v237
	v_med3_f32 v63, v63, s24, v237
	v_cvt_pk_fp8_f32 v0, v0, v4
	v_cvt_pk_fp8_f32 v0, v8, v12 op_sel:[0,0,1]
	v_cvt_pk_fp8_f32 v4, v1, v5
	v_cvt_pk_fp8_f32 v4, v9, v13 op_sel:[0,0,1]
	v_cvt_pk_fp8_f32 v8, v2, v6
	v_cvt_pk_fp8_f32 v8, v10, v14 op_sel:[0,0,1]
	v_cvt_pk_fp8_f32 v12, v3, v7
	v_cvt_pk_fp8_f32 v12, v11, v15 op_sel:[0,0,1]
	v_cvt_pk_fp8_f32 v1, v16, v20
	v_cvt_pk_fp8_f32 v1, v24, v28 op_sel:[0,0,1]
	v_cvt_pk_fp8_f32 v5, v17, v21
	v_cvt_pk_fp8_f32 v5, v25, v29 op_sel:[0,0,1]
	v_cvt_pk_fp8_f32 v9, v18, v22
	v_cvt_pk_fp8_f32 v9, v26, v30 op_sel:[0,0,1]
	v_cvt_pk_fp8_f32 v13, v19, v23
	v_cvt_pk_fp8_f32 v13, v27, v31 op_sel:[0,0,1]
	v_cvt_pk_fp8_f32 v2, v32, v36
	v_cvt_pk_fp8_f32 v2, v40, v44 op_sel:[0,0,1]
	v_cvt_pk_fp8_f32 v6, v33, v37
	v_cvt_pk_fp8_f32 v6, v41, v45 op_sel:[0,0,1]
	v_cvt_pk_fp8_f32 v10, v34, v38
	v_cvt_pk_fp8_f32 v10, v42, v46 op_sel:[0,0,1]
	v_cvt_pk_fp8_f32 v14, v35, v39
	v_cvt_pk_fp8_f32 v14, v43, v47 op_sel:[0,0,1]
	v_cvt_pk_fp8_f32 v3, v48, v52
	v_cvt_pk_fp8_f32 v3, v56, v60 op_sel:[0,0,1]
	v_cvt_pk_fp8_f32 v7, v49, v53
	v_cvt_pk_fp8_f32 v7, v57, v61 op_sel:[0,0,1]
	v_cvt_pk_fp8_f32 v11, v50, v54
	v_cvt_pk_fp8_f32 v11, v58, v62 op_sel:[0,0,1]
	v_cvt_pk_fp8_f32 v15, v51, v55
	v_cvt_pk_fp8_f32 v15, v59, v63 op_sel:[0,0,1]
	global_store_dwordx4 v250, v[0:3], s[42:43] nt
	global_store_dwordx4 v250, v[4:7], s[42:43] offset:2048 nt
	global_store_dwordx4 v251, v[8:11], s[42:43] nt
	global_store_dwordx4 v251, v[12:15], s[42:43] offset:2048 nt
	s_add_u32 s42, s42, 0x800000
	s_addc_u32 s43, s43, 0
	global_load_dwordx4 v[0:3], v246, s[4:5] nt
	global_load_dwordx4 v[4:7], v247, s[4:5] nt
	global_load_dwordx4 v[8:11], v248, s[4:5] nt
	global_load_dwordx4 v[12:15], v249, s[4:5] nt
	global_load_dwordx4 v[16:19], v246, s[6:7] nt
	global_load_dwordx4 v[20:23], v247, s[6:7] nt
	global_load_dwordx4 v[24:27], v248, s[6:7] nt
	global_load_dwordx4 v[28:31], v249, s[6:7] nt
	global_load_dwordx4 v[32:35], v246, s[8:9] nt
	global_load_dwordx4 v[36:39], v247, s[8:9] nt
	global_load_dwordx4 v[40:43], v248, s[8:9] nt
	global_load_dwordx4 v[44:47], v249, s[8:9] nt
	global_load_dwordx4 v[48:51], v246, s[38:39] nt
	global_load_dwordx4 v[52:55], v247, s[38:39] nt
	global_load_dwordx4 v[56:59], v248, s[38:39] nt
	global_load_dwordx4 v[60:63], v249, s[38:39] nt
	s_add_u32 s4, s4, 0x2000000
	s_addc_u32 s5, s5, 0
	s_add_u32 s6, s6, 0x2000000
	s_addc_u32 s7, s7, 0
	s_add_u32 s8, s8, 0x2000000
	s_addc_u32 s9, s9, 0
	s_add_u32 s38, s38, 0x2000000
	s_addc_u32 s39, s39, 0
	s_waitcnt vmcnt(40)
; #define GAS __attribute__((address_space(1)))
; template <bool GAIN, bool NT = false> __device__ __forceinline__ void titem8_load(const TItem& d, int lane, f32x4 (&r)[16], f32x4 (&g)[4]) {
;     const int q = lane & 7, kg = lane >> 3; const unsigned lo = (unsigned)((16 * kg) * d.N + 4 * q) * 4u;
;     const GAS char* base = (const GAS char*)d.src;
; #pragma unroll
;     for (int j = 0; j < 16; ++j) { const GAS f32x4* p = (const GAS f32x4*)(base + (size_t)j * (size_t)d.N * 4 + lo); r[j] = NT ? __builtin_nontemporal_load(p) : *p; }
; template <bool GAIN, bool NT = false> __device__ __forceinline__ void titem8_store(const TItem& d, int lane, const f32x4 (&r)[16], const f32x4 (&g)[4]) {
;     const int q = lane & 7, kg = lane >> 3; const unsigned lo = (unsigned)((4 * q) * d.ldk + 16 * kg);
;     GAS char* base = (GAS char*)d.dst;
;     f32x4 s[16];
; #pragma unroll
;     for (int j = 0; j < 16; ++j) s[j] = r[j] * ((GAIN ? g[j >> 2][j & 3] : 1.0f) * W8_SCALE);
; #pragma unroll
;     for (int i = 0; i < 4; ++i) { v4u w;
;         w.x = pk4_fp8w(s[0][i], s[1][i], s[2][i], s[3][i]); w.y = pk4_fp8w(s[4][i], s[5][i], s[6][i], s[7][i]);
;         w.z = pk4_fp8w(s[8][i], s[9][i], s[10][i], s[11][i]); w.w = pk4_fp8w(s[12][i], s[13][i], s[14][i], s[15][i]);
;         GAS v4u* p = (GAS v4u*)(base + (size_t)i * (size_t)d.ldk + lo);
;         if (NT) __builtin_nontemporal_store(w, p); else *p = w; }
; }
	v_pk_mul_f32 v[66:67], v[66:67], s[30:31] op_sel_hi:[1,0]
	v_pk_mul_f32 v[68:69], v[68:69], s[30:31] op_sel_hi:[1,0]
	v_pk_mul_f32 v[70:71], v[70:71], s[30:31] op_sel_hi:[1,0]
	v_pk_mul_f32 v[72:73], v[72:73], s[30:31] op_sel_hi:[1,0]
	v_pk_mul_f32 v[74:75], v[74:75], s[30:31] op_sel_hi:[1,0]
	v_pk_mul_f32 v[76:77], v[76:77], s[30:31] op_sel_hi:[1,0]
	v_pk_mul_f32 v[78:79], v[78:79], s[30:31] op_sel_hi:[1,0]
	v_pk_mul_f32 v[80:81], v[80:81], s[30:31] op_sel_hi:[1,0]
	v_pk_mul_f32 v[82:83], v[82:83], s[30:31] op_sel_hi:[1,0]
	v_pk_mul_f32 v[84:85], v[84:85], s[30:31] op_sel_hi:[1,0]
	v_pk_mul_f32 v[86:87], v[86:87], s[30:31] op_sel_hi:[1,0]
	v_pk_mul_f32 v[88:89], v[88:89], s[30:31] op_sel_hi:[1,0]
	v_pk_mul_f32 v[90:91], v[90:91], s[30:31] op_sel_hi:[1,0]
	v_pk_mul_f32 v[92:93], v[92:93], s[30:31] op_sel_hi:[1,0]
	v_pk_mul_f32 v[94:95], v[94:95], s[30:31] op_sel_hi:[1,0]
	v_pk_mul_f32 v[96:97], v[96:97], s[30:31] op_sel_hi:[1,0]
	v_pk_mul_f32 v[98:99], v[98:99], s[30:31] op_sel_hi:[1,0]
	v_pk_mul_f32 v[100:101], v[100:101], s[30:31] op_sel_hi:[1,0]
	v_pk_mul_f32 v[102:103], v[102:103], s[30:31] op_sel_hi:[1,0]
	v_pk_mul_f32 v[104:105], v[104:105], s[30:31] op_sel_hi:[1,0]
	v_pk_mul_f32 v[106:107], v[106:107], s[30:31] op_sel_hi:[1,0]
	v_pk_mul_f32 v[108:109], v[108:109], s[30:31] op_sel_hi:[1,0]
	v_pk_mul_f32 v[110:111], v[110:111], s[30:31] op_sel_hi:[1,0]
	v_pk_mul_f32 v[112:113], v[112:113], s[30:31] op_sel_hi:[1,0]
	v_pk_mul_f32 v[114:115], v[114:115], s[30:31] op_sel_hi:[1,0]
	v_pk_mul_f32 v[116:117], v[116:117], s[30:31] op_sel_hi:[1,0]
	v_pk_mul_f32 v[118:119], v[118:119], s[30:31] op_sel_hi:[1,0]
	v_pk_mul_f32 v[120:121], v[120:121], s[30:31] op_sel_hi:[1,0]
	v_pk_mul_f32 v[122:123], v[122:123], s[30:31] op_sel_hi:[1,0]
	v_pk_mul_f32 v[124:125], v[124:125], s[30:31] op_sel_hi:[1,0]
	v_pk_mul_f32 v[126:127], v[126:127], s[30:31] op_sel_hi:[1,0]
	v_pk_mul_f32 v[128:129], v[128:129], s[30:31] op_sel_hi:[1,0]
	v_med3_f32 v66, v66, s24, v237
	v_med3_f32 v67, v67, s24, v237
	v_med3_f32 v68, v68, s24, v237
	v_med3_f32 v69, v69, s24, v237
	v_med3_f32 v70, v70, s24, v237
	v_med3_f32 v71, v71, s24, v237
	v_med3_f32 v72, v72, s24, v237
	v_med3_f32 v73, v73, s24, v237
	v_med3_f32 v74, v74, s24, v237
	v_med3_f32 v75, v75, s24, v237
	v_med3_f32 v76, v76, s24, v237
	v_med3_f32 v77, v77, s24, v237
	v_med3_f32 v78, v78, s24, v237
	v_med3_f32 v79, v79, s24, v237
	v_med3_f32 v80, v80, s24, v237
	v_med3_f32 v81, v81, s24, v237
	v_med3_f32 v82, v82, s24, v237
	v_med3_f32 v83, v83, s24, v237
	v_med3_f32 v84, v84, s24, v237
	v_med3_f32 v85, v85, s24, v237
	v_med3_f32 v86, v86, s24, v237
	v_med3_f32 v87, v87, s24, v237
	v_med3_f32 v88, v88, s24, v237
	v_med3_f32 v89, v89, s24, v237
	v_med3_f32 v90, v90, s24, v237
	v_med3_f32 v91, v91, s24, v237
	v_med3_f32 v92, v92, s24, v237
	v_med3_f32 v93, v93, s24, v237
	v_med3_f32 v94, v94, s24, v237
	v_med3_f32 v95, v95, s24, v237
	v_med3_f32 v96, v96, s24, v237
	v_med3_f32 v97, v97, s24, v237
	v_med3_f32 v98, v98, s24, v237
	v_med3_f32 v99, v99, s24, v237
	v_med3_f32 v100, v100, s24, v237
	v_med3_f32 v101, v101, s24, v237
	v_med3_f32 v102, v102, s24, v237
	v_med3_f32 v103, v103, s24, v237
	v_med3_f32 v104, v104, s24, v237
	v_med3_f32 v105, v105, s24, v237
	v_med3_f32 v106, v106, s24, v237
	v_med3_f32 v107, v107, s24, v237
	v_med3_f32 v108, v108, s24, v237
	v_med3_f32 v109, v109, s24, v237
	v_med3_f32 v110, v110, s24, v237
	v_med3_f32 v111, v111, s24, v237
	v_med3_f32 v112, v112, s24, v237
	v_med3_f32 v113, v113, s24, v237
	v_med3_f32 v114, v114, s24, v237
	v_med3_f32 v115, v115, s24, v237
	v_med3_f32 v116, v116, s24, v237
	v_med3_f32 v117, v117, s24, v237
	v_med3_f32 v118, v118, s24, v237
	v_med3_f32 v119, v119, s24, v237
	v_med3_f32 v120, v120, s24, v237
	v_med3_f32 v121, v121, s24, v237
	v_med3_f32 v122, v122, s24, v237
	v_med3_f32 v123, v123, s24, v237
	v_med3_f32 v124, v124, s24, v237
	v_med3_f32 v125, v125, s24, v237
	v_med3_f32 v126, v126, s24, v237
	v_med3_f32 v127, v127, s24, v237
	v_med3_f32 v128, v128, s24, v237
	v_med3_f32 v129, v129, s24, v237
	v_cvt_pk_fp8_f32 v66, v66, v70
	v_cvt_pk_fp8_f32 v66, v74, v78 op_sel:[0,0,1]
	v_cvt_pk_fp8_f32 v70, v67, v71
	v_cvt_pk_fp8_f32 v70, v75, v79 op_sel:[0,0,1]
	v_cvt_pk_fp8_f32 v74, v68, v72
	v_cvt_pk_fp8_f32 v74, v76, v80 op_sel:[0,0,1]
	v_cvt_pk_fp8_f32 v78, v69, v73
	v_cvt_pk_fp8_f32 v78, v77, v81 op_sel:[0,0,1]
	v_cvt_pk_fp8_f32 v67, v82, v86
	v_cvt_pk_fp8_f32 v67, v90, v94 op_sel:[0,0,1]
	v_cvt_pk_fp8_f32 v71, v83, v87
	v_cvt_pk_fp8_f32 v71, v91, v95 op_sel:[0,0,1]
	v_cvt_pk_fp8_f32 v75, v84, v88
	v_cvt_pk_fp8_f32 v75, v92, v96 op_sel:[0,0,1]
	v_cvt_pk_fp8_f32 v79, v85, v89
	v_cvt_pk_fp8_f32 v79, v93, v97 op_sel:[0,0,1]
	v_cvt_pk_fp8_f32 v68, v98, v102
	v_cvt_pk_fp8_f32 v68, v106, v110 op_sel:[0,0,1]
	v_cvt_pk_fp8_f32 v72, v99, v103
	v_cvt_pk_fp8_f32 v72, v107, v111 op_sel:[0,0,1]
	v_cvt_pk_fp8_f32 v76, v100, v104
	v_cvt_pk_fp8_f32 v76, v108, v112 op_sel:[0,0,1]
	v_cvt_pk_fp8_f32 v80, v101, v105
	v_cvt_pk_fp8_f32 v80, v109, v113 op_sel:[0,0,1]
	v_cvt_pk_fp8_f32 v69, v114, v118
	v_cvt_pk_fp8_f32 v69, v122, v126 op_sel:[0,0,1]
	v_cvt_pk_fp8_f32 v73, v115, v119
	v_cvt_pk_fp8_f32 v73, v123, v127 op_sel:[0,0,1]
	v_cvt_pk_fp8_f32 v77, v116, v120
	v_cvt_pk_fp8_f32 v77, v124, v128 op_sel:[0,0,1]
	v_cvt_pk_fp8_f32 v81, v117, v121
	v_cvt_pk_fp8_f32 v81, v125, v129 op_sel:[0,0,1]
	global_store_dwordx4 v250, v[66:69], s[42:43] nt
	global_store_dwordx4 v250, v[70:73], s[42:43] offset:2048 nt
	global_store_dwordx4 v251, v[74:77], s[42:43] nt
	global_store_dwordx4 v251, v[78:81], s[42:43] offset:2048 nt
	s_add_u32 s42, s42, 0x800000
	s_addc_u32 s43, s43, 0
	global_load_dwordx4 v[66:69], v246, s[4:5] nt
	global_load_dwordx4 v[70:73], v247, s[4:5] nt
	global_load_dwordx4 v[74:77], v248, s[4:5] nt
	global_load_dwordx4 v[78:81], v249, s[4:5] nt
	global_load_dwordx4 v[82:85], v246, s[6:7] nt
	global_load_dwordx4 v[86:89], v247, s[6:7] nt
	global_load_dwordx4 v[90:93], v248, s[6:7] nt
	global_load_dwordx4 v[94:97], v249, s[6:7] nt
	global_load_dwordx4 v[98:101], v246, s[8:9] nt
	global_load_dwordx4 v[102:105], v247, s[8:9] nt
	global_load_dwordx4 v[106:109], v248, s[8:9] nt
	global_load_dwordx4 v[110:113], v249, s[8:9] nt
	global_load_dwordx4 v[114:117], v246, s[38:39] nt
	global_load_dwordx4 v[118:121], v247, s[38:39] nt
	global_load_dwordx4 v[122:125], v248, s[38:39] nt
	global_load_dwordx4 v[126:129], v249, s[38:39] nt
	s_add_u32 s4, s4, 0x2000000
	s_addc_u32 s5, s5, 0
	s_add_u32 s6, s6, 0x2000000
	s_addc_u32 s7, s7, 0
	s_add_u32 s8, s8, 0x2000000
	s_addc_u32 s9, s9, 0
	s_add_u32 s38, s38, 0x2000000
	s_addc_u32 s39, s39, 0
	s_waitcnt vmcnt(40)
; #define GAS __attribute__((address_space(1)))
; template <bool GAIN, bool NT = false> __device__ __forceinline__ void titem8_load(const TItem& d, int lane, f32x4 (&r)[16], f32x4 (&g)[4]) {
;     const int q = lane & 7, kg = lane >> 3; const unsigned lo = (unsigned)((16 * kg) * d.N + 4 * q) * 4u;
;     const GAS char* base = (const GAS char*)d.src;
; #pragma unroll
;     for (int j = 0; j < 16; ++j) { const GAS f32x4* p = (const GAS f32x4*)(base + (size_t)j * (size_t)d.N * 4 + lo); r[j] = NT ? __builtin_nontemporal_load(p) : *p; }
; template <bool GAIN, bool NT = false> __device__ __forceinline__ void titem8_store(const TItem& d, int lane, const f32x4 (&r)[16], const f32x4 (&g)[4]) {
;     const int q = lane & 7, kg = lane >> 3; const unsigned lo = (unsigned)((4 * q) * d.ldk + 16 * kg);
;     GAS char* base = (GAS char*)d.dst;
;     f32x4 s[16];
; #pragma unroll
;     for (int j = 0; j < 16; ++j) s[j] = r[j] * ((GAIN ? g[j >> 2][j & 3] : 1.0f) * W8_SCALE);
; #pragma unroll
;     for (int i = 0; i < 4; ++i) { v4u w;
;         w.x = pk4_fp8w(s[0][i], s[1][i], s[2][i], s[3][i]); w.y = pk4_fp8w(s[4][i], s[5][i], s[6][i], s[7][i]);
;         w.z = pk4_fp8w(s[8][i], s[9][i], s[10][i], s[11][i]); w.w = pk4_fp8w(s[12][i], s[13][i], s[14][i], s[15][i]);
;         GAS v4u* p = (GAS v4u*)(base + (size_t)i * (size_t)d.ldk + lo);
;         if (NT) __builtin_nontemporal_store(w, p); else *p = w; }
; }
	v_pk_mul_f32 v[130:131], v[130:131], s[30:31] op_sel_hi:[1,0]
	v_pk_mul_f32 v[132:133], v[132:133], s[30:31] op_sel_hi:[1,0]
	v_pk_mul_f32 v[134:135], v[134:135], s[30:31] op_sel_hi:[1,0]
	v_pk_mul_f32 v[136:137], v[136:137], s[30:31] op_sel_hi:[1,0]
	v_pk_mul_f32 v[138:139], v[138:139], s[30:31] op_sel_hi:[1,0]
	v_pk_mul_f32 v[140:141], v[140:141], s[30:31] op_sel_hi:[1,0]
	v_pk_mul_f32 v[142:143], v[142:143], s[30:31] op_sel_hi:[1,0]
	v_pk_mul_f32 v[144:145], v[144:145], s[30:31] op_sel_hi:[1,0]
	v_pk_mul_f32 v[146:147], v[146:147], s[30:31] op_sel_hi:[1,0]
	v_pk_mul_f32 v[148:149], v[148:149], s[30:31] op_sel_hi:[1,0]
	v_pk_mul_f32 v[150:151], v[150:151], s[30:31] op_sel_hi:[1,0]
	v_pk_mul_f32 v[152:153], v[152:153], s[30:31] op_sel_hi:[1,0]
	v_pk_mul_f32 v[154:155], v[154:155], s[30:31] op_sel_hi:[1,0]
	v_pk_mul_f32 v[156:157], v[156:157], s[30:31] op_sel_hi:[1,0]
	v_pk_mul_f32 v[158:159], v[158:159], s[30:31] op_sel_hi:[1,0]
	v_pk_mul_f32 v[160:161], v[160:161], s[30:31] op_sel_hi:[1,0]
	v_pk_mul_f32 v[162:163], v[162:163], s[30:31] op_sel_hi:[1,0]
	v_pk_mul_f32 v[164:165], v[164:165], s[30:31] op_sel_hi:[1,0]
	v_pk_mul_f32 v[166:167], v[166:167], s[30:31] op_sel_hi:[1,0]
	v_pk_mul_f32 v[168:169], v[168:169], s[30:31] op_sel_hi:[1,0]
	v_pk_mul_f32 v[170:171], v[170:171], s[30:31] op_sel_hi:[1,0]
	v_pk_mul_f32 v[172:173], v[172:173], s[30:31] op_sel_hi:[1,0]
	v_pk_mul_f32 v[174:175], v[174:175], s[30:31] op_sel_hi:[1,0]
	v_pk_mul_f32 v[176:177], v[176:177], s[30:31] op_sel_hi:[1,0]
	v_pk_mul_f32 v[178:179], v[178:179], s[30:31] op_sel_hi:[1,0]
	v_pk_mul_f32 v[180:181], v[180:181], s[30:31] op_sel_hi:[1,0]
	v_pk_mul_f32 v[182:183], v[182:183], s[30:31] op_sel_hi:[1,0]
	v_pk_mul_f32 v[184:185], v[184:185], s[30:31] op_sel_hi:[1,0]
	v_pk_mul_f32 v[186:187], v[186:187], s[30:31] op_sel_hi:[1,0]
	v_pk_mul_f32 v[188:189], v[188:189], s[30:31] op_sel_hi:[1,0]
	v_pk_mul_f32 v[190:191], v[190:191], s[30:31] op_sel_hi:[1,0]
	v_pk_mul_f32 v[192:193], v[192:193], s[30:31] op_sel_hi:[1,0]
	v_med3_f32 v130, v130, s24, v237
	v_med3_f32 v131, v131, s24, v237
	v_med3_f32 v132, v132, s24, v237
	v_med3_f32 v133, v133, s24, v237
	v_med3_f32 v134, v134, s24, v237
	v_med3_f32 v135, v135, s24, v237
	v_med3_f32 v136, v136, s24, v237
	v_med3_f32 v137, v137, s24, v237
	v_med3_f32 v138, v138, s24, v237
	v_med3_f32 v139, v139, s24, v237
	v_med3_f32 v140, v140, s24, v237
	v_med3_f32 v141, v141, s24, v237
	v_med3_f32 v142, v142, s24, v237
	v_med3_f32 v143, v143, s24, v237
	v_med3_f32 v144, v144, s24, v237
	v_med3_f32 v145, v145, s24, v237
	v_med3_f32 v146, v146, s24, v237
	v_med3_f32 v147, v147, s24, v237
	v_med3_f32 v148, v148, s24, v237
	v_med3_f32 v149, v149, s24, v237
	v_med3_f32 v150, v150, s24, v237
	v_med3_f32 v151, v151, s24, v237
	v_med3_f32 v152, v152, s24, v237
	v_med3_f32 v153, v153, s24, v237
	v_med3_f32 v154, v154, s24, v237
	v_med3_f32 v155, v155, s24, v237
	v_med3_f32 v156, v156, s24, v237
	v_med3_f32 v157, v157, s24, v237
	v_med3_f32 v158, v158, s24, v237
	v_med3_f32 v159, v159, s24, v237
	v_med3_f32 v160, v160, s24, v237
	v_med3_f32 v161, v161, s24, v237
	v_med3_f32 v162, v162, s24, v237
	v_med3_f32 v163, v163, s24, v237
	v_med3_f32 v164, v164, s24, v237
	v_med3_f32 v165, v165, s24, v237
	v_med3_f32 v166, v166, s24, v237
	v_med3_f32 v167, v167, s24, v237
	v_med3_f32 v168, v168, s24, v237
	v_med3_f32 v169, v169, s24, v237
	v_med3_f32 v170, v170, s24, v237
	v_med3_f32 v171, v171, s24, v237
	v_med3_f32 v172, v172, s24, v237
	v_med3_f32 v173, v173, s24, v237
	v_med3_f32 v174, v174, s24, v237
	v_med3_f32 v175, v175, s24, v237
	v_med3_f32 v176, v176, s24, v237
	v_med3_f32 v177, v177, s24, v237
	v_med3_f32 v178, v178, s24, v237
	v_med3_f32 v179, v179, s24, v237
	v_med3_f32 v180, v180, s24, v237
	v_med3_f32 v181, v181, s24, v237
	v_med3_f32 v182, v182, s24, v237
	v_med3_f32 v183, v183, s24, v237
	v_med3_f32 v184, v184, s24, v237
	v_med3_f32 v185, v185, s24, v237
	v_med3_f32 v186, v186, s24, v237
	v_med3_f32 v187, v187, s24, v237
	v_med3_f32 v188, v188, s24, v237
	v_med3_f32 v189, v189, s24, v237
	v_med3_f32 v190, v190, s24, v237
	v_med3_f32 v191, v191, s24, v237
	v_med3_f32 v192, v192, s24, v237
	v_med3_f32 v193, v193, s24, v237
	v_cvt_pk_fp8_f32 v130, v130, v134
	v_cvt_pk_fp8_f32 v130, v138, v142 op_sel:[0,0,1]
	v_cvt_pk_fp8_f32 v134, v131, v135
	v_cvt_pk_fp8_f32 v134, v139, v143 op_sel:[0,0,1]
	v_cvt_pk_fp8_f32 v138, v132, v136
	v_cvt_pk_fp8_f32 v138, v140, v144 op_sel:[0,0,1]
	v_cvt_pk_fp8_f32 v142, v133, v137
	v_cvt_pk_fp8_f32 v142, v141, v145 op_sel:[0,0,1]
	v_cvt_pk_fp8_f32 v131, v146, v150
	v_cvt_pk_fp8_f32 v131, v154, v158 op_sel:[0,0,1]
	v_cvt_pk_fp8_f32 v135, v147, v151
	v_cvt_pk_fp8_f32 v135, v155, v159 op_sel:[0,0,1]
	v_cvt_pk_fp8_f32 v139, v148, v152
	v_cvt_pk_fp8_f32 v139, v156, v160 op_sel:[0,0,1]
	v_cvt_pk_fp8_f32 v143, v149, v153
	v_cvt_pk_fp8_f32 v143, v157, v161 op_sel:[0,0,1]
	v_cvt_pk_fp8_f32 v132, v162, v166
	v_cvt_pk_fp8_f32 v132, v170, v174 op_sel:[0,0,1]
	v_cvt_pk_fp8_f32 v136, v163, v167
	v_cvt_pk_fp8_f32 v136, v171, v175 op_sel:[0,0,1]
	v_cvt_pk_fp8_f32 v140, v164, v168
	v_cvt_pk_fp8_f32 v140, v172, v176 op_sel:[0,0,1]
	v_cvt_pk_fp8_f32 v144, v165, v169
	v_cvt_pk_fp8_f32 v144, v173, v177 op_sel:[0,0,1]
	v_cvt_pk_fp8_f32 v133, v178, v182
	v_cvt_pk_fp8_f32 v133, v186, v190 op_sel:[0,0,1]
	v_cvt_pk_fp8_f32 v137, v179, v183
	v_cvt_pk_fp8_f32 v137, v187, v191 op_sel:[0,0,1]
	v_cvt_pk_fp8_f32 v141, v180, v184
	v_cvt_pk_fp8_f32 v141, v188, v192 op_sel:[0,0,1]
	v_cvt_pk_fp8_f32 v145, v181, v185
	v_cvt_pk_fp8_f32 v145, v189, v193 op_sel:[0,0,1]
	global_store_dwordx4 v250, v[130:133], s[42:43] nt
	global_store_dwordx4 v250, v[134:137], s[42:43] offset:2048 nt
	global_store_dwordx4 v251, v[138:141], s[42:43] nt
	global_store_dwordx4 v251, v[142:145], s[42:43] offset:2048 nt
	s_add_u32 s42, s42, 0x800000
	s_addc_u32 s43, s43, 0
	global_load_dwordx4 v[130:133], v246, s[4:5] nt
	global_load_dwordx4 v[134:137], v247, s[4:5] nt
	global_load_dwordx4 v[138:141], v248, s[4:5] nt
	global_load_dwordx4 v[142:145], v249, s[4:5] nt
	global_load_dwordx4 v[146:149], v246, s[6:7] nt
	global_load_dwordx4 v[150:153], v247, s[6:7] nt
	global_load_dwordx4 v[154:157], v248, s[6:7] nt
	global_load_dwordx4 v[158:161], v249, s[6:7] nt
	global_load_dwordx4 v[162:165], v246, s[8:9] nt
	global_load_dwordx4 v[166:169], v247, s[8:9] nt
	global_load_dwordx4 v[170:173], v248, s[8:9] nt
	global_load_dwordx4 v[174:177], v249, s[8:9] nt
	global_load_dwordx4 v[178:181], v246, s[38:39] nt
	global_load_dwordx4 v[182:185], v247, s[38:39] nt
	global_load_dwordx4 v[186:189], v248, s[38:39] nt
	global_load_dwordx4 v[190:193], v249, s[38:39] nt
	s_add_u32 s4, s4, 0x2000000
	s_addc_u32 s5, s5, 0
	s_add_u32 s6, s6, 0x2000000
	s_addc_u32 s7, s7, 0
	s_add_u32 s8, s8, 0x2000000
	s_addc_u32 s9, s9, 0
	s_add_u32 s38, s38, 0x2000000
	s_addc_u32 s39, s39, 0
	s_waitcnt vmcnt(40)
; #define GAS __attribute__((address_space(1)))
; template <bool GAIN, bool NT = false> __device__ __forceinline__ void titem8_load(const TItem& d, int lane, f32x4 (&r)[16], f32x4 (&g)[4]) {
;     const int q = lane & 7, kg = lane >> 3; const unsigned lo = (unsigned)((16 * kg) * d.N + 4 * q) * 4u;
;     const GAS char* base = (const GAS char*)d.src;
; #pragma unroll
;     for (int j = 0; j < 16; ++j) { const GAS f32x4* p = (const GAS f32x4*)(base + (size_t)j * (size_t)d.N * 4 + lo); r[j] = NT ? __builtin_nontemporal_load(p) : *p; }
; template <bool GAIN, bool NT = false> __device__ __forceinline__ void titem8_store(const TItem& d, int lane, const f32x4 (&r)[16], const f32x4 (&g)[4]) {
;     const int q = lane & 7, kg = lane >> 3; const unsigned lo = (unsigned)((4 * q) * d.ldk + 16 * kg);
;     GAS char* base = (GAS char*)d.dst;
;     f32x4 s[16];
; #pragma unroll
;     for (int j = 0; j < 16; ++j) s[j] = r[j] * ((GAIN ? g[j >> 2][j & 3] : 1.0f) * W8_SCALE);
; #pragma unroll
;     for (int i = 0; i < 4; ++i) { v4u w;
;         w.x = pk4_fp8w(s[0][i], s[1][i], s[2][i], s[3][i]); w.y = pk4_fp8w(s[4][i], s[5][i], s[6][i], s[7][i]);
;         w.z = pk4_fp8w(s[8][i], s[9][i], s[10][i], s[11][i]); w.w = pk4_fp8w(s[12][i], s[13][i], s[14][i], s[15][i]);
;         GAS v4u* p = (GAS v4u*)(base + (size_t)i * (size_t)d.ldk + lo);
;         if (NT) __builtin_nontemporal_store(w, p); else *p = w; }
; }
	v_pk_mul_f32 v[0:1], v[0:1], s[30:31] op_sel_hi:[1,0]
	v_pk_mul_f32 v[2:3], v[2:3], s[30:31] op_sel_hi:[1,0]
	v_pk_mul_f32 v[4:5], v[4:5], s[30:31] op_sel_hi:[1,0]
	v_pk_mul_f32 v[6:7], v[6:7], s[30:31] op_sel_hi:[1,0]
	v_pk_mul_f32 v[8:9], v[8:9], s[30:31] op_sel_hi:[1,0]
	v_pk_mul_f32 v[10:11], v[10:11], s[30:31] op_sel_hi:[1,0]
	v_pk_mul_f32 v[12:13], v[12:13], s[30:31] op_sel_hi:[1,0]
	v_pk_mul_f32 v[14:15], v[14:15], s[30:31] op_sel_hi:[1,0]
	v_pk_mul_f32 v[16:17], v[16:17], s[30:31] op_sel_hi:[1,0]
	v_pk_mul_f32 v[18:19], v[18:19], s[30:31] op_sel_hi:[1,0]
	v_pk_mul_f32 v[20:21], v[20:21], s[30:31] op_sel_hi:[1,0]
	v_pk_mul_f32 v[22:23], v[22:23], s[30:31] op_sel_hi:[1,0]
	v_pk_mul_f32 v[24:25], v[24:25], s[30:31] op_sel_hi:[1,0]
	v_pk_mul_f32 v[26:27], v[26:27], s[30:31] op_sel_hi:[1,0]
	v_pk_mul_f32 v[28:29], v[28:29], s[30:31] op_sel_hi:[1,0]
	v_pk_mul_f32 v[30:31], v[30:31], s[30:31] op_sel_hi:[1,0]
	v_pk_mul_f32 v[32:33], v[32:33], s[30:31] op_sel_hi:[1,0]
	v_pk_mul_f32 v[34:35], v[34:35], s[30:31] op_sel_hi:[1,0]
	v_pk_mul_f32 v[36:37], v[36:37], s[30:31] op_sel_hi:[1,0]
	v_pk_mul_f32 v[38:39], v[38:39], s[30:31] op_sel_hi:[1,0]
	v_pk_mul_f32 v[40:41], v[40:41], s[30:31] op_sel_hi:[1,0]
	v_pk_mul_f32 v[42:43], v[42:43], s[30:31] op_sel_hi:[1,0]
	v_pk_mul_f32 v[44:45], v[44:45], s[30:31] op_sel_hi:[1,0]
	v_pk_mul_f32 v[46:47], v[46:47], s[30:31] op_sel_hi:[1,0]
	v_pk_mul_f32 v[48:49], v[48:49], s[30:31] op_sel_hi:[1,0]
	v_pk_mul_f32 v[50:51], v[50:51], s[30:31] op_sel_hi:[1,0]
	v_pk_mul_f32 v[52:53], v[52:53], s[30:31] op_sel_hi:[1,0]
	v_pk_mul_f32 v[54:55], v[54:55], s[30:31] op_sel_hi:[1,0]
	v_pk_mul_f32 v[56:57], v[56:57], s[30:31] op_sel_hi:[1,0]
	v_pk_mul_f32 v[58:59], v[58:59], s[30:31] op_sel_hi:[1,0]
	v_pk_mul_f32 v[60:61], v[60:61], s[30:31] op_sel_hi:[1,0]
	v_pk_mul_f32 v[62:63], v[62:63], s[30:31] op_sel_hi:[1,0]
	v_med3_f32 v0, v0, s24, v237
	v_med3_f32 v1, v1, s24, v237
	v_med3_f32 v2, v2, s24, v237
	v_med3_f32 v3, v3, s24, v237
	v_med3_f32 v4, v4, s24, v237
	v_med3_f32 v5, v5, s24, v237
	v_med3_f32 v6, v6, s24, v237
	v_med3_f32 v7, v7, s24, v237
	v_med3_f32 v8, v8, s24, v237
	v_med3_f32 v9, v9, s24, v237
	v_med3_f32 v10, v10, s24, v237
	v_med3_f32 v11, v11, s24, v237
	v_med3_f32 v12, v12, s24, v237
	v_med3_f32 v13, v13, s24, v237
	v_med3_f32 v14, v14, s24, v237
	v_med3_f32 v15, v15, s24, v237
	v_med3_f32 v16, v16, s24, v237
	v_med3_f32 v17, v17, s24, v237
	v_med3_f32 v18, v18, s24, v237
	v_med3_f32 v19, v19, s24, v237
	v_med3_f32 v20, v20, s24, v237
	v_med3_f32 v21, v21, s24, v237
	v_med3_f32 v22, v22, s24, v237
	v_med3_f32 v23, v23, s24, v237
	v_med3_f32 v24, v24, s24, v237
	v_med3_f32 v25, v25, s24, v237
	v_med3_f32 v26, v26, s24, v237
	v_med3_f32 v27, v27, s24, v237
	v_med3_f32 v28, v28, s24, v237
	v_med3_f32 v29, v29, s24, v237
	v_med3_f32 v30, v30, s24, v237
	v_med3_f32 v31, v31, s24, v237
	v_med3_f32 v32, v32, s24, v237
	v_med3_f32 v33, v33, s24, v237
	v_med3_f32 v34, v34, s24, v237
	v_med3_f32 v35, v35, s24, v237
	v_med3_f32 v36, v36, s24, v237
	v_med3_f32 v37, v37, s24, v237
	v_med3_f32 v38, v38, s24, v237
	v_med3_f32 v39, v39, s24, v237
	v_med3_f32 v40, v40, s24, v237
	v_med3_f32 v41, v41, s24, v237
	v_med3_f32 v42, v42, s24, v237
	v_med3_f32 v43, v43, s24, v237
	v_med3_f32 v44, v44, s24, v237
	v_med3_f32 v45, v45, s24, v237
	v_med3_f32 v46, v46, s24, v237
	v_med3_f32 v47, v47, s24, v237
	v_med3_f32 v48, v48, s24, v237
	v_med3_f32 v49, v49, s24, v237
	v_med3_f32 v50, v50, s24, v237
	v_med3_f32 v51, v51, s24, v237
	v_med3_f32 v52, v52, s24, v237
	v_med3_f32 v53, v53, s24, v237
	v_med3_f32 v54, v54, s24, v237
	v_med3_f32 v55, v55, s24, v237
	v_med3_f32 v56, v56, s24, v237
	v_med3_f32 v57, v57, s24, v237
	v_med3_f32 v58, v58, s24, v237
	v_med3_f32 v59, v59, s24, v237
	v_med3_f32 v60, v60, s24, v237
	v_med3_f32 v61, v61, s24, v237
	v_med3_f32 v62, v62, s24, v237
	v_med3_f32 v63, v63, s24, v237
	v_cvt_pk_fp8_f32 v0, v0, v4
	v_cvt_pk_fp8_f32 v0, v8, v12 op_sel:[0,0,1]
	v_cvt_pk_fp8_f32 v4, v1, v5
	v_cvt_pk_fp8_f32 v4, v9, v13 op_sel:[0,0,1]
	v_cvt_pk_fp8_f32 v8, v2, v6
	v_cvt_pk_fp8_f32 v8, v10, v14 op_sel:[0,0,1]
	v_cvt_pk_fp8_f32 v12, v3, v7
	v_cvt_pk_fp8_f32 v12, v11, v15 op_sel:[0,0,1]
	v_cvt_pk_fp8_f32 v1, v16, v20
	v_cvt_pk_fp8_f32 v1, v24, v28 op_sel:[0,0,1]
	v_cvt_pk_fp8_f32 v5, v17, v21
	v_cvt_pk_fp8_f32 v5, v25, v29 op_sel:[0,0,1]
	v_cvt_pk_fp8_f32 v9, v18, v22
	v_cvt_pk_fp8_f32 v9, v26, v30 op_sel:[0,0,1]
	v_cvt_pk_fp8_f32 v13, v19, v23
	v_cvt_pk_fp8_f32 v13, v27, v31 op_sel:[0,0,1]
	v_cvt_pk_fp8_f32 v2, v32, v36
	v_cvt_pk_fp8_f32 v2, v40, v44 op_sel:[0,0,1]
	v_cvt_pk_fp8_f32 v6, v33, v37
	v_cvt_pk_fp8_f32 v6, v41, v45 op_sel:[0,0,1]
	v_cvt_pk_fp8_f32 v10, v34, v38
	v_cvt_pk_fp8_f32 v10, v42, v46 op_sel:[0,0,1]
	v_cvt_pk_fp8_f32 v14, v35, v39
	v_cvt_pk_fp8_f32 v14, v43, v47 op_sel:[0,0,1]
	v_cvt_pk_fp8_f32 v3, v48, v52
	v_cvt_pk_fp8_f32 v3, v56, v60 op_sel:[0,0,1]
	v_cvt_pk_fp8_f32 v7, v49, v53
	v_cvt_pk_fp8_f32 v7, v57, v61 op_sel:[0,0,1]
	v_cvt_pk_fp8_f32 v11, v50, v54
	v_cvt_pk_fp8_f32 v11, v58, v62 op_sel:[0,0,1]
	v_cvt_pk_fp8_f32 v15, v51, v55
	v_cvt_pk_fp8_f32 v15, v59, v63 op_sel:[0,0,1]
	global_store_dwordx4 v250, v[0:3], s[42:43] nt
	global_store_dwordx4 v250, v[4:7], s[42:43] offset:2048 nt
	global_store_dwordx4 v251, v[8:11], s[42:43] nt
	global_store_dwordx4 v251, v[12:15], s[42:43] offset:2048 nt
	s_add_u32 s42, s42, 0x800000
	s_addc_u32 s43, s43, 0
	global_load_dwordx4 v[0:3], v246, s[4:5] nt
	global_load_dwordx4 v[4:7], v247, s[4:5] nt
	global_load_dwordx4 v[8:11], v248, s[4:5] nt
	global_load_dwordx4 v[12:15], v249, s[4:5] nt
	global_load_dwordx4 v[16:19], v246, s[6:7] nt
	global_load_dwordx4 v[20:23], v247, s[6:7] nt
	global_load_dwordx4 v[24:27], v248, s[6:7] nt
	global_load_dwordx4 v[28:31], v249, s[6:7] nt
	global_load_dwordx4 v[32:35], v246, s[8:9] nt
	global_load_dwordx4 v[36:39], v247, s[8:9] nt
	global_load_dwordx4 v[40:43], v248, s[8:9] nt
	global_load_dwordx4 v[44:47], v249, s[8:9] nt
	global_load_dwordx4 v[48:51], v246, s[38:39] nt
	global_load_dwordx4 v[52:55], v247, s[38:39] nt
	global_load_dwordx4 v[56:59], v248, s[38:39] nt
	global_load_dwordx4 v[60:63], v249, s[38:39] nt
	s_add_u32 s4, s4, 0x2000000
	s_addc_u32 s5, s5, 0
	s_add_u32 s6, s6, 0x2000000
	s_addc_u32 s7, s7, 0
	s_add_u32 s8, s8, 0x2000000
	s_addc_u32 s9, s9, 0
	s_add_u32 s38, s38, 0x2000000
	s_addc_u32 s39, s39, 0
	s_waitcnt vmcnt(40)
; #define GAS __attribute__((address_space(1)))
; template <bool GAIN, bool NT = false> __device__ __forceinline__ void titem8_load(const TItem& d, int lane, f32x4 (&r)[16], f32x4 (&g)[4]) {
;     const int q = lane & 7, kg = lane >> 3; const unsigned lo = (unsigned)((16 * kg) * d.N + 4 * q) * 4u;
;     const GAS char* base = (const GAS char*)d.src;
; #pragma unroll
;     for (int j = 0; j < 16; ++j) { const GAS f32x4* p = (const GAS f32x4*)(base + (size_t)j * (size_t)d.N * 4 + lo); r[j] = NT ? __builtin_nontemporal_load(p) : *p; }
; template <bool GAIN, bool NT = false> __device__ __forceinline__ void titem8_store(const TItem& d, int lane, const f32x4 (&r)[16], const f32x4 (&g)[4]) {
;     const int q = lane & 7, kg = lane >> 3; const unsigned lo = (unsigned)((4 * q) * d.ldk + 16 * kg);
;     GAS char* base = (GAS char*)d.dst;
;     f32x4 s[16];
; #pragma unroll
;     for (int j = 0; j < 16; ++j) s[j] = r[j] * ((GAIN ? g[j >> 2][j & 3] : 1.0f) * W8_SCALE);
; #pragma unroll
;     for (int i = 0; i < 4; ++i) { v4u w;
;         w.x = pk4_fp8w(s[0][i], s[1][i], s[2][i], s[3][i]); w.y = pk4_fp8w(s[4][i], s[5][i], s[6][i], s[7][i]);
;         w.z = pk4_fp8w(s[8][i], s[9][i], s[10][i], s[11][i]); w.w = pk4_fp8w(s[12][i], s[13][i], s[14][i], s[15][i]);
;         GAS v4u* p = (GAS v4u*)(base + (size_t)i * (size_t)d.ldk + lo);
;         if (NT) __builtin_nontemporal_store(w, p); else *p = w; }
; }
	v_pk_mul_f32 v[66:67], v[66:67], s[30:31] op_sel_hi:[1,0]
	v_pk_mul_f32 v[68:69], v[68:69], s[30:31] op_sel_hi:[1,0]
	v_pk_mul_f32 v[70:71], v[70:71], s[30:31] op_sel_hi:[1,0]
	v_pk_mul_f32 v[72:73], v[72:73], s[30:31] op_sel_hi:[1,0]
	v_pk_mul_f32 v[74:75], v[74:75], s[30:31] op_sel_hi:[1,0]
	v_pk_mul_f32 v[76:77], v[76:77], s[30:31] op_sel_hi:[1,0]
	v_pk_mul_f32 v[78:79], v[78:79], s[30:31] op_sel_hi:[1,0]
	v_pk_mul_f32 v[80:81], v[80:81], s[30:31] op_sel_hi:[1,0]
	v_pk_mul_f32 v[82:83], v[82:83], s[30:31] op_sel_hi:[1,0]
	v_pk_mul_f32 v[84:85], v[84:85], s[30:31] op_sel_hi:[1,0]
	v_pk_mul_f32 v[86:87], v[86:87], s[30:31] op_sel_hi:[1,0]
	v_pk_mul_f32 v[88:89], v[88:89], s[30:31] op_sel_hi:[1,0]
	v_pk_mul_f32 v[90:91], v[90:91], s[30:31] op_sel_hi:[1,0]
	v_pk_mul_f32 v[92:93], v[92:93], s[30:31] op_sel_hi:[1,0]
	v_pk_mul_f32 v[94:95], v[94:95], s[30:31] op_sel_hi:[1,0]
	v_pk_mul_f32 v[96:97], v[96:97], s[30:31] op_sel_hi:[1,0]
	v_pk_mul_f32 v[98:99], v[98:99], s[30:31] op_sel_hi:[1,0]
	v_pk_mul_f32 v[100:101], v[100:101], s[30:31] op_sel_hi:[1,0]
	v_pk_mul_f32 v[102:103], v[102:103], s[30:31] op_sel_hi:[1,0]
	v_pk_mul_f32 v[104:105], v[104:105], s[30:31] op_sel_hi:[1,0]
	v_pk_mul_f32 v[106:107], v[106:107], s[30:31] op_sel_hi:[1,0]
	v_pk_mul_f32 v[108:109], v[108:109], s[30:31] op_sel_hi:[1,0]
	v_pk_mul_f32 v[110:111], v[110:111], s[30:31] op_sel_hi:[1,0]
	v_pk_mul_f32 v[112:113], v[112:113], s[30:31] op_sel_hi:[1,0]
	v_pk_mul_f32 v[114:115], v[114:115], s[30:31] op_sel_hi:[1,0]
	v_pk_mul_f32 v[116:117], v[116:117], s[30:31] op_sel_hi:[1,0]
	v_pk_mul_f32 v[118:119], v[118:119], s[30:31] op_sel_hi:[1,0]
	v_pk_mul_f32 v[120:121], v[120:121], s[30:31] op_sel_hi:[1,0]
	v_pk_mul_f32 v[122:123], v[122:123], s[30:31] op_sel_hi:[1,0]
	v_pk_mul_f32 v[124:125], v[124:125], s[30:31] op_sel_hi:[1,0]
	v_pk_mul_f32 v[126:127], v[126:127], s[30:31] op_sel_hi:[1,0]
	v_pk_mul_f32 v[128:129], v[128:129], s[30:31] op_sel_hi:[1,0]
	v_med3_f32 v66, v66, s24, v237
	v_med3_f32 v67, v67, s24, v237
	v_med3_f32 v68, v68, s24, v237
	v_med3_f32 v69, v69, s24, v237
	v_med3_f32 v70, v70, s24, v237
	v_med3_f32 v71, v71, s24, v237
	v_med3_f32 v72, v72, s24, v237
	v_med3_f32 v73, v73, s24, v237
	v_med3_f32 v74, v74, s24, v237
	v_med3_f32 v75, v75, s24, v237
	v_med3_f32 v76, v76, s24, v237
	v_med3_f32 v77, v77, s24, v237
	v_med3_f32 v78, v78, s24, v237
	v_med3_f32 v79, v79, s24, v237
	v_med3_f32 v80, v80, s24, v237
	v_med3_f32 v81, v81, s24, v237
	v_med3_f32 v82, v82, s24, v237
	v_med3_f32 v83, v83, s24, v237
	v_med3_f32 v84, v84, s24, v237
	v_med3_f32 v85, v85, s24, v237
	v_med3_f32 v86, v86, s24, v237
	v_med3_f32 v87, v87, s24, v237
	v_med3_f32 v88, v88, s24, v237
	v_med3_f32 v89, v89, s24, v237
	v_med3_f32 v90, v90, s24, v237
	v_med3_f32 v91, v91, s24, v237
	v_med3_f32 v92, v92, s24, v237
	v_med3_f32 v93, v93, s24, v237
	v_med3_f32 v94, v94, s24, v237
	v_med3_f32 v95, v95, s24, v237
	v_med3_f32 v96, v96, s24, v237
	v_med3_f32 v97, v97, s24, v237
	v_med3_f32 v98, v98, s24, v237
	v_med3_f32 v99, v99, s24, v237
	v_med3_f32 v100, v100, s24, v237
	v_med3_f32 v101, v101, s24, v237
	v_med3_f32 v102, v102, s24, v237
	v_med3_f32 v103, v103, s24, v237
	v_med3_f32 v104, v104, s24, v237
	v_med3_f32 v105, v105, s24, v237
	v_med3_f32 v106, v106, s24, v237
	v_med3_f32 v107, v107, s24, v237
	v_med3_f32 v108, v108, s24, v237
	v_med3_f32 v109, v109, s24, v237
	v_med3_f32 v110, v110, s24, v237
	v_med3_f32 v111, v111, s24, v237
	v_med3_f32 v112, v112, s24, v237
	v_med3_f32 v113, v113, s24, v237
	v_med3_f32 v114, v114, s24, v237
	v_med3_f32 v115, v115, s24, v237
	v_med3_f32 v116, v116, s24, v237
	v_med3_f32 v117, v117, s24, v237
	v_med3_f32 v118, v118, s24, v237
	v_med3_f32 v119, v119, s24, v237
	v_med3_f32 v120, v120, s24, v237
	v_med3_f32 v121, v121, s24, v237
	v_med3_f32 v122, v122, s24, v237
	v_med3_f32 v123, v123, s24, v237
	v_med3_f32 v124, v124, s24, v237
	v_med3_f32 v125, v125, s24, v237
	v_med3_f32 v126, v126, s24, v237
	v_med3_f32 v127, v127, s24, v237
	v_med3_f32 v128, v128, s24, v237
	v_med3_f32 v129, v129, s24, v237
	v_cvt_pk_fp8_f32 v66, v66, v70
	v_cvt_pk_fp8_f32 v66, v74, v78 op_sel:[0,0,1]
	v_cvt_pk_fp8_f32 v70, v67, v71
	v_cvt_pk_fp8_f32 v70, v75, v79 op_sel:[0,0,1]
	v_cvt_pk_fp8_f32 v74, v68, v72
	v_cvt_pk_fp8_f32 v74, v76, v80 op_sel:[0,0,1]
	v_cvt_pk_fp8_f32 v78, v69, v73
	v_cvt_pk_fp8_f32 v78, v77, v81 op_sel:[0,0,1]
	v_cvt_pk_fp8_f32 v67, v82, v86
	v_cvt_pk_fp8_f32 v67, v90, v94 op_sel:[0,0,1]
	v_cvt_pk_fp8_f32 v71, v83, v87
	v_cvt_pk_fp8_f32 v71, v91, v95 op_sel:[0,0,1]
	v_cvt_pk_fp8_f32 v75, v84, v88
	v_cvt_pk_fp8_f32 v75, v92, v96 op_sel:[0,0,1]
	v_cvt_pk_fp8_f32 v79, v85, v89
	v_cvt_pk_fp8_f32 v79, v93, v97 op_sel:[0,0,1]
	v_cvt_pk_fp8_f32 v68, v98, v102
	v_cvt_pk_fp8_f32 v68, v106, v110 op_sel:[0,0,1]
	v_cvt_pk_fp8_f32 v72, v99, v103
	v_cvt_pk_fp8_f32 v72, v107, v111 op_sel:[0,0,1]
	v_cvt_pk_fp8_f32 v76, v100, v104
	v_cvt_pk_fp8_f32 v76, v108, v112 op_sel:[0,0,1]
	v_cvt_pk_fp8_f32 v80, v101, v105
	v_cvt_pk_fp8_f32 v80, v109, v113 op_sel:[0,0,1]
	v_cvt_pk_fp8_f32 v69, v114, v118
	v_cvt_pk_fp8_f32 v69, v122, v126 op_sel:[0,0,1]
	v_cvt_pk_fp8_f32 v73, v115, v119
	v_cvt_pk_fp8_f32 v73, v123, v127 op_sel:[0,0,1]
	v_cvt_pk_fp8_f32 v77, v116, v120
	v_cvt_pk_fp8_f32 v77, v124, v128 op_sel:[0,0,1]
	v_cvt_pk_fp8_f32 v81, v117, v121
	v_cvt_pk_fp8_f32 v81, v125, v129 op_sel:[0,0,1]
	global_store_dwordx4 v250, v[66:69], s[42:43] nt
	global_store_dwordx4 v250, v[70:73], s[42:43] offset:2048 nt
	global_store_dwordx4 v251, v[74:77], s[42:43] nt
	global_store_dwordx4 v251, v[78:81], s[42:43] offset:2048 nt
	s_add_u32 s42, s42, 0x800000
	s_addc_u32 s43, s43, 0
	global_load_dwordx4 v[66:69], v246, s[4:5] nt
	global_load_dwordx4 v[70:73], v247, s[4:5] nt
	global_load_dwordx4 v[74:77], v248, s[4:5] nt
	global_load_dwordx4 v[78:81], v249, s[4:5] nt
	global_load_dwordx4 v[82:85], v246, s[6:7] nt
	global_load_dwordx4 v[86:89], v247, s[6:7] nt
	global_load_dwordx4 v[90:93], v248, s[6:7] nt
	global_load_dwordx4 v[94:97], v249, s[6:7] nt
	global_load_dwordx4 v[98:101], v246, s[8:9] nt
	global_load_dwordx4 v[102:105], v247, s[8:9] nt
	global_load_dwordx4 v[106:109], v248, s[8:9] nt
	global_load_dwordx4 v[110:113], v249, s[8:9] nt
	global_load_dwordx4 v[114:117], v246, s[38:39] nt
	global_load_dwordx4 v[118:121], v247, s[38:39] nt
	global_load_dwordx4 v[122:125], v248, s[38:39] nt
	global_load_dwordx4 v[126:129], v249, s[38:39] nt
	s_add_u32 s4, s4, 0x2000000
	s_addc_u32 s5, s5, 0
	s_add_u32 s6, s6, 0x2000000
	s_addc_u32 s7, s7, 0
	s_add_u32 s8, s8, 0x2000000
	s_addc_u32 s9, s9, 0
	s_add_u32 s38, s38, 0x2000000
	s_addc_u32 s39, s39, 0
	s_waitcnt vmcnt(40)
; #define GAS __attribute__((address_space(1)))
; template <bool GAIN, bool NT = false> __device__ __forceinline__ void titem8_load(const TItem& d, int lane, f32x4 (&r)[16], f32x4 (&g)[4]) {
;     const int q = lane & 7, kg = lane >> 3; const unsigned lo = (unsigned)((16 * kg) * d.N + 4 * q) * 4u;
;     const GAS char* base = (const GAS char*)d.src;
; #pragma unroll
;     for (int j = 0; j < 16; ++j) { const GAS f32x4* p = (const GAS f32x4*)(base + (size_t)j * (size_t)d.N * 4 + lo); r[j] = NT ? __builtin_nontemporal_load(p) : *p; }
; template <bool GAIN, bool NT = false> __device__ __forceinline__ void titem8_store(const TItem& d, int lane, const f32x4 (&r)[16], const f32x4 (&g)[4]) {
;     const int q = lane & 7, kg = lane >> 3; const unsigned lo = (unsigned)((4 * q) * d.ldk + 16 * kg);
;     GAS char* base = (GAS char*)d.dst;
;     f32x4 s[16];
; #pragma unroll
;     for (int j = 0; j < 16; ++j) s[j] = r[j] * ((GAIN ? g[j >> 2][j & 3] : 1.0f) * W8_SCALE);
; #pragma unroll
;     for (int i = 0; i < 4; ++i) { v4u w;
;         w.x = pk4_fp8w(s[0][i], s[1][i], s[2][i], s[3][i]); w.y = pk4_fp8w(s[4][i], s[5][i], s[6][i], s[7][i]);
;         w.z = pk4_fp8w(s[8][i], s[9][i], s[10][i], s[11][i]); w.w = pk4_fp8w(s[12][i], s[13][i], s[14][i], s[15][i]);
;         GAS v4u* p = (GAS v4u*)(base + (size_t)i * (size_t)d.ldk + lo);
;         if (NT) __builtin_nontemporal_store(w, p); else *p = w; }
; }
	v_pk_mul_f32 v[130:131], v[130:131], s[30:31] op_sel_hi:[1,0]
	v_pk_mul_f32 v[132:133], v[132:133], s[30:31] op_sel_hi:[1,0]
	v_pk_mul_f32 v[134:135], v[134:135], s[30:31] op_sel_hi:[1,0]
	v_pk_mul_f32 v[136:137], v[136:137], s[30:31] op_sel_hi:[1,0]
	v_pk_mul_f32 v[138:139], v[138:139], s[30:31] op_sel_hi:[1,0]
	v_pk_mul_f32 v[140:141], v[140:141], s[30:31] op_sel_hi:[1,0]
	v_pk_mul_f32 v[142:143], v[142:143], s[30:31] op_sel_hi:[1,0]
	v_pk_mul_f32 v[144:145], v[144:145], s[30:31] op_sel_hi:[1,0]
	v_pk_mul_f32 v[146:147], v[146:147], s[30:31] op_sel_hi:[1,0]
	v_pk_mul_f32 v[148:149], v[148:149], s[30:31] op_sel_hi:[1,0]
	v_pk_mul_f32 v[150:151], v[150:151], s[30:31] op_sel_hi:[1,0]
	v_pk_mul_f32 v[152:153], v[152:153], s[30:31] op_sel_hi:[1,0]
	v_pk_mul_f32 v[154:155], v[154:155], s[30:31] op_sel_hi:[1,0]
	v_pk_mul_f32 v[156:157], v[156:157], s[30:31] op_sel_hi:[1,0]
	v_pk_mul_f32 v[158:159], v[158:159], s[30:31] op_sel_hi:[1,0]
	v_pk_mul_f32 v[160:161], v[160:161], s[30:31] op_sel_hi:[1,0]
	v_pk_mul_f32 v[162:163], v[162:163], s[30:31] op_sel_hi:[1,0]
	v_pk_mul_f32 v[164:165], v[164:165], s[30:31] op_sel_hi:[1,0]
	v_pk_mul_f32 v[166:167], v[166:167], s[30:31] op_sel_hi:[1,0]
	v_pk_mul_f32 v[168:169], v[168:169], s[30:31] op_sel_hi:[1,0]
	v_pk_mul_f32 v[170:171], v[170:171], s[30:31] op_sel_hi:[1,0]
	v_pk_mul_f32 v[172:173], v[172:173], s[30:31] op_sel_hi:[1,0]
	v_pk_mul_f32 v[174:175], v[174:175], s[30:31] op_sel_hi:[1,0]
	v_pk_mul_f32 v[176:177], v[176:177], s[30:31] op_sel_hi:[1,0]
	v_pk_mul_f32 v[178:179], v[178:179], s[30:31] op_sel_hi:[1,0]
	v_pk_mul_f32 v[180:181], v[180:181], s[30:31] op_sel_hi:[1,0]
	v_pk_mul_f32 v[182:183], v[182:183], s[30:31] op_sel_hi:[1,0]
	v_pk_mul_f32 v[184:185], v[184:185], s[30:31] op_sel_hi:[1,0]
	v_pk_mul_f32 v[186:187], v[186:187], s[30:31] op_sel_hi:[1,0]
	v_pk_mul_f32 v[188:189], v[188:189], s[30:31] op_sel_hi:[1,0]
	v_pk_mul_f32 v[190:191], v[190:191], s[30:31] op_sel_hi:[1,0]
	v_pk_mul_f32 v[192:193], v[192:193], s[30:31] op_sel_hi:[1,0]
	v_med3_f32 v130, v130, s24, v237
	v_med3_f32 v131, v131, s24, v237
	v_med3_f32 v132, v132, s24, v237
	v_med3_f32 v133, v133, s24, v237
	v_med3_f32 v134, v134, s24, v237
	v_med3_f32 v135, v135, s24, v237
	v_med3_f32 v136, v136, s24, v237
	v_med3_f32 v137, v137, s24, v237
	v_med3_f32 v138, v138, s24, v237
	v_med3_f32 v139, v139, s24, v237
	v_med3_f32 v140, v140, s24, v237
	v_med3_f32 v141, v141, s24, v237
	v_med3_f32 v142, v142, s24, v237
	v_med3_f32 v143, v143, s24, v237
	v_med3_f32 v144, v144, s24, v237
	v_med3_f32 v145, v145, s24, v237
	v_med3_f32 v146, v146, s24, v237
	v_med3_f32 v147, v147, s24, v237
	v_med3_f32 v148, v148, s24, v237
	v_med3_f32 v149, v149, s24, v237
	v_med3_f32 v150, v150, s24, v237
	v_med3_f32 v151, v151, s24, v237
	v_med3_f32 v152, v152, s24, v237
	v_med3_f32 v153, v153, s24, v237
	v_med3_f32 v154, v154, s24, v237
	v_med3_f32 v155, v155, s24, v237
	v_med3_f32 v156, v156, s24, v237
	v_med3_f32 v157, v157, s24, v237
	v_med3_f32 v158, v158, s24, v237
	v_med3_f32 v159, v159, s24, v237
	v_med3_f32 v160, v160, s24, v237
	v_med3_f32 v161, v161, s24, v237
	v_med3_f32 v162, v162, s24, v237
	v_med3_f32 v163, v163, s24, v237
	v_med3_f32 v164, v164, s24, v237
	v_med3_f32 v165, v165, s24, v237
	v_med3_f32 v166, v166, s24, v237
	v_med3_f32 v167, v167, s24, v237
	v_med3_f32 v168, v168, s24, v237
	v_med3_f32 v169, v169, s24, v237
	v_med3_f32 v170, v170, s24, v237
	v_med3_f32 v171, v171, s24, v237
	v_med3_f32 v172, v172, s24, v237
	v_med3_f32 v173, v173, s24, v237
	v_med3_f32 v174, v174, s24, v237
	v_med3_f32 v175, v175, s24, v237
	v_med3_f32 v176, v176, s24, v237
	v_med3_f32 v177, v177, s24, v237
	v_med3_f32 v178, v178, s24, v237
	v_med3_f32 v179, v179, s24, v237
	v_med3_f32 v180, v180, s24, v237
	v_med3_f32 v181, v181, s24, v237
	v_med3_f32 v182, v182, s24, v237
	v_med3_f32 v183, v183, s24, v237
	v_med3_f32 v184, v184, s24, v237
	v_med3_f32 v185, v185, s24, v237
	v_med3_f32 v186, v186, s24, v237
	v_med3_f32 v187, v187, s24, v237
	v_med3_f32 v188, v188, s24, v237
	v_med3_f32 v189, v189, s24, v237
	v_med3_f32 v190, v190, s24, v237
	v_med3_f32 v191, v191, s24, v237
	v_med3_f32 v192, v192, s24, v237
	v_med3_f32 v193, v193, s24, v237
	v_cvt_pk_fp8_f32 v130, v130, v134
	v_cvt_pk_fp8_f32 v130, v138, v142 op_sel:[0,0,1]
	v_cvt_pk_fp8_f32 v134, v131, v135
	v_cvt_pk_fp8_f32 v134, v139, v143 op_sel:[0,0,1]
	v_cvt_pk_fp8_f32 v138, v132, v136
	v_cvt_pk_fp8_f32 v138, v140, v144 op_sel:[0,0,1]
	v_cvt_pk_fp8_f32 v142, v133, v137
	v_cvt_pk_fp8_f32 v142, v141, v145 op_sel:[0,0,1]
	v_cvt_pk_fp8_f32 v131, v146, v150
	v_cvt_pk_fp8_f32 v131, v154, v158 op_sel:[0,0,1]
	v_cvt_pk_fp8_f32 v135, v147, v151
	v_cvt_pk_fp8_f32 v135, v155, v159 op_sel:[0,0,1]
	v_cvt_pk_fp8_f32 v139, v148, v152
	v_cvt_pk_fp8_f32 v139, v156, v160 op_sel:[0,0,1]
	v_cvt_pk_fp8_f32 v143, v149, v153
	v_cvt_pk_fp8_f32 v143, v157, v161 op_sel:[0,0,1]
	v_cvt_pk_fp8_f32 v132, v162, v166
	v_cvt_pk_fp8_f32 v132, v170, v174 op_sel:[0,0,1]
	v_cvt_pk_fp8_f32 v136, v163, v167
	v_cvt_pk_fp8_f32 v136, v171, v175 op_sel:[0,0,1]
	v_cvt_pk_fp8_f32 v140, v164, v168
	v_cvt_pk_fp8_f32 v140, v172, v176 op_sel:[0,0,1]
	v_cvt_pk_fp8_f32 v144, v165, v169
	v_cvt_pk_fp8_f32 v144, v173, v177 op_sel:[0,0,1]
	v_cvt_pk_fp8_f32 v133, v178, v182
	v_cvt_pk_fp8_f32 v133, v186, v190 op_sel:[0,0,1]
	v_cvt_pk_fp8_f32 v137, v179, v183
	v_cvt_pk_fp8_f32 v137, v187, v191 op_sel:[0,0,1]
	v_cvt_pk_fp8_f32 v141, v180, v184
	v_cvt_pk_fp8_f32 v141, v188, v192 op_sel:[0,0,1]
	v_cvt_pk_fp8_f32 v145, v181, v185
	v_cvt_pk_fp8_f32 v145, v189, v193 op_sel:[0,0,1]
	global_store_dwordx4 v250, v[130:133], s[42:43] nt
	global_store_dwordx4 v250, v[134:137], s[42:43] offset:2048 nt
	global_store_dwordx4 v251, v[138:141], s[42:43] nt
	global_store_dwordx4 v251, v[142:145], s[42:43] offset:2048 nt
	s_add_u32 s42, s42, 0x800000
	s_addc_u32 s43, s43, 0
	global_load_dwordx4 v[130:133], v246, s[4:5] nt
	global_load_dwordx4 v[134:137], v247, s[4:5] nt
	global_load_dwordx4 v[138:141], v248, s[4:5] nt
	global_load_dwordx4 v[142:145], v249, s[4:5] nt
	global_load_dwordx4 v[146:149], v246, s[6:7] nt
	global_load_dwordx4 v[150:153], v247, s[6:7] nt
	global_load_dwordx4 v[154:157], v248, s[6:7] nt
	global_load_dwordx4 v[158:161], v249, s[6:7] nt
	global_load_dwordx4 v[162:165], v246, s[8:9] nt
	global_load_dwordx4 v[166:169], v247, s[8:9] nt
	global_load_dwordx4 v[170:173], v248, s[8:9] nt
	global_load_dwordx4 v[174:177], v249, s[8:9] nt
	global_load_dwordx4 v[178:181], v246, s[38:39] nt
	global_load_dwordx4 v[182:185], v247, s[38:39] nt
	global_load_dwordx4 v[186:189], v248, s[38:39] nt
	global_load_dwordx4 v[190:193], v249, s[38:39] nt
	s_add_u32 s4, s4, 0x2000000
	s_addc_u32 s5, s5, 0
	s_add_u32 s6, s6, 0x2000000
	s_addc_u32 s7, s7, 0
	s_add_u32 s8, s8, 0x2000000
	s_addc_u32 s9, s9, 0
	s_add_u32 s38, s38, 0x2000000
	s_addc_u32 s39, s39, 0
	s_waitcnt vmcnt(40)
; #define GAS __attribute__((address_space(1)))
; template <bool GAIN, bool NT = false> __device__ __forceinline__ void titem8_load(const TItem& d, int lane, f32x4 (&r)[16], f32x4 (&g)[4]) {
;     const int q = lane & 7, kg = lane >> 3; const unsigned lo = (unsigned)((16 * kg) * d.N + 4 * q) * 4u;
;     const GAS char* base = (const GAS char*)d.src;
; #pragma unroll
;     for (int j = 0; j < 16; ++j) { const GAS f32x4* p = (const GAS f32x4*)(base + (size_t)j * (size_t)d.N * 4 + lo); r[j] = NT ? __builtin_nontemporal_load(p) : *p; }
; template <bool GAIN, bool NT = false> __device__ __forceinline__ void titem8_store(const TItem& d, int lane, const f32x4 (&r)[16], const f32x4 (&g)[4]) {
;     const int q = lane & 7, kg = lane >> 3; const unsigned lo = (unsigned)((4 * q) * d.ldk + 16 * kg);
;     GAS char* base = (GAS char*)d.dst;
;     f32x4 s[16];
; #pragma unroll
;     for (int j = 0; j < 16; ++j) s[j] = r[j] * ((GAIN ? g[j >> 2][j & 3] : 1.0f) * W8_SCALE);
; #pragma unroll
;     for (int i = 0; i < 4; ++i) { v4u w;
;         w.x = pk4_fp8w(s[0][i], s[1][i], s[2][i], s[3][i]); w.y = pk4_fp8w(s[4][i], s[5][i], s[6][i], s[7][i]);
;         w.z = pk4_fp8w(s[8][i], s[9][i], s[10][i], s[11][i]); w.w = pk4_fp8w(s[12][i], s[13][i], s[14][i], s[15][i]);
;         GAS v4u* p = (GAS v4u*)(base + (size_t)i * (size_t)d.ldk + lo);
;         if (NT) __builtin_nontemporal_store(w, p); else *p = w; }
; }
	v_pk_mul_f32 v[0:1], v[0:1], s[30:31] op_sel_hi:[1,0]
	v_pk_mul_f32 v[2:3], v[2:3], s[30:31] op_sel_hi:[1,0]
	v_pk_mul_f32 v[4:5], v[4:5], s[30:31] op_sel_hi:[1,0]
	v_pk_mul_f32 v[6:7], v[6:7], s[30:31] op_sel_hi:[1,0]
	v_pk_mul_f32 v[8:9], v[8:9], s[30:31] op_sel_hi:[1,0]
	v_pk_mul_f32 v[10:11], v[10:11], s[30:31] op_sel_hi:[1,0]
	v_pk_mul_f32 v[12:13], v[12:13], s[30:31] op_sel_hi:[1,0]
	v_pk_mul_f32 v[14:15], v[14:15], s[30:31] op_sel_hi:[1,0]
	v_pk_mul_f32 v[16:17], v[16:17], s[30:31] op_sel_hi:[1,0]
	v_pk_mul_f32 v[18:19], v[18:19], s[30:31] op_sel_hi:[1,0]
	v_pk_mul_f32 v[20:21], v[20:21], s[30:31] op_sel_hi:[1,0]
	v_pk_mul_f32 v[22:23], v[22:23], s[30:31] op_sel_hi:[1,0]
	v_pk_mul_f32 v[24:25], v[24:25], s[30:31] op_sel_hi:[1,0]
	v_pk_mul_f32 v[26:27], v[26:27], s[30:31] op_sel_hi:[1,0]
	v_pk_mul_f32 v[28:29], v[28:29], s[30:31] op_sel_hi:[1,0]
	v_pk_mul_f32 v[30:31], v[30:31], s[30:31] op_sel_hi:[1,0]
	v_pk_mul_f32 v[32:33], v[32:33], s[30:31] op_sel_hi:[1,0]
	v_pk_mul_f32 v[34:35], v[34:35], s[30:31] op_sel_hi:[1,0]
	v_pk_mul_f32 v[36:37], v[36:37], s[30:31] op_sel_hi:[1,0]
	v_pk_mul_f32 v[38:39], v[38:39], s[30:31] op_sel_hi:[1,0]
	v_pk_mul_f32 v[40:41], v[40:41], s[30:31] op_sel_hi:[1,0]
	v_pk_mul_f32 v[42:43], v[42:43], s[30:31] op_sel_hi:[1,0]
	v_pk_mul_f32 v[44:45], v[44:45], s[30:31] op_sel_hi:[1,0]
	v_pk_mul_f32 v[46:47], v[46:47], s[30:31] op_sel_hi:[1,0]
	v_pk_mul_f32 v[48:49], v[48:49], s[30:31] op_sel_hi:[1,0]
	v_pk_mul_f32 v[50:51], v[50:51], s[30:31] op_sel_hi:[1,0]
	v_pk_mul_f32 v[52:53], v[52:53], s[30:31] op_sel_hi:[1,0]
	v_pk_mul_f32 v[54:55], v[54:55], s[30:31] op_sel_hi:[1,0]
	v_pk_mul_f32 v[56:57], v[56:57], s[30:31] op_sel_hi:[1,0]
	v_pk_mul_f32 v[58:59], v[58:59], s[30:31] op_sel_hi:[1,0]
	v_pk_mul_f32 v[60:61], v[60:61], s[30:31] op_sel_hi:[1,0]
	v_pk_mul_f32 v[62:63], v[62:63], s[30:31] op_sel_hi:[1,0]
	v_med3_f32 v0, v0, s24, v237
	v_med3_f32 v1, v1, s24, v237
	v_med3_f32 v2, v2, s24, v237
	v_med3_f32 v3, v3, s24, v237
	v_med3_f32 v4, v4, s24, v237
	v_med3_f32 v5, v5, s24, v237
	v_med3_f32 v6, v6, s24, v237
	v_med3_f32 v7, v7, s24, v237
	v_med3_f32 v8, v8, s24, v237
	v_med3_f32 v9, v9, s24, v237
	v_med3_f32 v10, v10, s24, v237
	v_med3_f32 v11, v11, s24, v237
	v_med3_f32 v12, v12, s24, v237
	v_med3_f32 v13, v13, s24, v237
	v_med3_f32 v14, v14, s24, v237
	v_med3_f32 v15, v15, s24, v237
	v_med3_f32 v16, v16, s24, v237
	v_med3_f32 v17, v17, s24, v237
	v_med3_f32 v18, v18, s24, v237
	v_med3_f32 v19, v19, s24, v237
	v_med3_f32 v20, v20, s24, v237
	v_med3_f32 v21, v21, s24, v237
	v_med3_f32 v22, v22, s24, v237
	v_med3_f32 v23, v23, s24, v237
	v_med3_f32 v24, v24, s24, v237
	v_med3_f32 v25, v25, s24, v237
	v_med3_f32 v26, v26, s24, v237
	v_med3_f32 v27, v27, s24, v237
	v_med3_f32 v28, v28, s24, v237
	v_med3_f32 v29, v29, s24, v237
	v_med3_f32 v30, v30, s24, v237
	v_med3_f32 v31, v31, s24, v237
	v_med3_f32 v32, v32, s24, v237
	v_med3_f32 v33, v33, s24, v237
	v_med3_f32 v34, v34, s24, v237
	v_med3_f32 v35, v35, s24, v237
	v_med3_f32 v36, v36, s24, v237
	v_med3_f32 v37, v37, s24, v237
	v_med3_f32 v38, v38, s24, v237
	v_med3_f32 v39, v39, s24, v237
	v_med3_f32 v40, v40, s24, v237
	v_med3_f32 v41, v41, s24, v237
	v_med3_f32 v42, v42, s24, v237
	v_med3_f32 v43, v43, s24, v237
	v_med3_f32 v44, v44, s24, v237
	v_med3_f32 v45, v45, s24, v237
	v_med3_f32 v46, v46, s24, v237
	v_med3_f32 v47, v47, s24, v237
	v_med3_f32 v48, v48, s24, v237
	v_med3_f32 v49, v49, s24, v237
	v_med3_f32 v50, v50, s24, v237
	v_med3_f32 v51, v51, s24, v237
	v_med3_f32 v52, v52, s24, v237
	v_med3_f32 v53, v53, s24, v237
	v_med3_f32 v54, v54, s24, v237
	v_med3_f32 v55, v55, s24, v237
	v_med3_f32 v56, v56, s24, v237
	v_med3_f32 v57, v57, s24, v237
	v_med3_f32 v58, v58, s24, v237
	v_med3_f32 v59, v59, s24, v237
	v_med3_f32 v60, v60, s24, v237
	v_med3_f32 v61, v61, s24, v237
	v_med3_f32 v62, v62, s24, v237
	v_med3_f32 v63, v63, s24, v237
	v_cvt_pk_fp8_f32 v0, v0, v4
	v_cvt_pk_fp8_f32 v0, v8, v12 op_sel:[0,0,1]
	v_cvt_pk_fp8_f32 v4, v1, v5
	v_cvt_pk_fp8_f32 v4, v9, v13 op_sel:[0,0,1]
	v_cvt_pk_fp8_f32 v8, v2, v6
	v_cvt_pk_fp8_f32 v8, v10, v14 op_sel:[0,0,1]
	v_cvt_pk_fp8_f32 v12, v3, v7
	v_cvt_pk_fp8_f32 v12, v11, v15 op_sel:[0,0,1]
	v_cvt_pk_fp8_f32 v1, v16, v20
	v_cvt_pk_fp8_f32 v1, v24, v28 op_sel:[0,0,1]
	v_cvt_pk_fp8_f32 v5, v17, v21
	v_cvt_pk_fp8_f32 v5, v25, v29 op_sel:[0,0,1]
	v_cvt_pk_fp8_f32 v9, v18, v22
	v_cvt_pk_fp8_f32 v9, v26, v30 op_sel:[0,0,1]
	v_cvt_pk_fp8_f32 v13, v19, v23
	v_cvt_pk_fp8_f32 v13, v27, v31 op_sel:[0,0,1]
	v_cvt_pk_fp8_f32 v2, v32, v36
	v_cvt_pk_fp8_f32 v2, v40, v44 op_sel:[0,0,1]
	v_cvt_pk_fp8_f32 v6, v33, v37
	v_cvt_pk_fp8_f32 v6, v41, v45 op_sel:[0,0,1]
	v_cvt_pk_fp8_f32 v10, v34, v38
	v_cvt_pk_fp8_f32 v10, v42, v46 op_sel:[0,0,1]
	v_cvt_pk_fp8_f32 v14, v35, v39
	v_cvt_pk_fp8_f32 v14, v43, v47 op_sel:[0,0,1]
	v_cvt_pk_fp8_f32 v3, v48, v52
	v_cvt_pk_fp8_f32 v3, v56, v60 op_sel:[0,0,1]
	v_cvt_pk_fp8_f32 v7, v49, v53
	v_cvt_pk_fp8_f32 v7, v57, v61 op_sel:[0,0,1]
	v_cvt_pk_fp8_f32 v11, v50, v54
	v_cvt_pk_fp8_f32 v11, v58, v62 op_sel:[0,0,1]
	v_cvt_pk_fp8_f32 v15, v51, v55
	v_cvt_pk_fp8_f32 v15, v59, v63 op_sel:[0,0,1]
	global_store_dwordx4 v250, v[0:3], s[42:43] nt
	global_store_dwordx4 v250, v[4:7], s[42:43] offset:2048 nt
	global_store_dwordx4 v251, v[8:11], s[42:43] nt
	global_store_dwordx4 v251, v[12:15], s[42:43] offset:2048 nt
	s_add_u32 s42, s42, 0x800000
	s_addc_u32 s43, s43, 0
	global_load_dwordx4 v[0:3], v246, s[4:5] nt
	global_load_dwordx4 v[4:7], v247, s[4:5] nt
	global_load_dwordx4 v[8:11], v248, s[4:5] nt
	global_load_dwordx4 v[12:15], v249, s[4:5] nt
	global_load_dwordx4 v[16:19], v246, s[6:7] nt
	global_load_dwordx4 v[20:23], v247, s[6:7] nt
	global_load_dwordx4 v[24:27], v248, s[6:7] nt
	global_load_dwordx4 v[28:31], v249, s[6:7] nt
	global_load_dwordx4 v[32:35], v246, s[8:9] nt
	global_load_dwordx4 v[36:39], v247, s[8:9] nt
	global_load_dwordx4 v[40:43], v248, s[8:9] nt
	global_load_dwordx4 v[44:47], v249, s[8:9] nt
	global_load_dwordx4 v[48:51], v246, s[38:39] nt
	global_load_dwordx4 v[52:55], v247, s[38:39] nt
	global_load_dwordx4 v[56:59], v248, s[38:39] nt
	global_load_dwordx4 v[60:63], v249, s[38:39] nt
	s_add_u32 s4, s4, 0x2000000
	s_addc_u32 s5, s5, 0
	s_add_u32 s6, s6, 0x2000000
	s_addc_u32 s7, s7, 0
	s_add_u32 s8, s8, 0x2000000
	s_addc_u32 s9, s9, 0
	s_add_u32 s38, s38, 0x2000000
	s_addc_u32 s39, s39, 0
	s_waitcnt vmcnt(40)
; #define GAS __attribute__((address_space(1)))
; template <bool GAIN, bool NT = false> __device__ __forceinline__ void titem8_store(const TItem& d, int lane, const f32x4 (&r)[16], const f32x4 (&g)[4]) {
;     const int q = lane & 7, kg = lane >> 3; const unsigned lo = (unsigned)((4 * q) * d.ldk + 16 * kg);
;     GAS char* base = (GAS char*)d.dst;
;     f32x4 s[16];
; #pragma unroll
;     for (int j = 0; j < 16; ++j) s[j] = r[j] * ((GAIN ? g[j >> 2][j & 3] : 1.0f) * W8_SCALE);
; #pragma unroll
;     for (int i = 0; i < 4; ++i) { v4u w;
;         w.x = pk4_fp8w(s[0][i], s[1][i], s[2][i], s[3][i]); w.y = pk4_fp8w(s[4][i], s[5][i], s[6][i], s[7][i]);
;         w.z = pk4_fp8w(s[8][i], s[9][i], s[10][i], s[11][i]); w.w = pk4_fp8w(s[12][i], s[13][i], s[14][i], s[15][i]);
;         GAS v4u* p = (GAS v4u*)(base + (size_t)i * (size_t)d.ldk + lo);
;         if (NT) __builtin_nontemporal_store(w, p); else *p = w; }
; }
	v_pk_mul_f32 v[66:67], v[66:67], s[30:31] op_sel_hi:[1,0]
	v_pk_mul_f32 v[68:69], v[68:69], s[30:31] op_sel_hi:[1,0]
	v_pk_mul_f32 v[70:71], v[70:71], s[30:31] op_sel_hi:[1,0]
	v_pk_mul_f32 v[72:73], v[72:73], s[30:31] op_sel_hi:[1,0]
	v_pk_mul_f32 v[74:75], v[74:75], s[30:31] op_sel_hi:[1,0]
	v_pk_mul_f32 v[76:77], v[76:77], s[30:31] op_sel_hi:[1,0]
	v_pk_mul_f32 v[78:79], v[78:79], s[30:31] op_sel_hi:[1,0]
	v_pk_mul_f32 v[80:81], v[80:81], s[30:31] op_sel_hi:[1,0]
	v_pk_mul_f32 v[82:83], v[82:83], s[30:31] op_sel_hi:[1,0]
	v_pk_mul_f32 v[84:85], v[84:85], s[30:31] op_sel_hi:[1,0]
	v_pk_mul_f32 v[86:87], v[86:87], s[30:31] op_sel_hi:[1,0]
	v_pk_mul_f32 v[88:89], v[88:89], s[30:31] op_sel_hi:[1,0]
	v_pk_mul_f32 v[90:91], v[90:91], s[30:31] op_sel_hi:[1,0]
	v_pk_mul_f32 v[92:93], v[92:93], s[30:31] op_sel_hi:[1,0]
	v_pk_mul_f32 v[94:95], v[94:95], s[30:31] op_sel_hi:[1,0]
	v_pk_mul_f32 v[96:97], v[96:97], s[30:31] op_sel_hi:[1,0]
	v_pk_mul_f32 v[98:99], v[98:99], s[30:31] op_sel_hi:[1,0]
	v_pk_mul_f32 v[100:101], v[100:101], s[30:31] op_sel_hi:[1,0]
	v_pk_mul_f32 v[102:103], v[102:103], s[30:31] op_sel_hi:[1,0]
	v_pk_mul_f32 v[104:105], v[104:105], s[30:31] op_sel_hi:[1,0]
	v_pk_mul_f32 v[106:107], v[106:107], s[30:31] op_sel_hi:[1,0]
	v_pk_mul_f32 v[108:109], v[108:109], s[30:31] op_sel_hi:[1,0]
	v_pk_mul_f32 v[110:111], v[110:111], s[30:31] op_sel_hi:[1,0]
	v_pk_mul_f32 v[112:113], v[112:113], s[30:31] op_sel_hi:[1,0]
	v_pk_mul_f32 v[114:115], v[114:115], s[30:31] op_sel_hi:[1,0]
	v_pk_mul_f32 v[116:117], v[116:117], s[30:31] op_sel_hi:[1,0]
	v_pk_mul_f32 v[118:119], v[118:119], s[30:31] op_sel_hi:[1,0]
	v_pk_mul_f32 v[120:121], v[120:121], s[30:31] op_sel_hi:[1,0]
	v_pk_mul_f32 v[122:123], v[122:123], s[30:31] op_sel_hi:[1,0]
	v_pk_mul_f32 v[124:125], v[124:125], s[30:31] op_sel_hi:[1,0]
	v_pk_mul_f32 v[126:127], v[126:127], s[30:31] op_sel_hi:[1,0]
	v_pk_mul_f32 v[128:129], v[128:129], s[30:31] op_sel_hi:[1,0]
	v_med3_f32 v66, v66, s24, v237
	v_med3_f32 v67, v67, s24, v237
	v_med3_f32 v68, v68, s24, v237
	v_med3_f32 v69, v69, s24, v237
	v_med3_f32 v70, v70, s24, v237
	v_med3_f32 v71, v71, s24, v237
	v_med3_f32 v72, v72, s24, v237
	v_med3_f32 v73, v73, s24, v237
	v_med3_f32 v74, v74, s24, v237
	v_med3_f32 v75, v75, s24, v237
	v_med3_f32 v76, v76, s24, v237
	v_med3_f32 v77, v77, s24, v237
	v_med3_f32 v78, v78, s24, v237
	v_med3_f32 v79, v79, s24, v237
	v_med3_f32 v80, v80, s24, v237
	v_med3_f32 v81, v81, s24, v237
	v_med3_f32 v82, v82, s24, v237
	v_med3_f32 v83, v83, s24, v237
	v_med3_f32 v84, v84, s24, v237
	v_med3_f32 v85, v85, s24, v237
	v_med3_f32 v86, v86, s24, v237
	v_med3_f32 v87, v87, s24, v237
	v_med3_f32 v88, v88, s24, v237
	v_med3_f32 v89, v89, s24, v237
	v_med3_f32 v90, v90, s24, v237
	v_med3_f32 v91, v91, s24, v237
	v_med3_f32 v92, v92, s24, v237
	v_med3_f32 v93, v93, s24, v237
	v_med3_f32 v94, v94, s24, v237
	v_med3_f32 v95, v95, s24, v237
	v_med3_f32 v96, v96, s24, v237
	v_med3_f32 v97, v97, s24, v237
	v_med3_f32 v98, v98, s24, v237
	v_med3_f32 v99, v99, s24, v237
	v_med3_f32 v100, v100, s24, v237
	v_med3_f32 v101, v101, s24, v237
	v_med3_f32 v102, v102, s24, v237
	v_med3_f32 v103, v103, s24, v237
	v_med3_f32 v104, v104, s24, v237
	v_med3_f32 v105, v105, s24, v237
	v_med3_f32 v106, v106, s24, v237
	v_med3_f32 v107, v107, s24, v237
	v_med3_f32 v108, v108, s24, v237
	v_med3_f32 v109, v109, s24, v237
	v_med3_f32 v110, v110, s24, v237
	v_med3_f32 v111, v111, s24, v237
	v_med3_f32 v112, v112, s24, v237
	v_med3_f32 v113, v113, s24, v237
	v_med3_f32 v114, v114, s24, v237
	v_med3_f32 v115, v115, s24, v237
	v_med3_f32 v116, v116, s24, v237
	v_med3_f32 v117, v117, s24, v237
	v_med3_f32 v118, v118, s24, v237
	v_med3_f32 v119, v119, s24, v237
	v_med3_f32 v120, v120, s24, v237
	v_med3_f32 v121, v121, s24, v237
	v_med3_f32 v122, v122, s24, v237
	v_med3_f32 v123, v123, s24, v237
	v_med3_f32 v124, v124, s24, v237
	v_med3_f32 v125, v125, s24, v237
	v_med3_f32 v126, v126, s24, v237
	v_med3_f32 v127, v127, s24, v237
	v_med3_f32 v128, v128, s24, v237
	v_med3_f32 v129, v129, s24, v237
	v_cvt_pk_fp8_f32 v66, v66, v70
	v_cvt_pk_fp8_f32 v66, v74, v78 op_sel:[0,0,1]
	v_cvt_pk_fp8_f32 v70, v67, v71
	v_cvt_pk_fp8_f32 v70, v75, v79 op_sel:[0,0,1]
	v_cvt_pk_fp8_f32 v74, v68, v72
	v_cvt_pk_fp8_f32 v74, v76, v80 op_sel:[0,0,1]
	v_cvt_pk_fp8_f32 v78, v69, v73
	v_cvt_pk_fp8_f32 v78, v77, v81 op_sel:[0,0,1]
	v_cvt_pk_fp8_f32 v67, v82, v86
	v_cvt_pk_fp8_f32 v67, v90, v94 op_sel:[0,0,1]
	v_cvt_pk_fp8_f32 v71, v83, v87
	v_cvt_pk_fp8_f32 v71, v91, v95 op_sel:[0,0,1]
	v_cvt_pk_fp8_f32 v75, v84, v88
	v_cvt_pk_fp8_f32 v75, v92, v96 op_sel:[0,0,1]
	v_cvt_pk_fp8_f32 v79, v85, v89
	v_cvt_pk_fp8_f32 v79, v93, v97 op_sel:[0,0,1]
	v_cvt_pk_fp8_f32 v68, v98, v102
	v_cvt_pk_fp8_f32 v68, v106, v110 op_sel:[0,0,1]
	v_cvt_pk_fp8_f32 v72, v99, v103
	v_cvt_pk_fp8_f32 v72, v107, v111 op_sel:[0,0,1]
	v_cvt_pk_fp8_f32 v76, v100, v104
	v_cvt_pk_fp8_f32 v76, v108, v112 op_sel:[0,0,1]
	v_cvt_pk_fp8_f32 v80, v101, v105
	v_cvt_pk_fp8_f32 v80, v109, v113 op_sel:[0,0,1]
	v_cvt_pk_fp8_f32 v69, v114, v118
	v_cvt_pk_fp8_f32 v69, v122, v126 op_sel:[0,0,1]
	v_cvt_pk_fp8_f32 v73, v115, v119
	v_cvt_pk_fp8_f32 v73, v123, v127 op_sel:[0,0,1]
	v_cvt_pk_fp8_f32 v77, v116, v120
	v_cvt_pk_fp8_f32 v77, v124, v128 op_sel:[0,0,1]
	v_cvt_pk_fp8_f32 v81, v117, v121
	v_cvt_pk_fp8_f32 v81, v125, v129 op_sel:[0,0,1]
	global_store_dwordx4 v250, v[66:69], s[42:43] nt
	global_store_dwordx4 v250, v[70:73], s[42:43] offset:2048 nt
	global_store_dwordx4 v251, v[74:77], s[42:43] nt
	global_store_dwordx4 v251, v[78:81], s[42:43] offset:2048 nt
	s_add_u32 s42, s42, 0x800000
	s_addc_u32 s43, s43, 0
	s_waitcnt vmcnt(24)
; #define GAS __attribute__((address_space(1)))
; template <bool GAIN, bool NT = false> __device__ __forceinline__ void titem8_store(const TItem& d, int lane, const f32x4 (&r)[16], const f32x4 (&g)[4]) {
;     const int q = lane & 7, kg = lane >> 3; const unsigned lo = (unsigned)((4 * q) * d.ldk + 16 * kg);
;     GAS char* base = (GAS char*)d.dst;
;     f32x4 s[16];
; #pragma unroll
;     for (int j = 0; j < 16; ++j) s[j] = r[j] * ((GAIN ? g[j >> 2][j & 3] : 1.0f) * W8_SCALE);
; #pragma unroll
;     for (int i = 0; i < 4; ++i) { v4u w;
;         w.x = pk4_fp8w(s[0][i], s[1][i], s[2][i], s[3][i]); w.y = pk4_fp8w(s[4][i], s[5][i], s[6][i], s[7][i]);
;         w.z = pk4_fp8w(s[8][i], s[9][i], s[10][i], s[11][i]); w.w = pk4_fp8w(s[12][i], s[13][i], s[14][i], s[15][i]);
;         GAS v4u* p = (GAS v4u*)(base + (size_t)i * (size_t)d.ldk + lo);
;         if (NT) __builtin_nontemporal_store(w, p); else *p = w; }
; }
	v_pk_mul_f32 v[130:131], v[130:131], s[30:31] op_sel_hi:[1,0]
	v_pk_mul_f32 v[132:133], v[132:133], s[30:31] op_sel_hi:[1,0]
	v_pk_mul_f32 v[134:135], v[134:135], s[30:31] op_sel_hi:[1,0]
	v_pk_mul_f32 v[136:137], v[136:137], s[30:31] op_sel_hi:[1,0]
	v_pk_mul_f32 v[138:139], v[138:139], s[30:31] op_sel_hi:[1,0]
	v_pk_mul_f32 v[140:141], v[140:141], s[30:31] op_sel_hi:[1,0]
	v_pk_mul_f32 v[142:143], v[142:143], s[30:31] op_sel_hi:[1,0]
	v_pk_mul_f32 v[144:145], v[144:145], s[30:31] op_sel_hi:[1,0]
	v_pk_mul_f32 v[146:147], v[146:147], s[30:31] op_sel_hi:[1,0]
	v_pk_mul_f32 v[148:149], v[148:149], s[30:31] op_sel_hi:[1,0]
	v_pk_mul_f32 v[150:151], v[150:151], s[30:31] op_sel_hi:[1,0]
	v_pk_mul_f32 v[152:153], v[152:153], s[30:31] op_sel_hi:[1,0]
	v_pk_mul_f32 v[154:155], v[154:155], s[30:31] op_sel_hi:[1,0]
	v_pk_mul_f32 v[156:157], v[156:157], s[30:31] op_sel_hi:[1,0]
	v_pk_mul_f32 v[158:159], v[158:159], s[30:31] op_sel_hi:[1,0]
	v_pk_mul_f32 v[160:161], v[160:161], s[30:31] op_sel_hi:[1,0]
	v_pk_mul_f32 v[162:163], v[162:163], s[30:31] op_sel_hi:[1,0]
	v_pk_mul_f32 v[164:165], v[164:165], s[30:31] op_sel_hi:[1,0]
	v_pk_mul_f32 v[166:167], v[166:167], s[30:31] op_sel_hi:[1,0]
	v_pk_mul_f32 v[168:169], v[168:169], s[30:31] op_sel_hi:[1,0]
	v_pk_mul_f32 v[170:171], v[170:171], s[30:31] op_sel_hi:[1,0]
	v_pk_mul_f32 v[172:173], v[172:173], s[30:31] op_sel_hi:[1,0]
	v_pk_mul_f32 v[174:175], v[174:175], s[30:31] op_sel_hi:[1,0]
	v_pk_mul_f32 v[176:177], v[176:177], s[30:31] op_sel_hi:[1,0]
	v_pk_mul_f32 v[178:179], v[178:179], s[30:31] op_sel_hi:[1,0]
	v_pk_mul_f32 v[180:181], v[180:181], s[30:31] op_sel_hi:[1,0]
	v_pk_mul_f32 v[182:183], v[182:183], s[30:31] op_sel_hi:[1,0]
	v_pk_mul_f32 v[184:185], v[184:185], s[30:31] op_sel_hi:[1,0]
	v_pk_mul_f32 v[186:187], v[186:187], s[30:31] op_sel_hi:[1,0]
	v_pk_mul_f32 v[188:189], v[188:189], s[30:31] op_sel_hi:[1,0]
	v_pk_mul_f32 v[190:191], v[190:191], s[30:31] op_sel_hi:[1,0]
	v_pk_mul_f32 v[192:193], v[192:193], s[30:31] op_sel_hi:[1,0]
	v_med3_f32 v130, v130, s24, v237
	v_med3_f32 v131, v131, s24, v237
	v_med3_f32 v132, v132, s24, v237
	v_med3_f32 v133, v133, s24, v237
	v_med3_f32 v134, v134, s24, v237
	v_med3_f32 v135, v135, s24, v237
	v_med3_f32 v136, v136, s24, v237
	v_med3_f32 v137, v137, s24, v237
	v_med3_f32 v138, v138, s24, v237
	v_med3_f32 v139, v139, s24, v237
	v_med3_f32 v140, v140, s24, v237
	v_med3_f32 v141, v141, s24, v237
	v_med3_f32 v142, v142, s24, v237
	v_med3_f32 v143, v143, s24, v237
	v_med3_f32 v144, v144, s24, v237
	v_med3_f32 v145, v145, s24, v237
	v_med3_f32 v146, v146, s24, v237
	v_med3_f32 v147, v147, s24, v237
	v_med3_f32 v148, v148, s24, v237
	v_med3_f32 v149, v149, s24, v237
	v_med3_f32 v150, v150, s24, v237
	v_med3_f32 v151, v151, s24, v237
	v_med3_f32 v152, v152, s24, v237
	v_med3_f32 v153, v153, s24, v237
	v_med3_f32 v154, v154, s24, v237
	v_med3_f32 v155, v155, s24, v237
	v_med3_f32 v156, v156, s24, v237
	v_med3_f32 v157, v157, s24, v237
	v_med3_f32 v158, v158, s24, v237
	v_med3_f32 v159, v159, s24, v237
	v_med3_f32 v160, v160, s24, v237
	v_med3_f32 v161, v161, s24, v237
	v_med3_f32 v162, v162, s24, v237
	v_med3_f32 v163, v163, s24, v237
	v_med3_f32 v164, v164, s24, v237
	v_med3_f32 v165, v165, s24, v237
	v_med3_f32 v166, v166, s24, v237
	v_med3_f32 v167, v167, s24, v237
	v_med3_f32 v168, v168, s24, v237
	v_med3_f32 v169, v169, s24, v237
	v_med3_f32 v170, v170, s24, v237
	v_med3_f32 v171, v171, s24, v237
	v_med3_f32 v172, v172, s24, v237
	v_med3_f32 v173, v173, s24, v237
	v_med3_f32 v174, v174, s24, v237
	v_med3_f32 v175, v175, s24, v237
	v_med3_f32 v176, v176, s24, v237
	v_med3_f32 v177, v177, s24, v237
	v_med3_f32 v178, v178, s24, v237
	v_med3_f32 v179, v179, s24, v237
	v_med3_f32 v180, v180, s24, v237
	v_med3_f32 v181, v181, s24, v237
	v_med3_f32 v182, v182, s24, v237
	v_med3_f32 v183, v183, s24, v237
	v_med3_f32 v184, v184, s24, v237
	v_med3_f32 v185, v185, s24, v237
	v_med3_f32 v186, v186, s24, v237
	v_med3_f32 v187, v187, s24, v237
	v_med3_f32 v188, v188, s24, v237
	v_med3_f32 v189, v189, s24, v237
	v_med3_f32 v190, v190, s24, v237
	v_med3_f32 v191, v191, s24, v237
	v_med3_f32 v192, v192, s24, v237
	v_med3_f32 v193, v193, s24, v237
	v_cvt_pk_fp8_f32 v130, v130, v134
	v_cvt_pk_fp8_f32 v130, v138, v142 op_sel:[0,0,1]
	v_cvt_pk_fp8_f32 v134, v131, v135
	v_cvt_pk_fp8_f32 v134, v139, v143 op_sel:[0,0,1]
	v_cvt_pk_fp8_f32 v138, v132, v136
	v_cvt_pk_fp8_f32 v138, v140, v144 op_sel:[0,0,1]
	v_cvt_pk_fp8_f32 v142, v133, v137
	v_cvt_pk_fp8_f32 v142, v141, v145 op_sel:[0,0,1]
	v_cvt_pk_fp8_f32 v131, v146, v150
	v_cvt_pk_fp8_f32 v131, v154, v158 op_sel:[0,0,1]
	v_cvt_pk_fp8_f32 v135, v147, v151
	v_cvt_pk_fp8_f32 v135, v155, v159 op_sel:[0,0,1]
	v_cvt_pk_fp8_f32 v139, v148, v152
	v_cvt_pk_fp8_f32 v139, v156, v160 op_sel:[0,0,1]
	v_cvt_pk_fp8_f32 v143, v149, v153
	v_cvt_pk_fp8_f32 v143, v157, v161 op_sel:[0,0,1]
	v_cvt_pk_fp8_f32 v132, v162, v166
	v_cvt_pk_fp8_f32 v132, v170, v174 op_sel:[0,0,1]
	v_cvt_pk_fp8_f32 v136, v163, v167
	v_cvt_pk_fp8_f32 v136, v171, v175 op_sel:[0,0,1]
	v_cvt_pk_fp8_f32 v140, v164, v168
	v_cvt_pk_fp8_f32 v140, v172, v176 op_sel:[0,0,1]
	v_cvt_pk_fp8_f32 v144, v165, v169
	v_cvt_pk_fp8_f32 v144, v173, v177 op_sel:[0,0,1]
	v_cvt_pk_fp8_f32 v133, v178, v182
	v_cvt_pk_fp8_f32 v133, v186, v190 op_sel:[0,0,1]
	v_cvt_pk_fp8_f32 v137, v179, v183
	v_cvt_pk_fp8_f32 v137, v187, v191 op_sel:[0,0,1]
	v_cvt_pk_fp8_f32 v141, v180, v184
	v_cvt_pk_fp8_f32 v141, v188, v192 op_sel:[0,0,1]
	v_cvt_pk_fp8_f32 v145, v181, v185
	v_cvt_pk_fp8_f32 v145, v189, v193 op_sel:[0,0,1]
	global_store_dwordx4 v250, v[130:133], s[42:43] nt
	global_store_dwordx4 v250, v[134:137], s[42:43] offset:2048 nt
	global_store_dwordx4 v251, v[138:141], s[42:43] nt
	global_store_dwordx4 v251, v[142:145], s[42:43] offset:2048 nt
	s_add_u32 s42, s42, 0x800000
	s_addc_u32 s43, s43, 0
	s_waitcnt vmcnt(8)
; #define GAS __attribute__((address_space(1)))
; template <bool GAIN, bool NT = false> __device__ __forceinline__ void titem8_store(const TItem& d, int lane, const f32x4 (&r)[16], const f32x4 (&g)[4]) {
;     const int q = lane & 7, kg = lane >> 3; const unsigned lo = (unsigned)((4 * q) * d.ldk + 16 * kg);
;     GAS char* base = (GAS char*)d.dst;
;     f32x4 s[16];
; #pragma unroll
;     for (int j = 0; j < 16; ++j) s[j] = r[j] * ((GAIN ? g[j >> 2][j & 3] : 1.0f) * W8_SCALE);
; #pragma unroll
;     for (int i = 0; i < 4; ++i) { v4u w;
;         w.x = pk4_fp8w(s[0][i], s[1][i], s[2][i], s[3][i]); w.y = pk4_fp8w(s[4][i], s[5][i], s[6][i], s[7][i]);
;         w.z = pk4_fp8w(s[8][i], s[9][i], s[10][i], s[11][i]); w.w = pk4_fp8w(s[12][i], s[13][i], s[14][i], s[15][i]);
;         GAS v4u* p = (GAS v4u*)(base + (size_t)i * (size_t)d.ldk + lo);
;         if (NT) __builtin_nontemporal_store(w, p); else *p = w; }
; }
	v_pk_mul_f32 v[0:1], v[0:1], s[30:31] op_sel_hi:[1,0]
	v_pk_mul_f32 v[2:3], v[2:3], s[30:31] op_sel_hi:[1,0]
	v_pk_mul_f32 v[4:5], v[4:5], s[30:31] op_sel_hi:[1,0]
	v_pk_mul_f32 v[6:7], v[6:7], s[30:31] op_sel_hi:[1,0]
	v_pk_mul_f32 v[8:9], v[8:9], s[30:31] op_sel_hi:[1,0]
	v_pk_mul_f32 v[10:11], v[10:11], s[30:31] op_sel_hi:[1,0]
	v_pk_mul_f32 v[12:13], v[12:13], s[30:31] op_sel_hi:[1,0]
	v_pk_mul_f32 v[14:15], v[14:15], s[30:31] op_sel_hi:[1,0]
	v_pk_mul_f32 v[16:17], v[16:17], s[30:31] op_sel_hi:[1,0]
	v_pk_mul_f32 v[18:19], v[18:19], s[30:31] op_sel_hi:[1,0]
	v_pk_mul_f32 v[20:21], v[20:21], s[30:31] op_sel_hi:[1,0]
	v_pk_mul_f32 v[22:23], v[22:23], s[30:31] op_sel_hi:[1,0]
	v_pk_mul_f32 v[24:25], v[24:25], s[30:31] op_sel_hi:[1,0]
	v_pk_mul_f32 v[26:27], v[26:27], s[30:31] op_sel_hi:[1,0]
	v_pk_mul_f32 v[28:29], v[28:29], s[30:31] op_sel_hi:[1,0]
	v_pk_mul_f32 v[30:31], v[30:31], s[30:31] op_sel_hi:[1,0]
	v_pk_mul_f32 v[32:33], v[32:33], s[30:31] op_sel_hi:[1,0]
	v_pk_mul_f32 v[34:35], v[34:35], s[30:31] op_sel_hi:[1,0]
	v_pk_mul_f32 v[36:37], v[36:37], s[30:31] op_sel_hi:[1,0]
	v_pk_mul_f32 v[38:39], v[38:39], s[30:31] op_sel_hi:[1,0]
	v_pk_mul_f32 v[40:41], v[40:41], s[30:31] op_sel_hi:[1,0]
	v_pk_mul_f32 v[42:43], v[42:43], s[30:31] op_sel_hi:[1,0]
	v_pk_mul_f32 v[44:45], v[44:45], s[30:31] op_sel_hi:[1,0]
	v_pk_mul_f32 v[46:47], v[46:47], s[30:31] op_sel_hi:[1,0]
	v_pk_mul_f32 v[48:49], v[48:49], s[30:31] op_sel_hi:[1,0]
	v_pk_mul_f32 v[50:51], v[50:51], s[30:31] op_sel_hi:[1,0]
	v_pk_mul_f32 v[52:53], v[52:53], s[30:31] op_sel_hi:[1,0]
	v_pk_mul_f32 v[54:55], v[54:55], s[30:31] op_sel_hi:[1,0]
	v_pk_mul_f32 v[56:57], v[56:57], s[30:31] op_sel_hi:[1,0]
	v_pk_mul_f32 v[58:59], v[58:59], s[30:31] op_sel_hi:[1,0]
	v_pk_mul_f32 v[60:61], v[60:61], s[30:31] op_sel_hi:[1,0]
	v_pk_mul_f32 v[62:63], v[62:63], s[30:31] op_sel_hi:[1,0]
	v_med3_f32 v0, v0, s24, v237
	v_med3_f32 v1, v1, s24, v237
	v_med3_f32 v2, v2, s24, v237
	v_med3_f32 v3, v3, s24, v237
	v_med3_f32 v4, v4, s24, v237
	v_med3_f32 v5, v5, s24, v237
	v_med3_f32 v6, v6, s24, v237
	v_med3_f32 v7, v7, s24, v237
	v_med3_f32 v8, v8, s24, v237
	v_med3_f32 v9, v9, s24, v237
	v_med3_f32 v10, v10, s24, v237
	v_med3_f32 v11, v11, s24, v237
	v_med3_f32 v12, v12, s24, v237
	v_med3_f32 v13, v13, s24, v237
	v_med3_f32 v14, v14, s24, v237
	v_med3_f32 v15, v15, s24, v237
	v_med3_f32 v16, v16, s24, v237
	v_med3_f32 v17, v17, s24, v237
	v_med3_f32 v18, v18, s24, v237
	v_med3_f32 v19, v19, s24, v237
	v_med3_f32 v20, v20, s24, v237
	v_med3_f32 v21, v21, s24, v237
	v_med3_f32 v22, v22, s24, v237
	v_med3_f32 v23, v23, s24, v237
	v_med3_f32 v24, v24, s24, v237
	v_med3_f32 v25, v25, s24, v237
	v_med3_f32 v26, v26, s24, v237
	v_med3_f32 v27, v27, s24, v237
	v_med3_f32 v28, v28, s24, v237
	v_med3_f32 v29, v29, s24, v237
	v_med3_f32 v30, v30, s24, v237
	v_med3_f32 v31, v31, s24, v237
	v_med3_f32 v32, v32, s24, v237
	v_med3_f32 v33, v33, s24, v237
	v_med3_f32 v34, v34, s24, v237
	v_med3_f32 v35, v35, s24, v237
	v_med3_f32 v36, v36, s24, v237
	v_med3_f32 v37, v37, s24, v237
	v_med3_f32 v38, v38, s24, v237
	v_med3_f32 v39, v39, s24, v237
	v_med3_f32 v40, v40, s24, v237
	v_med3_f32 v41, v41, s24, v237
	v_med3_f32 v42, v42, s24, v237
	v_med3_f32 v43, v43, s24, v237
	v_med3_f32 v44, v44, s24, v237
	v_med3_f32 v45, v45, s24, v237
	v_med3_f32 v46, v46, s24, v237
	v_med3_f32 v47, v47, s24, v237
	v_med3_f32 v48, v48, s24, v237
	v_med3_f32 v49, v49, s24, v237
	v_med3_f32 v50, v50, s24, v237
	v_med3_f32 v51, v51, s24, v237
	v_med3_f32 v52, v52, s24, v237
	v_med3_f32 v53, v53, s24, v237
	v_med3_f32 v54, v54, s24, v237
	v_med3_f32 v55, v55, s24, v237
	v_med3_f32 v56, v56, s24, v237
	v_med3_f32 v57, v57, s24, v237
	v_med3_f32 v58, v58, s24, v237
	v_med3_f32 v59, v59, s24, v237
	v_med3_f32 v60, v60, s24, v237
	v_med3_f32 v61, v61, s24, v237
	v_med3_f32 v62, v62, s24, v237
	v_med3_f32 v63, v63, s24, v237
	v_cvt_pk_fp8_f32 v0, v0, v4
	v_cvt_pk_fp8_f32 v0, v8, v12 op_sel:[0,0,1]
	v_cvt_pk_fp8_f32 v4, v1, v5
	v_cvt_pk_fp8_f32 v4, v9, v13 op_sel:[0,0,1]
	v_cvt_pk_fp8_f32 v8, v2, v6
	v_cvt_pk_fp8_f32 v8, v10, v14 op_sel:[0,0,1]
	v_cvt_pk_fp8_f32 v12, v3, v7
	v_cvt_pk_fp8_f32 v12, v11, v15 op_sel:[0,0,1]
	v_cvt_pk_fp8_f32 v1, v16, v20
	v_cvt_pk_fp8_f32 v1, v24, v28 op_sel:[0,0,1]
	v_cvt_pk_fp8_f32 v5, v17, v21
	v_cvt_pk_fp8_f32 v5, v25, v29 op_sel:[0,0,1]
	v_cvt_pk_fp8_f32 v9, v18, v22
	v_cvt_pk_fp8_f32 v9, v26, v30 op_sel:[0,0,1]
	v_cvt_pk_fp8_f32 v13, v19, v23
	v_cvt_pk_fp8_f32 v13, v27, v31 op_sel:[0,0,1]
	v_cvt_pk_fp8_f32 v2, v32, v36
	v_cvt_pk_fp8_f32 v2, v40, v44 op_sel:[0,0,1]
	v_cvt_pk_fp8_f32 v6, v33, v37
	v_cvt_pk_fp8_f32 v6, v41, v45 op_sel:[0,0,1]
	v_cvt_pk_fp8_f32 v10, v34, v38
	v_cvt_pk_fp8_f32 v10, v42, v46 op_sel:[0,0,1]
	v_cvt_pk_fp8_f32 v14, v35, v39
	v_cvt_pk_fp8_f32 v14, v43, v47 op_sel:[0,0,1]
	v_cvt_pk_fp8_f32 v3, v48, v52
	v_cvt_pk_fp8_f32 v3, v56, v60 op_sel:[0,0,1]
	v_cvt_pk_fp8_f32 v7, v49, v53
	v_cvt_pk_fp8_f32 v7, v57, v61 op_sel:[0,0,1]
	v_cvt_pk_fp8_f32 v11, v50, v54
	v_cvt_pk_fp8_f32 v11, v58, v62 op_sel:[0,0,1]
	v_cvt_pk_fp8_f32 v15, v51, v55
	v_cvt_pk_fp8_f32 v15, v59, v63 op_sel:[0,0,1]
	global_store_dwordx4 v250, v[0:3], s[42:43] nt
	global_store_dwordx4 v250, v[4:7], s[42:43] offset:2048 nt
	global_store_dwordx4 v251, v[8:11], s[42:43] nt
	global_store_dwordx4 v251, v[12:15], s[42:43] offset:2048 nt
	s_add_u32 s42, s42, 0x800000
	s_addc_u32 s43, s43, 0
	v_mov_b32_e32 v65, 0
